# v049 + K-loop role priority with both toggles on the load path (raise before the waits that open the MFMA block, drop right behind the barrier that closes it)
# baseline (speedup 1.0000x reference)
.LBB0_260:
	s_ashr_i32 s69, s68, 31
	s_lshl_b64 s[26:27], s[68:69], 20
	v_readlane_b32 s8, v254, 56
	v_readlane_b32 s9, v254, 57
	s_add_u32 s70, s8, s26
	s_addc_u32 s71, s9, s27
	s_and_b64 s[26:27], s[0:1], exec
	s_cselect_b32 s69, s71, s83
	s_cselect_b32 s75, s70, s82
	s_ashr_i32 s57, s56, 31
	s_lshl_b64 s[26:27], s[56:57], 20
	s_add_u32 s72, s84, s26
	s_addc_u32 s73, s85, s27
	s_and_b64 s[26:27], s[0:1], exec
	s_cselect_b32 s57, s73, s81
	s_cselect_b32 s96, s72, s80
	s_add_u32 s97, s80, 0x10000
	s_addc_u32 vcc_lo, s81, 0
	s_add_u32 s80, s82, 0x80080
	s_addc_u32 s81, s83, 0
	s_mov_b32 vcc_hi, -2
	ds_read_b128 v[144:147], v170
	ds_read_b128 v[148:151], v170 offset:1024
	ds_read_b128 v[174:177], v170 offset:2048
	ds_read_b128 v[178:181], v170 offset:3072
	ds_read_b128 v[182:185], v171
	ds_read_b128 v[186:189], v171 offset:1024
	ds_read_b128 v[190:193], v171 offset:2048
	ds_read_b128 v[194:197], v171 offset:3072
	s_add_u32 s26, s80, 0xfff80080
	s_addc_u32 s27, s81, -1
	s_cmp_eq_u32 vcc_hi, 28
	s_cselect_b32 s83, s69, s27
	s_cselect_b32 s82, s75, s26
	s_cselect_b32 s27, s57, vcc_lo
	s_cselect_b32 s26, s96, s97
	v_lshl_add_u64 v[152:153], s[80:81], 0, v[134:135]
	s_add_i32 m0, s87, 0xc000
	ds_read_b128 v[198:201], v172
	ds_read_b128 v[202:205], v172 offset:1024
	ds_read_b128 v[206:209], v172 offset:2048
	ds_read_b128 v[210:213], v172 offset:3072
	ds_read_b128 v[214:217], v172 offset:4096
	ds_read_b128 v[220:223], v172 offset:5120
	ds_read_b128 v[224:227], v172 offset:6144
	ds_read_b128 v[228:231], v172 offset:7168
	global_load_lds_dwordx4 v[152:153], off
	v_lshl_add_u64 v[152:153], s[80:81], 0, v[138:139]
	s_add_i32 m0, s87, 0xe000
	s_nop 0
	global_load_lds_dwordx4 v[152:153], off
	s_setprio 1
	s_waitcnt vmcnt(8)
	s_waitcnt lgkmcnt(0)
	s_barrier
	v_mfma_f32_16x16x32_bf16 v[122:125], v[144:147], v[198:201], 0
	v_mfma_f32_16x16x32_bf16 v[118:121], v[174:177], v[198:201], 0
	v_mfma_f32_16x16x32_bf16 v[106:109], v[144:147], v[206:209], 0
	v_mfma_f32_16x16x32_bf16 v[102:105], v[174:177], v[206:209], 0
	v_mfma_f32_16x16x32_bf16 v[90:93], v[144:147], v[214:217], 0
	v_mfma_f32_16x16x32_bf16 v[86:89], v[174:177], v[214:217], 0
	v_mfma_f32_16x16x32_bf16 v[74:77], v[144:147], v[224:227], 0
	v_mfma_f32_16x16x32_bf16 v[70:73], v[174:177], v[224:227], 0
	v_mfma_f32_16x16x32_bf16 v[122:125], v[148:151], v[202:205], v[122:125]
	v_mfma_f32_16x16x32_bf16 v[118:121], v[178:181], v[202:205], v[118:121]
	v_mfma_f32_16x16x32_bf16 v[106:109], v[148:151], v[210:213], v[106:109]
	v_mfma_f32_16x16x32_bf16 v[102:105], v[178:181], v[210:213], v[102:105]
	v_mfma_f32_16x16x32_bf16 v[90:93], v[148:151], v[220:223], v[90:93]
	v_mfma_f32_16x16x32_bf16 v[86:89], v[178:181], v[220:223], v[86:89]
	v_mfma_f32_16x16x32_bf16 v[74:77], v[148:151], v[228:231], v[74:77]
	v_mfma_f32_16x16x32_bf16 v[70:73], v[178:181], v[228:231], v[70:73]
	v_mfma_f32_16x16x32_bf16 v[126:129], v[182:185], v[198:201], 0
	v_mfma_f32_16x16x32_bf16 v[114:117], v[190:193], v[198:201], 0
	v_mfma_f32_16x16x32_bf16 v[110:113], v[182:185], v[206:209], 0
	v_mfma_f32_16x16x32_bf16 v[98:101], v[190:193], v[206:209], 0
	v_mfma_f32_16x16x32_bf16 v[94:97], v[182:185], v[214:217], 0
	v_mfma_f32_16x16x32_bf16 v[82:85], v[190:193], v[214:217], 0
	v_mfma_f32_16x16x32_bf16 v[78:81], v[182:185], v[224:227], 0
	v_mfma_f32_16x16x32_bf16 v[66:69], v[190:193], v[224:227], 0
	v_mfma_f32_16x16x32_bf16 v[126:129], v[186:189], v[202:205], v[126:129]
	v_mfma_f32_16x16x32_bf16 v[114:117], v[194:197], v[202:205], v[114:117]
	v_mfma_f32_16x16x32_bf16 v[110:113], v[186:189], v[210:213], v[110:113]
	v_mfma_f32_16x16x32_bf16 v[98:101], v[194:197], v[210:213], v[98:101]
	v_mfma_f32_16x16x32_bf16 v[94:97], v[186:189], v[220:223], v[94:97]
	v_mfma_f32_16x16x32_bf16 v[82:85], v[194:197], v[220:223], v[82:85]
	v_mfma_f32_16x16x32_bf16 v[78:81], v[186:189], v[228:231], v[78:81]
	v_mfma_f32_16x16x32_bf16 v[66:69], v[194:197], v[228:231], v[66:69]
	s_barrier
	s_setprio 0
	v_lshl_add_u64 v[152:153], s[26:27], 0, v[162:163]
	s_add_i32 s26, s94, s86
	s_mov_b32 m0, s26
	ds_read_b128 v[198:201], v172 offset:16384
	ds_read_b128 v[202:205], v172 offset:17408
	ds_read_b128 v[206:209], v172 offset:18432
	ds_read_b128 v[210:213], v172 offset:19456
	ds_read_b128 v[214:217], v172 offset:20480
	ds_read_b128 v[220:223], v172 offset:21504
	ds_read_b128 v[224:227], v172 offset:22528
	ds_read_b128 v[228:231], v172 offset:23552
	global_load_lds_dwordx4 v[152:153], off
	v_lshl_add_u64 v[232:233], v[152:153], 0, s[10:11]
	s_add_i32 m0, s26, 0x2000
	s_add_i32 s26, s95, s86
	global_load_lds_dwordx4 v[232:233], off
	v_lshl_add_u64 v[232:233], v[152:153], 0, s[12:13]
	s_mov_b32 m0, s26
	v_lshl_add_u64 v[234:235], s[82:83], 0, v[132:133]
	global_load_lds_dwordx4 v[232:233], off
	v_lshl_add_u64 v[232:233], v[152:153], 0, s[14:15]
	s_add_i32 m0, s26, 0x2000
	s_nop 0
	global_load_lds_dwordx4 v[232:233], off
	v_lshl_add_u64 v[232:233], s[82:83], 0, v[130:131]
	s_mov_b32 m0, s87
	s_nop 0
	global_load_lds_dwordx4 v[232:233], off
	s_mov_b32 m0, s88
	s_nop 0
	global_load_lds_dwordx4 v[234:235], off
	s_setprio 1
	s_waitcnt vmcnt(8)
	s_waitcnt lgkmcnt(0)
	s_barrier
	v_mfma_f32_16x16x32_bf16 v[58:61], v[144:147], v[198:201], 0
	v_mfma_f32_16x16x32_bf16 v[54:57], v[174:177], v[198:201], 0
	v_mfma_f32_16x16x32_bf16 v[42:45], v[144:147], v[206:209], 0
	v_mfma_f32_16x16x32_bf16 v[38:41], v[174:177], v[206:209], 0
	v_mfma_f32_16x16x32_bf16 v[26:29], v[144:147], v[214:217], 0
	v_mfma_f32_16x16x32_bf16 v[22:25], v[174:177], v[214:217], 0
	v_mfma_f32_16x16x32_bf16 v[10:13], v[144:147], v[224:227], 0
	v_mfma_f32_16x16x32_bf16 v[6:9], v[174:177], v[224:227], 0
	v_mfma_f32_16x16x32_bf16 v[58:61], v[148:151], v[202:205], v[58:61]
	v_mfma_f32_16x16x32_bf16 v[54:57], v[178:181], v[202:205], v[54:57]
	v_mfma_f32_16x16x32_bf16 v[42:45], v[148:151], v[210:213], v[42:45]
	v_mfma_f32_16x16x32_bf16 v[38:41], v[178:181], v[210:213], v[38:41]
	v_mfma_f32_16x16x32_bf16 v[26:29], v[148:151], v[220:223], v[26:29]
	v_mfma_f32_16x16x32_bf16 v[22:25], v[178:181], v[220:223], v[22:25]
	v_mfma_f32_16x16x32_bf16 v[10:13], v[148:151], v[228:231], v[10:13]
	v_mfma_f32_16x16x32_bf16 v[6:9], v[178:181], v[228:231], v[6:9]
	v_mfma_f32_16x16x32_bf16 v[62:65], v[182:185], v[198:201], 0
	v_mfma_f32_16x16x32_bf16 v[50:53], v[190:193], v[198:201], 0
	v_mfma_f32_16x16x32_bf16 v[46:49], v[182:185], v[206:209], 0
	v_mfma_f32_16x16x32_bf16 v[34:37], v[190:193], v[206:209], 0
	v_mfma_f32_16x16x32_bf16 v[30:33], v[182:185], v[214:217], 0
	v_mfma_f32_16x16x32_bf16 v[18:21], v[190:193], v[214:217], 0
	v_mfma_f32_16x16x32_bf16 v[14:17], v[182:185], v[224:227], 0
	v_mfma_f32_16x16x32_bf16 v[2:5], v[190:193], v[224:227], 0
	v_mfma_f32_16x16x32_bf16 v[62:65], v[186:189], v[202:205], v[62:65]
	v_mfma_f32_16x16x32_bf16 v[50:53], v[194:197], v[202:205], v[50:53]
	v_mfma_f32_16x16x32_bf16 v[46:49], v[186:189], v[210:213], v[46:49]
	v_mfma_f32_16x16x32_bf16 v[34:37], v[194:197], v[210:213], v[34:37]
	v_mfma_f32_16x16x32_bf16 v[30:33], v[186:189], v[220:223], v[30:33]
	v_mfma_f32_16x16x32_bf16 v[18:21], v[194:197], v[220:223], v[18:21]
	v_mfma_f32_16x16x32_bf16 v[14:17], v[186:189], v[228:231], v[14:17]
	v_mfma_f32_16x16x32_bf16 v[2:5], v[194:197], v[228:231], v[2:5]
	s_barrier
	s_setprio 0
	s_add_i32 s33, 0, 0x18000
	v_add_u32_e32 v136, s33, v167
	s_add_i32 s8, 0, 0x1c000
	ds_read_b128 v[144:147], v136
	ds_read_b128 v[148:151], v136 offset:1024
	ds_read_b128 v[174:177], v136 offset:2048
	ds_read_b128 v[178:181], v136 offset:3072
	v_add_u32_e32 v136, s8, v167
	ds_read_b128 v[182:185], v136
	ds_read_b128 v[186:189], v136 offset:1024
	ds_read_b128 v[190:193], v136 offset:2048
	ds_read_b128 v[194:197], v136 offset:3072
	s_add_u32 s26, s82, 0x80000
	s_addc_u32 s27, s83, 0
	s_mov_b32 m0, s89
	v_lshl_add_u64 v[236:237], s[26:27], 0, v[130:131]
	ds_read_b128 v[198:201], v172 offset:32768
	ds_read_b128 v[202:205], v172 offset:33792
	ds_read_b128 v[206:209], v172 offset:34816
	ds_read_b128 v[210:213], v172 offset:35840
	ds_read_b128 v[214:217], v172 offset:36864
	ds_read_b128 v[220:223], v172 offset:37888
	ds_read_b128 v[224:227], v172 offset:38912
	ds_read_b128 v[228:231], v172 offset:39936
	global_load_lds_dwordx4 v[236:237], off
	v_lshl_add_u64 v[236:237], s[26:27], 0, v[132:133]
	s_mov_b32 m0, s90
	s_nop 0
	global_load_lds_dwordx4 v[236:237], off
	s_setprio 1
	s_waitcnt vmcnt(8)
	s_waitcnt lgkmcnt(0)
	s_barrier
	v_mfma_f32_16x16x32_bf16 v[122:125], v[144:147], v[198:201], v[122:125]
	v_mfma_f32_16x16x32_bf16 v[118:121], v[174:177], v[198:201], v[118:121]
	v_mfma_f32_16x16x32_bf16 v[106:109], v[144:147], v[206:209], v[106:109]
	v_mfma_f32_16x16x32_bf16 v[102:105], v[174:177], v[206:209], v[102:105]
	v_mfma_f32_16x16x32_bf16 v[90:93], v[144:147], v[214:217], v[90:93]
	v_mfma_f32_16x16x32_bf16 v[86:89], v[174:177], v[214:217], v[86:89]
	v_mfma_f32_16x16x32_bf16 v[74:77], v[144:147], v[224:227], v[74:77]
	v_mfma_f32_16x16x32_bf16 v[70:73], v[174:177], v[224:227], v[70:73]
	v_mfma_f32_16x16x32_bf16 v[122:125], v[148:151], v[202:205], v[122:125]
	v_mfma_f32_16x16x32_bf16 v[118:121], v[178:181], v[202:205], v[118:121]
	v_mfma_f32_16x16x32_bf16 v[106:109], v[148:151], v[210:213], v[106:109]
	v_mfma_f32_16x16x32_bf16 v[102:105], v[178:181], v[210:213], v[102:105]
	v_mfma_f32_16x16x32_bf16 v[90:93], v[148:151], v[220:223], v[90:93]
	v_mfma_f32_16x16x32_bf16 v[86:89], v[178:181], v[220:223], v[86:89]
	v_mfma_f32_16x16x32_bf16 v[74:77], v[148:151], v[228:231], v[74:77]
	v_mfma_f32_16x16x32_bf16 v[70:73], v[178:181], v[228:231], v[70:73]
	v_mfma_f32_16x16x32_bf16 v[126:129], v[182:185], v[198:201], v[126:129]
	v_mfma_f32_16x16x32_bf16 v[114:117], v[190:193], v[198:201], v[114:117]
	v_mfma_f32_16x16x32_bf16 v[110:113], v[182:185], v[206:209], v[110:113]
	v_mfma_f32_16x16x32_bf16 v[98:101], v[190:193], v[206:209], v[98:101]
	v_mfma_f32_16x16x32_bf16 v[94:97], v[182:185], v[214:217], v[94:97]
	v_mfma_f32_16x16x32_bf16 v[82:85], v[190:193], v[214:217], v[82:85]
	v_mfma_f32_16x16x32_bf16 v[78:81], v[182:185], v[224:227], v[78:81]
	v_mfma_f32_16x16x32_bf16 v[66:69], v[190:193], v[224:227], v[66:69]
	v_mfma_f32_16x16x32_bf16 v[126:129], v[186:189], v[202:205], v[126:129]
	v_mfma_f32_16x16x32_bf16 v[114:117], v[194:197], v[202:205], v[114:117]
	v_mfma_f32_16x16x32_bf16 v[110:113], v[186:189], v[210:213], v[110:113]
	v_mfma_f32_16x16x32_bf16 v[98:101], v[194:197], v[210:213], v[98:101]
	v_mfma_f32_16x16x32_bf16 v[94:97], v[186:189], v[220:223], v[94:97]
	v_mfma_f32_16x16x32_bf16 v[82:85], v[194:197], v[220:223], v[82:85]
	v_mfma_f32_16x16x32_bf16 v[78:81], v[186:189], v[228:231], v[78:81]
	v_mfma_f32_16x16x32_bf16 v[66:69], v[194:197], v[228:231], v[66:69]
	s_barrier
	s_setprio 0
	s_add_i32 s9, s33, s86
	v_lshl_add_u64 v[236:237], v[152:153], 0, s[20:21]
	s_mov_b32 m0, s9
	ds_read_b128 v[198:201], v172 offset:49152
	ds_read_b128 v[202:205], v172 offset:50176
	ds_read_b128 v[206:209], v172 offset:51200
	ds_read_b128 v[210:213], v172 offset:52224
	ds_read_b128 v[214:217], v172 offset:53248
	ds_read_b128 v[220:223], v172 offset:54272
	ds_read_b128 v[224:227], v172 offset:55296
	ds_read_b128 v[228:231], v172 offset:56320
	global_load_lds_dwordx4 v[236:237], off
	v_lshl_add_u64 v[236:237], v[152:153], 0, s[22:23]
	s_add_i32 m0, s9, 0x2000
	s_add_i32 s8, s8, s86
	global_load_lds_dwordx4 v[236:237], off
	v_lshl_add_u64 v[236:237], v[152:153], 0, s[40:41]
	s_mov_b32 m0, s8
	v_lshl_add_u64 v[152:153], v[152:153], 0, s[44:45]
	global_load_lds_dwordx4 v[236:237], off
	s_add_i32 m0, s8, 0x2000
	s_nop 0
	global_load_lds_dwordx4 v[152:153], off
	v_lshl_add_u64 v[152:153], v[232:233], 0, s[24:25]
	s_mov_b32 m0, s91
	s_nop 0
	global_load_lds_dwordx4 v[152:153], off
	v_lshl_add_u64 v[152:153], v[234:235], 0, s[24:25]
	s_mov_b32 m0, s92
	s_nop 0
	global_load_lds_dwordx4 v[152:153], off
	s_setprio 1
	s_waitcnt vmcnt(8)
	s_waitcnt lgkmcnt(0)
	s_barrier
	v_mfma_f32_16x16x32_bf16 v[58:61], v[144:147], v[198:201], v[58:61]
	v_mfma_f32_16x16x32_bf16 v[54:57], v[174:177], v[198:201], v[54:57]
	v_mfma_f32_16x16x32_bf16 v[42:45], v[144:147], v[206:209], v[42:45]
	v_mfma_f32_16x16x32_bf16 v[38:41], v[174:177], v[206:209], v[38:41]
	v_mfma_f32_16x16x32_bf16 v[26:29], v[144:147], v[214:217], v[26:29]
	v_mfma_f32_16x16x32_bf16 v[22:25], v[174:177], v[214:217], v[22:25]
	v_mfma_f32_16x16x32_bf16 v[10:13], v[144:147], v[224:227], v[10:13]
	v_mfma_f32_16x16x32_bf16 v[6:9], v[174:177], v[224:227], v[6:9]
	v_mfma_f32_16x16x32_bf16 v[58:61], v[148:151], v[202:205], v[58:61]
	v_mfma_f32_16x16x32_bf16 v[54:57], v[178:181], v[202:205], v[54:57]
	v_mfma_f32_16x16x32_bf16 v[42:45], v[148:151], v[210:213], v[42:45]
	v_mfma_f32_16x16x32_bf16 v[38:41], v[178:181], v[210:213], v[38:41]
	v_mfma_f32_16x16x32_bf16 v[26:29], v[148:151], v[220:223], v[26:29]
	v_mfma_f32_16x16x32_bf16 v[22:25], v[178:181], v[220:223], v[22:25]
	v_mfma_f32_16x16x32_bf16 v[10:13], v[148:151], v[228:231], v[10:13]
	v_mfma_f32_16x16x32_bf16 v[6:9], v[178:181], v[228:231], v[6:9]
	v_mfma_f32_16x16x32_bf16 v[62:65], v[182:185], v[198:201], v[62:65]
	v_mfma_f32_16x16x32_bf16 v[50:53], v[190:193], v[198:201], v[50:53]
	v_mfma_f32_16x16x32_bf16 v[46:49], v[182:185], v[206:209], v[46:49]
	v_mfma_f32_16x16x32_bf16 v[34:37], v[190:193], v[206:209], v[34:37]
	v_mfma_f32_16x16x32_bf16 v[30:33], v[182:185], v[214:217], v[30:33]
	v_mfma_f32_16x16x32_bf16 v[18:21], v[190:193], v[214:217], v[18:21]
	v_mfma_f32_16x16x32_bf16 v[14:17], v[182:185], v[224:227], v[14:17]
	v_mfma_f32_16x16x32_bf16 v[2:5], v[190:193], v[224:227], v[2:5]
	v_mfma_f32_16x16x32_bf16 v[62:65], v[186:189], v[202:205], v[62:65]
	v_mfma_f32_16x16x32_bf16 v[50:53], v[194:197], v[202:205], v[50:53]
	v_mfma_f32_16x16x32_bf16 v[46:49], v[186:189], v[210:213], v[46:49]
	v_mfma_f32_16x16x32_bf16 v[34:37], v[194:197], v[210:213], v[34:37]
	v_mfma_f32_16x16x32_bf16 v[30:33], v[186:189], v[220:223], v[30:33]
	v_mfma_f32_16x16x32_bf16 v[18:21], v[194:197], v[220:223], v[18:21]
	v_mfma_f32_16x16x32_bf16 v[14:17], v[186:189], v[228:231], v[14:17]
	v_mfma_f32_16x16x32_bf16 v[2:5], v[194:197], v[228:231], v[2:5]
	s_barrier
	s_setprio 0
	s_add_i32 vcc_hi, vcc_hi, 2
	s_add_u32 s97, s97, 0x10000
	s_addc_u32 vcc_lo, vcc_lo, 0
	s_add_u32 s80, s80, 0x100
	s_addc_u32 s81, s81, 0
	s_cmp_gt_u32 vcc_hi, 29
.LBB0_261:
	ds_read_b128 v[144:147], v170
	ds_read_b128 v[148:151], v170 offset:1024
	ds_read_b128 v[174:177], v170 offset:2048
	ds_read_b128 v[178:181], v170 offset:3072
	ds_read_b128 v[182:185], v171
	ds_read_b128 v[186:189], v171 offset:1024
	ds_read_b128 v[190:193], v171 offset:2048
	ds_read_b128 v[194:197], v171 offset:3072
	s_add_u32 s26, s80, 0xfff80080
	s_addc_u32 s27, s81, -1
	s_cmp_eq_u32 vcc_hi, 28
	s_cselect_b32 s83, s69, s27
	s_cselect_b32 s82, s75, s26
	s_cselect_b32 s27, s57, vcc_lo
	s_cselect_b32 s26, s96, s97
	v_lshl_add_u64 v[152:153], s[80:81], 0, v[134:135]
	s_add_i32 m0, s87, 0xc000
	ds_read_b128 v[198:201], v172
	ds_read_b128 v[202:205], v172 offset:1024
	ds_read_b128 v[206:209], v172 offset:2048
	ds_read_b128 v[210:213], v172 offset:3072
	ds_read_b128 v[214:217], v172 offset:4096
	ds_read_b128 v[220:223], v172 offset:5120
	ds_read_b128 v[224:227], v172 offset:6144
	ds_read_b128 v[228:231], v172 offset:7168
	global_load_lds_dwordx4 v[152:153], off
	v_lshl_add_u64 v[152:153], s[80:81], 0, v[138:139]
	s_add_i32 m0, s87, 0xe000
	s_nop 0
	global_load_lds_dwordx4 v[152:153], off
	s_setprio 1
	s_waitcnt vmcnt(8)
	s_waitcnt lgkmcnt(0)
	s_barrier
	v_mfma_f32_16x16x32_bf16 v[122:125], v[144:147], v[198:201], v[122:125]
	v_mfma_f32_16x16x32_bf16 v[118:121], v[174:177], v[198:201], v[118:121]
	v_mfma_f32_16x16x32_bf16 v[106:109], v[144:147], v[206:209], v[106:109]
	v_mfma_f32_16x16x32_bf16 v[102:105], v[174:177], v[206:209], v[102:105]
	v_mfma_f32_16x16x32_bf16 v[90:93], v[144:147], v[214:217], v[90:93]
	v_mfma_f32_16x16x32_bf16 v[86:89], v[174:177], v[214:217], v[86:89]
	v_mfma_f32_16x16x32_bf16 v[74:77], v[144:147], v[224:227], v[74:77]
	v_mfma_f32_16x16x32_bf16 v[70:73], v[174:177], v[224:227], v[70:73]
	v_mfma_f32_16x16x32_bf16 v[122:125], v[148:151], v[202:205], v[122:125]
	v_mfma_f32_16x16x32_bf16 v[118:121], v[178:181], v[202:205], v[118:121]
	v_mfma_f32_16x16x32_bf16 v[106:109], v[148:151], v[210:213], v[106:109]
	v_mfma_f32_16x16x32_bf16 v[102:105], v[178:181], v[210:213], v[102:105]
	v_mfma_f32_16x16x32_bf16 v[90:93], v[148:151], v[220:223], v[90:93]
	v_mfma_f32_16x16x32_bf16 v[86:89], v[178:181], v[220:223], v[86:89]
	v_mfma_f32_16x16x32_bf16 v[74:77], v[148:151], v[228:231], v[74:77]
	v_mfma_f32_16x16x32_bf16 v[70:73], v[178:181], v[228:231], v[70:73]
	v_mfma_f32_16x16x32_bf16 v[126:129], v[182:185], v[198:201], v[126:129]
	v_mfma_f32_16x16x32_bf16 v[114:117], v[190:193], v[198:201], v[114:117]
	v_mfma_f32_16x16x32_bf16 v[110:113], v[182:185], v[206:209], v[110:113]
	v_mfma_f32_16x16x32_bf16 v[98:101], v[190:193], v[206:209], v[98:101]
	v_mfma_f32_16x16x32_bf16 v[94:97], v[182:185], v[214:217], v[94:97]
	v_mfma_f32_16x16x32_bf16 v[82:85], v[190:193], v[214:217], v[82:85]
	v_mfma_f32_16x16x32_bf16 v[78:81], v[182:185], v[224:227], v[78:81]
	v_mfma_f32_16x16x32_bf16 v[66:69], v[190:193], v[224:227], v[66:69]
	v_mfma_f32_16x16x32_bf16 v[126:129], v[186:189], v[202:205], v[126:129]
	v_mfma_f32_16x16x32_bf16 v[114:117], v[194:197], v[202:205], v[114:117]
	v_mfma_f32_16x16x32_bf16 v[110:113], v[186:189], v[210:213], v[110:113]
	v_mfma_f32_16x16x32_bf16 v[98:101], v[194:197], v[210:213], v[98:101]
	v_mfma_f32_16x16x32_bf16 v[94:97], v[186:189], v[220:223], v[94:97]
	v_mfma_f32_16x16x32_bf16 v[82:85], v[194:197], v[220:223], v[82:85]
	v_mfma_f32_16x16x32_bf16 v[78:81], v[186:189], v[228:231], v[78:81]
	v_mfma_f32_16x16x32_bf16 v[66:69], v[194:197], v[228:231], v[66:69]
	s_barrier
	s_setprio 0
	v_lshl_add_u64 v[152:153], s[26:27], 0, v[162:163]
	s_add_i32 s26, s94, s86
	s_mov_b32 m0, s26
	ds_read_b128 v[198:201], v172 offset:16384
	ds_read_b128 v[202:205], v172 offset:17408
	ds_read_b128 v[206:209], v172 offset:18432
	ds_read_b128 v[210:213], v172 offset:19456
	ds_read_b128 v[214:217], v172 offset:20480
	ds_read_b128 v[220:223], v172 offset:21504
	ds_read_b128 v[224:227], v172 offset:22528
	ds_read_b128 v[228:231], v172 offset:23552
	global_load_lds_dwordx4 v[152:153], off
	v_lshl_add_u64 v[232:233], v[152:153], 0, s[10:11]
	s_add_i32 m0, s26, 0x2000
	s_add_i32 s26, s95, s86
	global_load_lds_dwordx4 v[232:233], off
	v_lshl_add_u64 v[232:233], v[152:153], 0, s[12:13]
	s_mov_b32 m0, s26
	v_lshl_add_u64 v[234:235], s[82:83], 0, v[132:133]
	global_load_lds_dwordx4 v[232:233], off
	v_lshl_add_u64 v[232:233], v[152:153], 0, s[14:15]
	s_add_i32 m0, s26, 0x2000
	s_nop 0
	global_load_lds_dwordx4 v[232:233], off
	v_lshl_add_u64 v[232:233], s[82:83], 0, v[130:131]
	s_mov_b32 m0, s87
	s_nop 0
	global_load_lds_dwordx4 v[232:233], off
	s_mov_b32 m0, s88
	s_nop 0
	global_load_lds_dwordx4 v[234:235], off
	s_setprio 1
	s_waitcnt vmcnt(8)
	s_waitcnt lgkmcnt(0)
	s_barrier
	v_mfma_f32_16x16x32_bf16 v[58:61], v[144:147], v[198:201], v[58:61]
	v_mfma_f32_16x16x32_bf16 v[54:57], v[174:177], v[198:201], v[54:57]
	v_mfma_f32_16x16x32_bf16 v[42:45], v[144:147], v[206:209], v[42:45]
	v_mfma_f32_16x16x32_bf16 v[38:41], v[174:177], v[206:209], v[38:41]
	v_mfma_f32_16x16x32_bf16 v[26:29], v[144:147], v[214:217], v[26:29]
	v_mfma_f32_16x16x32_bf16 v[22:25], v[174:177], v[214:217], v[22:25]
	v_mfma_f32_16x16x32_bf16 v[10:13], v[144:147], v[224:227], v[10:13]
	v_mfma_f32_16x16x32_bf16 v[6:9], v[174:177], v[224:227], v[6:9]
	v_mfma_f32_16x16x32_bf16 v[58:61], v[148:151], v[202:205], v[58:61]
	v_mfma_f32_16x16x32_bf16 v[54:57], v[178:181], v[202:205], v[54:57]
	v_mfma_f32_16x16x32_bf16 v[42:45], v[148:151], v[210:213], v[42:45]
	v_mfma_f32_16x16x32_bf16 v[38:41], v[178:181], v[210:213], v[38:41]
	v_mfma_f32_16x16x32_bf16 v[26:29], v[148:151], v[220:223], v[26:29]
	v_mfma_f32_16x16x32_bf16 v[22:25], v[178:181], v[220:223], v[22:25]
	v_mfma_f32_16x16x32_bf16 v[10:13], v[148:151], v[228:231], v[10:13]
	v_mfma_f32_16x16x32_bf16 v[6:9], v[178:181], v[228:231], v[6:9]
	v_mfma_f32_16x16x32_bf16 v[62:65], v[182:185], v[198:201], v[62:65]
	v_mfma_f32_16x16x32_bf16 v[50:53], v[190:193], v[198:201], v[50:53]
	v_mfma_f32_16x16x32_bf16 v[46:49], v[182:185], v[206:209], v[46:49]
	v_mfma_f32_16x16x32_bf16 v[34:37], v[190:193], v[206:209], v[34:37]
	v_mfma_f32_16x16x32_bf16 v[30:33], v[182:185], v[214:217], v[30:33]
	v_mfma_f32_16x16x32_bf16 v[18:21], v[190:193], v[214:217], v[18:21]
	v_mfma_f32_16x16x32_bf16 v[14:17], v[182:185], v[224:227], v[14:17]
	v_mfma_f32_16x16x32_bf16 v[2:5], v[190:193], v[224:227], v[2:5]
	v_mfma_f32_16x16x32_bf16 v[62:65], v[186:189], v[202:205], v[62:65]
	v_mfma_f32_16x16x32_bf16 v[50:53], v[194:197], v[202:205], v[50:53]
	v_mfma_f32_16x16x32_bf16 v[46:49], v[186:189], v[210:213], v[46:49]
	v_mfma_f32_16x16x32_bf16 v[34:37], v[194:197], v[210:213], v[34:37]
	v_mfma_f32_16x16x32_bf16 v[30:33], v[186:189], v[220:223], v[30:33]
	v_mfma_f32_16x16x32_bf16 v[18:21], v[194:197], v[220:223], v[18:21]
	v_mfma_f32_16x16x32_bf16 v[14:17], v[186:189], v[228:231], v[14:17]
	v_mfma_f32_16x16x32_bf16 v[2:5], v[194:197], v[228:231], v[2:5]
	s_barrier
	s_setprio 0
	s_add_i32 s33, 0, 0x18000
	v_add_u32_e32 v136, s33, v167
	s_add_i32 s8, 0, 0x1c000
	ds_read_b128 v[144:147], v136
	ds_read_b128 v[148:151], v136 offset:1024
	ds_read_b128 v[174:177], v136 offset:2048
	ds_read_b128 v[178:181], v136 offset:3072
	v_add_u32_e32 v136, s8, v167
	ds_read_b128 v[182:185], v136
	ds_read_b128 v[186:189], v136 offset:1024
	ds_read_b128 v[190:193], v136 offset:2048
	ds_read_b128 v[194:197], v136 offset:3072
	s_add_u32 s26, s82, 0x80000
	s_addc_u32 s27, s83, 0
	s_mov_b32 m0, s89
	v_lshl_add_u64 v[236:237], s[26:27], 0, v[130:131]
	ds_read_b128 v[198:201], v172 offset:32768
	ds_read_b128 v[202:205], v172 offset:33792
	ds_read_b128 v[206:209], v172 offset:34816
	ds_read_b128 v[210:213], v172 offset:35840
	ds_read_b128 v[214:217], v172 offset:36864
	ds_read_b128 v[220:223], v172 offset:37888
	ds_read_b128 v[224:227], v172 offset:38912
	ds_read_b128 v[228:231], v172 offset:39936
	global_load_lds_dwordx4 v[236:237], off
	v_lshl_add_u64 v[236:237], s[26:27], 0, v[132:133]
	s_mov_b32 m0, s90
	s_nop 0
	global_load_lds_dwordx4 v[236:237], off
	s_setprio 1
	s_waitcnt vmcnt(8)
	s_waitcnt lgkmcnt(0)
	s_barrier
	v_mfma_f32_16x16x32_bf16 v[122:125], v[144:147], v[198:201], v[122:125]
	v_mfma_f32_16x16x32_bf16 v[118:121], v[174:177], v[198:201], v[118:121]
	v_mfma_f32_16x16x32_bf16 v[106:109], v[144:147], v[206:209], v[106:109]
	v_mfma_f32_16x16x32_bf16 v[102:105], v[174:177], v[206:209], v[102:105]
	v_mfma_f32_16x16x32_bf16 v[90:93], v[144:147], v[214:217], v[90:93]
	v_mfma_f32_16x16x32_bf16 v[86:89], v[174:177], v[214:217], v[86:89]
	v_mfma_f32_16x16x32_bf16 v[74:77], v[144:147], v[224:227], v[74:77]
	v_mfma_f32_16x16x32_bf16 v[70:73], v[174:177], v[224:227], v[70:73]
	v_mfma_f32_16x16x32_bf16 v[122:125], v[148:151], v[202:205], v[122:125]
	v_mfma_f32_16x16x32_bf16 v[118:121], v[178:181], v[202:205], v[118:121]
	v_mfma_f32_16x16x32_bf16 v[106:109], v[148:151], v[210:213], v[106:109]
	v_mfma_f32_16x16x32_bf16 v[102:105], v[178:181], v[210:213], v[102:105]
	v_mfma_f32_16x16x32_bf16 v[90:93], v[148:151], v[220:223], v[90:93]
	v_mfma_f32_16x16x32_bf16 v[86:89], v[178:181], v[220:223], v[86:89]
	v_mfma_f32_16x16x32_bf16 v[74:77], v[148:151], v[228:231], v[74:77]
	v_mfma_f32_16x16x32_bf16 v[70:73], v[178:181], v[228:231], v[70:73]
	v_mfma_f32_16x16x32_bf16 v[126:129], v[182:185], v[198:201], v[126:129]
	v_mfma_f32_16x16x32_bf16 v[114:117], v[190:193], v[198:201], v[114:117]
	v_mfma_f32_16x16x32_bf16 v[110:113], v[182:185], v[206:209], v[110:113]
	v_mfma_f32_16x16x32_bf16 v[98:101], v[190:193], v[206:209], v[98:101]
	v_mfma_f32_16x16x32_bf16 v[94:97], v[182:185], v[214:217], v[94:97]
	v_mfma_f32_16x16x32_bf16 v[82:85], v[190:193], v[214:217], v[82:85]
	v_mfma_f32_16x16x32_bf16 v[78:81], v[182:185], v[224:227], v[78:81]
	v_mfma_f32_16x16x32_bf16 v[66:69], v[190:193], v[224:227], v[66:69]
	v_mfma_f32_16x16x32_bf16 v[126:129], v[186:189], v[202:205], v[126:129]
	v_mfma_f32_16x16x32_bf16 v[114:117], v[194:197], v[202:205], v[114:117]
	v_mfma_f32_16x16x32_bf16 v[110:113], v[186:189], v[210:213], v[110:113]
	v_mfma_f32_16x16x32_bf16 v[98:101], v[194:197], v[210:213], v[98:101]
	v_mfma_f32_16x16x32_bf16 v[94:97], v[186:189], v[220:223], v[94:97]
	v_mfma_f32_16x16x32_bf16 v[82:85], v[194:197], v[220:223], v[82:85]
	v_mfma_f32_16x16x32_bf16 v[78:81], v[186:189], v[228:231], v[78:81]
	v_mfma_f32_16x16x32_bf16 v[66:69], v[194:197], v[228:231], v[66:69]
	s_barrier
	s_setprio 0
	s_add_i32 s9, s33, s86
	v_lshl_add_u64 v[236:237], v[152:153], 0, s[20:21]
	s_mov_b32 m0, s9
	ds_read_b128 v[198:201], v172 offset:49152
	ds_read_b128 v[202:205], v172 offset:50176
	ds_read_b128 v[206:209], v172 offset:51200
	ds_read_b128 v[210:213], v172 offset:52224
	ds_read_b128 v[214:217], v172 offset:53248
	ds_read_b128 v[220:223], v172 offset:54272
	ds_read_b128 v[224:227], v172 offset:55296
	ds_read_b128 v[228:231], v172 offset:56320
	global_load_lds_dwordx4 v[236:237], off
	v_lshl_add_u64 v[236:237], v[152:153], 0, s[22:23]
	s_add_i32 m0, s9, 0x2000
	s_add_i32 s8, s8, s86
	global_load_lds_dwordx4 v[236:237], off
	v_lshl_add_u64 v[236:237], v[152:153], 0, s[40:41]
	s_mov_b32 m0, s8
	v_lshl_add_u64 v[152:153], v[152:153], 0, s[44:45]
	global_load_lds_dwordx4 v[236:237], off
	s_add_i32 m0, s8, 0x2000
	s_nop 0
	global_load_lds_dwordx4 v[152:153], off
	v_lshl_add_u64 v[152:153], v[232:233], 0, s[24:25]
	s_mov_b32 m0, s91
	s_nop 0
	global_load_lds_dwordx4 v[152:153], off
	v_lshl_add_u64 v[152:153], v[234:235], 0, s[24:25]
	s_mov_b32 m0, s92
	s_nop 0
	global_load_lds_dwordx4 v[152:153], off
	s_setprio 1
	s_waitcnt vmcnt(8)
	s_waitcnt lgkmcnt(0)
	s_barrier
	v_mfma_f32_16x16x32_bf16 v[58:61], v[144:147], v[198:201], v[58:61]
	v_mfma_f32_16x16x32_bf16 v[54:57], v[174:177], v[198:201], v[54:57]
	v_mfma_f32_16x16x32_bf16 v[42:45], v[144:147], v[206:209], v[42:45]
	v_mfma_f32_16x16x32_bf16 v[38:41], v[174:177], v[206:209], v[38:41]
	v_mfma_f32_16x16x32_bf16 v[26:29], v[144:147], v[214:217], v[26:29]
	v_mfma_f32_16x16x32_bf16 v[22:25], v[174:177], v[214:217], v[22:25]
	v_mfma_f32_16x16x32_bf16 v[10:13], v[144:147], v[224:227], v[10:13]
	v_mfma_f32_16x16x32_bf16 v[6:9], v[174:177], v[224:227], v[6:9]
	v_mfma_f32_16x16x32_bf16 v[58:61], v[148:151], v[202:205], v[58:61]
	v_mfma_f32_16x16x32_bf16 v[54:57], v[178:181], v[202:205], v[54:57]
	v_mfma_f32_16x16x32_bf16 v[42:45], v[148:151], v[210:213], v[42:45]
	v_mfma_f32_16x16x32_bf16 v[38:41], v[178:181], v[210:213], v[38:41]
	v_mfma_f32_16x16x32_bf16 v[26:29], v[148:151], v[220:223], v[26:29]
	v_mfma_f32_16x16x32_bf16 v[22:25], v[178:181], v[220:223], v[22:25]
	v_mfma_f32_16x16x32_bf16 v[10:13], v[148:151], v[228:231], v[10:13]
	v_mfma_f32_16x16x32_bf16 v[6:9], v[178:181], v[228:231], v[6:9]
	v_mfma_f32_16x16x32_bf16 v[62:65], v[182:185], v[198:201], v[62:65]
	v_mfma_f32_16x16x32_bf16 v[50:53], v[190:193], v[198:201], v[50:53]
	v_mfma_f32_16x16x32_bf16 v[46:49], v[182:185], v[206:209], v[46:49]
	v_mfma_f32_16x16x32_bf16 v[34:37], v[190:193], v[206:209], v[34:37]
	v_mfma_f32_16x16x32_bf16 v[30:33], v[182:185], v[214:217], v[30:33]
	v_mfma_f32_16x16x32_bf16 v[18:21], v[190:193], v[214:217], v[18:21]
	v_mfma_f32_16x16x32_bf16 v[14:17], v[182:185], v[224:227], v[14:17]
	v_mfma_f32_16x16x32_bf16 v[2:5], v[190:193], v[224:227], v[2:5]
	v_mfma_f32_16x16x32_bf16 v[62:65], v[186:189], v[202:205], v[62:65]
	v_mfma_f32_16x16x32_bf16 v[50:53], v[194:197], v[202:205], v[50:53]
	v_mfma_f32_16x16x32_bf16 v[46:49], v[186:189], v[210:213], v[46:49]
	v_mfma_f32_16x16x32_bf16 v[34:37], v[194:197], v[210:213], v[34:37]
	v_mfma_f32_16x16x32_bf16 v[30:33], v[186:189], v[220:223], v[30:33]
	v_mfma_f32_16x16x32_bf16 v[18:21], v[194:197], v[220:223], v[18:21]
	v_mfma_f32_16x16x32_bf16 v[14:17], v[186:189], v[228:231], v[14:17]
	v_mfma_f32_16x16x32_bf16 v[2:5], v[194:197], v[228:231], v[2:5]
	s_barrier
	s_setprio 0
	s_add_i32 vcc_hi, vcc_hi, 2
	s_add_u32 s97, s97, 0x10000
	s_addc_u32 vcc_lo, vcc_lo, 0
	s_add_u32 s80, s80, 0x100
	s_addc_u32 s81, s81, 0
	s_cmp_gt_u32 vcc_hi, 29
	s_cbranch_scc0 .LBB0_261
	s_and_b64 vcc, exec, s[50:51]
	s_cbranch_vccz .LBB0_264
	s_barrier
	s_setprio 3

.LBB0_284:
	s_ashr_i32 s51, s50, 31
	s_lshl_b64 s[26:27], s[50:51], 19
	v_readlane_b32 s54, v254, 58
	v_readlane_b32 s55, v254, 59
	s_add_u32 s54, s54, s26
	s_addc_u32 s55, s55, s27
	s_and_b64 s[26:27], s[0:1], exec
	s_cselect_b32 s51, s55, s73
	s_cselect_b32 s90, s54, s72
	s_ashr_i32 s45, s44, 31
	s_lshl_b64 s[26:27], s[44:45], 19
	s_add_u32 s56, s81, s26
	s_addc_u32 s57, s82, s27
	s_and_b64 s[26:27], s[0:1], exec
	s_cselect_b32 s45, s57, s71
	s_cselect_b32 s91, s56, s70
	s_add_u32 s92, s70, 0x10000
	s_addc_u32 s93, s71, 0
	s_add_u32 s70, s72, 0x40080
	s_addc_u32 s71, s73, 0
	s_mov_b32 s94, -2
	ds_read_b128 v[26:29], v1
	ds_read_b128 v[30:33], v1 offset:1024
	ds_read_b128 v[18:21], v1 offset:2048
	ds_read_b128 v[22:25], v1 offset:3072
	ds_read_b128 v[10:13], v185
	ds_read_b128 v[14:17], v185 offset:1024
	ds_read_b128 v[2:5], v185 offset:2048
	ds_read_b128 v[6:9], v185 offset:3072
	s_add_u32 s26, s70, 0xfffc0080
	s_addc_u32 s27, s71, -1
	s_cmp_eq_u32 s94, 12
	s_cselect_b32 s73, s51, s27
	s_cselect_b32 s72, s90, s26
	s_cselect_b32 s75, s45, s93
	s_cselect_b32 s74, s91, s92
	v_lshl_add_u64 v[176:177], s[70:71], 0, v[168:169]
	s_add_i32 m0, s33, 0xc000
	ds_read_b128 v[190:193], v186
	ds_read_b128 v[194:197], v186 offset:1024
	ds_read_b128 v[198:201], v186 offset:2048
	ds_read_b128 v[202:205], v186 offset:3072
	ds_read_b128 v[206:209], v186 offset:4096
	ds_read_b128 v[210:213], v186 offset:5120
	ds_read_b128 v[220:223], v186 offset:6144
	ds_read_b128 v[224:227], v186 offset:7168
	global_load_lds_dwordx4 v[176:177], off
	v_lshl_add_u64 v[176:177], s[70:71], 0, v[170:171]
	s_add_i32 m0, s33, 0xe000
	s_nop 0
	global_load_lds_dwordx4 v[176:177], off
	s_setprio 1
	s_waitcnt vmcnt(24)
	s_waitcnt lgkmcnt(0)
	s_barrier
	v_mfma_scale_f32_16x16x128_f8f6f4 v[158:161], v[26:33], v[190:197], 0, v187, v188 op_sel_hi:[0,0,0]
	v_mfma_scale_f32_16x16x128_f8f6f4 v[154:157], v[18:25], v[190:197], 0, v187, v188 op_sel_hi:[0,0,0]
	v_mfma_scale_f32_16x16x128_f8f6f4 v[150:153], v[26:33], v[198:205], 0, v187, v188 op_sel_hi:[0,0,0]
	v_mfma_scale_f32_16x16x128_f8f6f4 v[142:145], v[18:25], v[198:205], 0, v187, v188 op_sel_hi:[0,0,0]
	v_mfma_scale_f32_16x16x128_f8f6f4 v[134:137], v[26:33], v[206:213], 0, v187, v188 op_sel_hi:[0,0,0]
	v_mfma_scale_f32_16x16x128_f8f6f4 v[126:129], v[18:25], v[206:213], 0, v187, v188 op_sel_hi:[0,0,0]
	v_mfma_scale_f32_16x16x128_f8f6f4 v[118:121], v[26:33], v[220:227], 0, v187, v188 op_sel_hi:[0,0,0]
	v_mfma_scale_f32_16x16x128_f8f6f4 v[110:113], v[18:25], v[220:227], 0, v187, v188 op_sel_hi:[0,0,0]
	v_mfma_scale_f32_16x16x128_f8f6f4 v[146:149], v[10:17], v[190:197], 0, v187, v188 op_sel_hi:[0,0,0]
	v_mfma_scale_f32_16x16x128_f8f6f4 v[138:141], v[2:9], v[190:197], 0, v187, v188 op_sel_hi:[0,0,0]
	v_mfma_scale_f32_16x16x128_f8f6f4 v[130:133], v[10:17], v[198:205], 0, v187, v188 op_sel_hi:[0,0,0]
	v_mfma_scale_f32_16x16x128_f8f6f4 v[122:125], v[2:9], v[198:205], 0, v187, v188 op_sel_hi:[0,0,0]
	v_mfma_scale_f32_16x16x128_f8f6f4 v[114:117], v[10:17], v[206:213], 0, v187, v188 op_sel_hi:[0,0,0]
	v_mfma_scale_f32_16x16x128_f8f6f4 v[106:109], v[2:9], v[206:213], 0, v187, v188 op_sel_hi:[0,0,0]
	v_mfma_scale_f32_16x16x128_f8f6f4 v[102:105], v[10:17], v[220:227], 0, v187, v188 op_sel_hi:[0,0,0]
	v_mfma_scale_f32_16x16x128_f8f6f4 v[98:101], v[2:9], v[220:227], 0, v187, v188 op_sel_hi:[0,0,0]
	s_barrier
	s_setprio 0
	s_add_i32 s26, s88, s80
	v_lshl_add_u64 v[176:177], s[74:75], 0, v[162:163]
	s_mov_b32 m0, s26
	ds_read_b128 v[190:193], v186 offset:16384
	ds_read_b128 v[194:197], v186 offset:17408
	ds_read_b128 v[198:201], v186 offset:18432
	ds_read_b128 v[202:205], v186 offset:19456
	ds_read_b128 v[206:209], v186 offset:20480
	ds_read_b128 v[210:213], v186 offset:21504
	ds_read_b128 v[220:223], v186 offset:22528
	ds_read_b128 v[224:227], v186 offset:23552
	global_load_lds_dwordx4 v[176:177], off
	v_lshl_add_u64 v[178:179], v[176:177], 0, s[8:9]
	s_add_i32 m0, s26, 0x2000
	s_add_i32 s26, s89, s80
	global_load_lds_dwordx4 v[178:179], off
	v_lshl_add_u64 v[178:179], v[176:177], 0, s[10:11]
	s_mov_b32 m0, s26
	v_lshl_add_u64 v[180:181], s[72:73], 0, v[166:167]
	global_load_lds_dwordx4 v[178:179], off
	v_lshl_add_u64 v[178:179], v[176:177], 0, s[12:13]
	s_add_i32 m0, s26, 0x2000
	s_nop 0
	global_load_lds_dwordx4 v[178:179], off
	v_lshl_add_u64 v[178:179], s[72:73], 0, v[164:165]
	s_mov_b32 m0, s33
	s_nop 0
	global_load_lds_dwordx4 v[178:179], off
	s_mov_b32 m0, s69
	s_nop 0
	global_load_lds_dwordx4 v[180:181], off
	s_setprio 1
	s_waitcnt vmcnt(24)
	s_waitcnt lgkmcnt(0)
	s_barrier
	v_mfma_scale_f32_16x16x128_f8f6f4 v[94:97], v[26:33], v[190:197], 0, v187, v188 op_sel_hi:[0,0,0]
	v_mfma_scale_f32_16x16x128_f8f6f4 v[90:93], v[18:25], v[190:197], 0, v187, v188 op_sel_hi:[0,0,0]
	v_mfma_scale_f32_16x16x128_f8f6f4 v[86:89], v[26:33], v[198:205], 0, v187, v188 op_sel_hi:[0,0,0]
	v_mfma_scale_f32_16x16x128_f8f6f4 v[78:81], v[18:25], v[198:205], 0, v187, v188 op_sel_hi:[0,0,0]
	v_mfma_scale_f32_16x16x128_f8f6f4 v[70:73], v[26:33], v[206:213], 0, v187, v188 op_sel_hi:[0,0,0]
	v_mfma_scale_f32_16x16x128_f8f6f4 v[62:65], v[18:25], v[206:213], 0, v187, v188 op_sel_hi:[0,0,0]
	v_mfma_scale_f32_16x16x128_f8f6f4 v[54:57], v[26:33], v[220:227], 0, v187, v188 op_sel_hi:[0,0,0]
	v_mfma_scale_f32_16x16x128_f8f6f4 v[46:49], v[18:25], v[220:227], 0, v187, v188 op_sel_hi:[0,0,0]
	v_mfma_scale_f32_16x16x128_f8f6f4 v[82:85], v[10:17], v[190:197], 0, v187, v188 op_sel_hi:[0,0,0]
	v_mfma_scale_f32_16x16x128_f8f6f4 v[74:77], v[2:9], v[190:197], 0, v187, v188 op_sel_hi:[0,0,0]
	v_mfma_scale_f32_16x16x128_f8f6f4 v[66:69], v[10:17], v[198:205], 0, v187, v188 op_sel_hi:[0,0,0]
	v_mfma_scale_f32_16x16x128_f8f6f4 v[58:61], v[2:9], v[198:205], 0, v187, v188 op_sel_hi:[0,0,0]
	v_mfma_scale_f32_16x16x128_f8f6f4 v[50:53], v[10:17], v[206:213], 0, v187, v188 op_sel_hi:[0,0,0]
	v_mfma_scale_f32_16x16x128_f8f6f4 v[42:45], v[2:9], v[206:213], 0, v187, v188 op_sel_hi:[0,0,0]
	v_mfma_scale_f32_16x16x128_f8f6f4 v[38:41], v[10:17], v[220:227], 0, v187, v188 op_sel_hi:[0,0,0]
	v_mfma_scale_f32_16x16x128_f8f6f4 v[34:37], v[2:9], v[220:227], 0, v187, v188 op_sel_hi:[0,0,0]
	s_barrier
	s_setprio 0
	s_add_i32 s74, 0, 0x18000
	s_add_i32 s75, 0, 0x1c000
	v_add_u32_e32 v14, s74, v183
	v_add_u32_e32 v30, s75, v183
	ds_read_b128 v[2:5], v14
	ds_read_b128 v[6:9], v14 offset:1024
	ds_read_b128 v[10:13], v14 offset:2048
	ds_read_b128 v[14:17], v14 offset:3072
	ds_read_b128 v[18:21], v30
	ds_read_b128 v[22:25], v30 offset:1024
	ds_read_b128 v[26:29], v30 offset:2048
	ds_read_b128 v[30:33], v30 offset:3072
	s_add_u32 s26, s72, 0x40000
	s_addc_u32 s27, s73, 0
	s_mov_b32 m0, s83
	v_lshl_add_u64 v[214:215], s[26:27], 0, v[164:165]
	ds_read_b128 v[190:193], v186 offset:32768
	ds_read_b128 v[194:197], v186 offset:33792
	ds_read_b128 v[198:201], v186 offset:34816
	ds_read_b128 v[202:205], v186 offset:35840
	ds_read_b128 v[206:209], v186 offset:36864
	ds_read_b128 v[210:213], v186 offset:37888
	ds_read_b128 v[220:223], v186 offset:38912
	ds_read_b128 v[224:227], v186 offset:39936
	global_load_lds_dwordx4 v[214:215], off
	v_lshl_add_u64 v[214:215], s[26:27], 0, v[166:167]
	s_mov_b32 m0, s84
	s_nop 0
	global_load_lds_dwordx4 v[214:215], off
	s_setprio 1
	s_waitcnt vmcnt(8)
	s_waitcnt lgkmcnt(0)
	s_barrier
	v_mfma_scale_f32_16x16x128_f8f6f4 v[158:161], v[2:9], v[190:197], v[158:161], v187, v188 op_sel_hi:[0,0,0]
	v_mfma_scale_f32_16x16x128_f8f6f4 v[154:157], v[10:17], v[190:197], v[154:157], v187, v188 op_sel_hi:[0,0,0]
	v_mfma_scale_f32_16x16x128_f8f6f4 v[150:153], v[2:9], v[198:205], v[150:153], v187, v188 op_sel_hi:[0,0,0]
	v_mfma_scale_f32_16x16x128_f8f6f4 v[142:145], v[10:17], v[198:205], v[142:145], v187, v188 op_sel_hi:[0,0,0]
	v_mfma_scale_f32_16x16x128_f8f6f4 v[134:137], v[2:9], v[206:213], v[134:137], v187, v188 op_sel_hi:[0,0,0]
	v_mfma_scale_f32_16x16x128_f8f6f4 v[126:129], v[10:17], v[206:213], v[126:129], v187, v188 op_sel_hi:[0,0,0]
	v_mfma_scale_f32_16x16x128_f8f6f4 v[118:121], v[2:9], v[220:227], v[118:121], v187, v188 op_sel_hi:[0,0,0]
	v_mfma_scale_f32_16x16x128_f8f6f4 v[110:113], v[10:17], v[220:227], v[110:113], v187, v188 op_sel_hi:[0,0,0]
	v_mfma_scale_f32_16x16x128_f8f6f4 v[146:149], v[18:25], v[190:197], v[146:149], v187, v188 op_sel_hi:[0,0,0]
	v_mfma_scale_f32_16x16x128_f8f6f4 v[138:141], v[26:33], v[190:197], v[138:141], v187, v188 op_sel_hi:[0,0,0]
	v_mfma_scale_f32_16x16x128_f8f6f4 v[130:133], v[18:25], v[198:205], v[130:133], v187, v188 op_sel_hi:[0,0,0]
	v_mfma_scale_f32_16x16x128_f8f6f4 v[122:125], v[26:33], v[198:205], v[122:125], v187, v188 op_sel_hi:[0,0,0]
	v_mfma_scale_f32_16x16x128_f8f6f4 v[114:117], v[18:25], v[206:213], v[114:117], v187, v188 op_sel_hi:[0,0,0]
	v_mfma_scale_f32_16x16x128_f8f6f4 v[106:109], v[26:33], v[206:213], v[106:109], v187, v188 op_sel_hi:[0,0,0]
	v_mfma_scale_f32_16x16x128_f8f6f4 v[102:105], v[18:25], v[220:227], v[102:105], v187, v188 op_sel_hi:[0,0,0]
	v_mfma_scale_f32_16x16x128_f8f6f4 v[98:101], v[26:33], v[220:227], v[98:101], v187, v188 op_sel_hi:[0,0,0]
	s_barrier
	s_setprio 0
	s_add_i32 s26, s74, s80
	v_lshl_add_u64 v[214:215], v[176:177], 0, s[16:17]
	s_mov_b32 m0, s26
	ds_read_b128 v[190:193], v186 offset:49152
	ds_read_b128 v[194:197], v186 offset:50176
	ds_read_b128 v[198:201], v186 offset:51200
	ds_read_b128 v[202:205], v186 offset:52224
	ds_read_b128 v[206:209], v186 offset:53248
	ds_read_b128 v[210:213], v186 offset:54272
	ds_read_b128 v[220:223], v186 offset:55296
	ds_read_b128 v[224:227], v186 offset:56320
	global_load_lds_dwordx4 v[214:215], off
	v_lshl_add_u64 v[214:215], v[176:177], 0, s[18:19]
	s_add_i32 m0, s26, 0x2000
	s_add_i32 s26, s75, s80
	global_load_lds_dwordx4 v[214:215], off
	v_lshl_add_u64 v[214:215], v[176:177], 0, s[22:23]
	s_mov_b32 m0, s26
	v_lshl_add_u64 v[176:177], v[176:177], 0, s[24:25]
	global_load_lds_dwordx4 v[214:215], off
	s_add_i32 m0, s26, 0x2000
	s_nop 0
	global_load_lds_dwordx4 v[176:177], off
	v_lshl_add_u64 v[176:177], v[178:179], 0, s[20:21]
	s_mov_b32 m0, s86
	s_nop 0
	global_load_lds_dwordx4 v[176:177], off
	v_lshl_add_u64 v[176:177], v[180:181], 0, s[20:21]
	s_mov_b32 m0, s87
	s_nop 0
	global_load_lds_dwordx4 v[176:177], off
	s_setprio 1
	s_waitcnt vmcnt(8)
	s_waitcnt lgkmcnt(0)
	s_barrier
	v_mfma_scale_f32_16x16x128_f8f6f4 v[94:97], v[2:9], v[190:197], v[94:97], v187, v188 op_sel_hi:[0,0,0]
	v_mfma_scale_f32_16x16x128_f8f6f4 v[90:93], v[10:17], v[190:197], v[90:93], v187, v188 op_sel_hi:[0,0,0]
	v_mfma_scale_f32_16x16x128_f8f6f4 v[86:89], v[2:9], v[198:205], v[86:89], v187, v188 op_sel_hi:[0,0,0]
	v_mfma_scale_f32_16x16x128_f8f6f4 v[78:81], v[10:17], v[198:205], v[78:81], v187, v188 op_sel_hi:[0,0,0]
	v_mfma_scale_f32_16x16x128_f8f6f4 v[70:73], v[2:9], v[206:213], v[70:73], v187, v188 op_sel_hi:[0,0,0]
	v_mfma_scale_f32_16x16x128_f8f6f4 v[62:65], v[10:17], v[206:213], v[62:65], v187, v188 op_sel_hi:[0,0,0]
	v_mfma_scale_f32_16x16x128_f8f6f4 v[54:57], v[2:9], v[220:227], v[54:57], v187, v188 op_sel_hi:[0,0,0]
	v_mfma_scale_f32_16x16x128_f8f6f4 v[46:49], v[10:17], v[220:227], v[46:49], v187, v188 op_sel_hi:[0,0,0]
	v_mfma_scale_f32_16x16x128_f8f6f4 v[82:85], v[18:25], v[190:197], v[82:85], v187, v188 op_sel_hi:[0,0,0]
	v_mfma_scale_f32_16x16x128_f8f6f4 v[74:77], v[26:33], v[190:197], v[74:77], v187, v188 op_sel_hi:[0,0,0]
	v_mfma_scale_f32_16x16x128_f8f6f4 v[66:69], v[18:25], v[198:205], v[66:69], v187, v188 op_sel_hi:[0,0,0]
	v_mfma_scale_f32_16x16x128_f8f6f4 v[58:61], v[26:33], v[198:205], v[58:61], v187, v188 op_sel_hi:[0,0,0]
	v_mfma_scale_f32_16x16x128_f8f6f4 v[50:53], v[18:25], v[206:213], v[50:53], v187, v188 op_sel_hi:[0,0,0]
	v_mfma_scale_f32_16x16x128_f8f6f4 v[42:45], v[26:33], v[206:213], v[42:45], v187, v188 op_sel_hi:[0,0,0]
	v_mfma_scale_f32_16x16x128_f8f6f4 v[38:41], v[18:25], v[220:227], v[38:41], v187, v188 op_sel_hi:[0,0,0]
	v_mfma_scale_f32_16x16x128_f8f6f4 v[34:37], v[26:33], v[220:227], v[34:37], v187, v188 op_sel_hi:[0,0,0]
	s_barrier
	s_setprio 0
	s_add_i32 s94, s94, 2
	s_add_u32 s92, s92, 0x10000
	s_addc_u32 s93, s93, 0
	s_add_u32 s70, s70, 0x100
	s_addc_u32 s71, s71, 0
	s_cmp_gt_u32 s94, 13
.LBB0_285:
	ds_read_b128 v[26:29], v1
	ds_read_b128 v[30:33], v1 offset:1024
	ds_read_b128 v[18:21], v1 offset:2048
	ds_read_b128 v[22:25], v1 offset:3072
	ds_read_b128 v[10:13], v185
	ds_read_b128 v[14:17], v185 offset:1024
	ds_read_b128 v[2:5], v185 offset:2048
	ds_read_b128 v[6:9], v185 offset:3072
	s_add_u32 s26, s70, 0xfffc0080
	s_addc_u32 s27, s71, -1
	s_cmp_eq_u32 s94, 12
	s_cselect_b32 s73, s51, s27
	s_cselect_b32 s72, s90, s26
	s_cselect_b32 s75, s45, s93
	s_cselect_b32 s74, s91, s92
	v_lshl_add_u64 v[176:177], s[70:71], 0, v[168:169]
	s_add_i32 m0, s33, 0xc000
	ds_read_b128 v[190:193], v186
	ds_read_b128 v[194:197], v186 offset:1024
	ds_read_b128 v[198:201], v186 offset:2048
	ds_read_b128 v[202:205], v186 offset:3072
	ds_read_b128 v[206:209], v186 offset:4096
	ds_read_b128 v[210:213], v186 offset:5120
	ds_read_b128 v[220:223], v186 offset:6144
	ds_read_b128 v[224:227], v186 offset:7168
	global_load_lds_dwordx4 v[176:177], off
	v_lshl_add_u64 v[176:177], s[70:71], 0, v[170:171]
	s_add_i32 m0, s33, 0xe000
	s_nop 0
	global_load_lds_dwordx4 v[176:177], off
	s_setprio 1
	s_waitcnt vmcnt(8)
	s_waitcnt lgkmcnt(0)
	s_barrier
	v_mfma_scale_f32_16x16x128_f8f6f4 v[158:161], v[26:33], v[190:197], v[158:161], v187, v188 op_sel_hi:[0,0,0]
	v_mfma_scale_f32_16x16x128_f8f6f4 v[154:157], v[18:25], v[190:197], v[154:157], v187, v188 op_sel_hi:[0,0,0]
	v_mfma_scale_f32_16x16x128_f8f6f4 v[150:153], v[26:33], v[198:205], v[150:153], v187, v188 op_sel_hi:[0,0,0]
	v_mfma_scale_f32_16x16x128_f8f6f4 v[142:145], v[18:25], v[198:205], v[142:145], v187, v188 op_sel_hi:[0,0,0]
	v_mfma_scale_f32_16x16x128_f8f6f4 v[134:137], v[26:33], v[206:213], v[134:137], v187, v188 op_sel_hi:[0,0,0]
	v_mfma_scale_f32_16x16x128_f8f6f4 v[126:129], v[18:25], v[206:213], v[126:129], v187, v188 op_sel_hi:[0,0,0]
	v_mfma_scale_f32_16x16x128_f8f6f4 v[118:121], v[26:33], v[220:227], v[118:121], v187, v188 op_sel_hi:[0,0,0]
	v_mfma_scale_f32_16x16x128_f8f6f4 v[110:113], v[18:25], v[220:227], v[110:113], v187, v188 op_sel_hi:[0,0,0]
	v_mfma_scale_f32_16x16x128_f8f6f4 v[146:149], v[10:17], v[190:197], v[146:149], v187, v188 op_sel_hi:[0,0,0]
	v_mfma_scale_f32_16x16x128_f8f6f4 v[138:141], v[2:9], v[190:197], v[138:141], v187, v188 op_sel_hi:[0,0,0]
	v_mfma_scale_f32_16x16x128_f8f6f4 v[130:133], v[10:17], v[198:205], v[130:133], v187, v188 op_sel_hi:[0,0,0]
	v_mfma_scale_f32_16x16x128_f8f6f4 v[122:125], v[2:9], v[198:205], v[122:125], v187, v188 op_sel_hi:[0,0,0]
	v_mfma_scale_f32_16x16x128_f8f6f4 v[114:117], v[10:17], v[206:213], v[114:117], v187, v188 op_sel_hi:[0,0,0]
	v_mfma_scale_f32_16x16x128_f8f6f4 v[106:109], v[2:9], v[206:213], v[106:109], v187, v188 op_sel_hi:[0,0,0]
	v_mfma_scale_f32_16x16x128_f8f6f4 v[102:105], v[10:17], v[220:227], v[102:105], v187, v188 op_sel_hi:[0,0,0]
	v_mfma_scale_f32_16x16x128_f8f6f4 v[98:101], v[2:9], v[220:227], v[98:101], v187, v188 op_sel_hi:[0,0,0]
	s_barrier
	s_setprio 0
	s_add_i32 s26, s88, s80
	v_lshl_add_u64 v[176:177], s[74:75], 0, v[162:163]
	s_mov_b32 m0, s26
	ds_read_b128 v[190:193], v186 offset:16384
	ds_read_b128 v[194:197], v186 offset:17408
	ds_read_b128 v[198:201], v186 offset:18432
	ds_read_b128 v[202:205], v186 offset:19456
	ds_read_b128 v[206:209], v186 offset:20480
	ds_read_b128 v[210:213], v186 offset:21504
	ds_read_b128 v[220:223], v186 offset:22528
	ds_read_b128 v[224:227], v186 offset:23552
	global_load_lds_dwordx4 v[176:177], off
	v_lshl_add_u64 v[178:179], v[176:177], 0, s[8:9]
	s_add_i32 m0, s26, 0x2000
	s_add_i32 s26, s89, s80
	global_load_lds_dwordx4 v[178:179], off
	v_lshl_add_u64 v[178:179], v[176:177], 0, s[10:11]
	s_mov_b32 m0, s26
	v_lshl_add_u64 v[180:181], s[72:73], 0, v[166:167]
	global_load_lds_dwordx4 v[178:179], off
	v_lshl_add_u64 v[178:179], v[176:177], 0, s[12:13]
	s_add_i32 m0, s26, 0x2000
	s_nop 0
	global_load_lds_dwordx4 v[178:179], off
	v_lshl_add_u64 v[178:179], s[72:73], 0, v[164:165]
	s_mov_b32 m0, s33
	s_nop 0
	global_load_lds_dwordx4 v[178:179], off
	s_mov_b32 m0, s69
	s_nop 0
	global_load_lds_dwordx4 v[180:181], off
	s_setprio 1
	s_waitcnt vmcnt(8)
	s_waitcnt lgkmcnt(0)
	s_barrier
	v_mfma_scale_f32_16x16x128_f8f6f4 v[94:97], v[26:33], v[190:197], v[94:97], v187, v188 op_sel_hi:[0,0,0]
	v_mfma_scale_f32_16x16x128_f8f6f4 v[90:93], v[18:25], v[190:197], v[90:93], v187, v188 op_sel_hi:[0,0,0]
	v_mfma_scale_f32_16x16x128_f8f6f4 v[86:89], v[26:33], v[198:205], v[86:89], v187, v188 op_sel_hi:[0,0,0]
	v_mfma_scale_f32_16x16x128_f8f6f4 v[78:81], v[18:25], v[198:205], v[78:81], v187, v188 op_sel_hi:[0,0,0]
	v_mfma_scale_f32_16x16x128_f8f6f4 v[70:73], v[26:33], v[206:213], v[70:73], v187, v188 op_sel_hi:[0,0,0]
	v_mfma_scale_f32_16x16x128_f8f6f4 v[62:65], v[18:25], v[206:213], v[62:65], v187, v188 op_sel_hi:[0,0,0]
	v_mfma_scale_f32_16x16x128_f8f6f4 v[54:57], v[26:33], v[220:227], v[54:57], v187, v188 op_sel_hi:[0,0,0]
	v_mfma_scale_f32_16x16x128_f8f6f4 v[46:49], v[18:25], v[220:227], v[46:49], v187, v188 op_sel_hi:[0,0,0]
	v_mfma_scale_f32_16x16x128_f8f6f4 v[82:85], v[10:17], v[190:197], v[82:85], v187, v188 op_sel_hi:[0,0,0]
	v_mfma_scale_f32_16x16x128_f8f6f4 v[74:77], v[2:9], v[190:197], v[74:77], v187, v188 op_sel_hi:[0,0,0]
	v_mfma_scale_f32_16x16x128_f8f6f4 v[66:69], v[10:17], v[198:205], v[66:69], v187, v188 op_sel_hi:[0,0,0]
	v_mfma_scale_f32_16x16x128_f8f6f4 v[58:61], v[2:9], v[198:205], v[58:61], v187, v188 op_sel_hi:[0,0,0]
	v_mfma_scale_f32_16x16x128_f8f6f4 v[50:53], v[10:17], v[206:213], v[50:53], v187, v188 op_sel_hi:[0,0,0]
	v_mfma_scale_f32_16x16x128_f8f6f4 v[42:45], v[2:9], v[206:213], v[42:45], v187, v188 op_sel_hi:[0,0,0]
	v_mfma_scale_f32_16x16x128_f8f6f4 v[38:41], v[10:17], v[220:227], v[38:41], v187, v188 op_sel_hi:[0,0,0]
	v_mfma_scale_f32_16x16x128_f8f6f4 v[34:37], v[2:9], v[220:227], v[34:37], v187, v188 op_sel_hi:[0,0,0]
	s_barrier
	s_setprio 0
	s_add_i32 s74, 0, 0x18000
	s_add_i32 s75, 0, 0x1c000
	v_add_u32_e32 v14, s74, v183
	v_add_u32_e32 v30, s75, v183
	ds_read_b128 v[2:5], v14
	ds_read_b128 v[6:9], v14 offset:1024
	ds_read_b128 v[10:13], v14 offset:2048
	ds_read_b128 v[14:17], v14 offset:3072
	ds_read_b128 v[18:21], v30
	ds_read_b128 v[22:25], v30 offset:1024
	ds_read_b128 v[26:29], v30 offset:2048
	ds_read_b128 v[30:33], v30 offset:3072
	s_add_u32 s26, s72, 0x40000
	s_addc_u32 s27, s73, 0
	s_mov_b32 m0, s83
	v_lshl_add_u64 v[214:215], s[26:27], 0, v[164:165]
	ds_read_b128 v[190:193], v186 offset:32768
	ds_read_b128 v[194:197], v186 offset:33792
	ds_read_b128 v[198:201], v186 offset:34816
	ds_read_b128 v[202:205], v186 offset:35840
	ds_read_b128 v[206:209], v186 offset:36864
	ds_read_b128 v[210:213], v186 offset:37888
	ds_read_b128 v[220:223], v186 offset:38912
	ds_read_b128 v[224:227], v186 offset:39936
	global_load_lds_dwordx4 v[214:215], off
	v_lshl_add_u64 v[214:215], s[26:27], 0, v[166:167]
	s_mov_b32 m0, s84
	s_nop 0
	global_load_lds_dwordx4 v[214:215], off
	s_setprio 1
	s_waitcnt vmcnt(8)
	s_waitcnt lgkmcnt(0)
	s_barrier
	v_mfma_scale_f32_16x16x128_f8f6f4 v[158:161], v[2:9], v[190:197], v[158:161], v187, v188 op_sel_hi:[0,0,0]
	v_mfma_scale_f32_16x16x128_f8f6f4 v[154:157], v[10:17], v[190:197], v[154:157], v187, v188 op_sel_hi:[0,0,0]
	v_mfma_scale_f32_16x16x128_f8f6f4 v[150:153], v[2:9], v[198:205], v[150:153], v187, v188 op_sel_hi:[0,0,0]
	v_mfma_scale_f32_16x16x128_f8f6f4 v[142:145], v[10:17], v[198:205], v[142:145], v187, v188 op_sel_hi:[0,0,0]
	v_mfma_scale_f32_16x16x128_f8f6f4 v[134:137], v[2:9], v[206:213], v[134:137], v187, v188 op_sel_hi:[0,0,0]
	v_mfma_scale_f32_16x16x128_f8f6f4 v[126:129], v[10:17], v[206:213], v[126:129], v187, v188 op_sel_hi:[0,0,0]
	v_mfma_scale_f32_16x16x128_f8f6f4 v[118:121], v[2:9], v[220:227], v[118:121], v187, v188 op_sel_hi:[0,0,0]
	v_mfma_scale_f32_16x16x128_f8f6f4 v[110:113], v[10:17], v[220:227], v[110:113], v187, v188 op_sel_hi:[0,0,0]
	v_mfma_scale_f32_16x16x128_f8f6f4 v[146:149], v[18:25], v[190:197], v[146:149], v187, v188 op_sel_hi:[0,0,0]
	v_mfma_scale_f32_16x16x128_f8f6f4 v[138:141], v[26:33], v[190:197], v[138:141], v187, v188 op_sel_hi:[0,0,0]
	v_mfma_scale_f32_16x16x128_f8f6f4 v[130:133], v[18:25], v[198:205], v[130:133], v187, v188 op_sel_hi:[0,0,0]
	v_mfma_scale_f32_16x16x128_f8f6f4 v[122:125], v[26:33], v[198:205], v[122:125], v187, v188 op_sel_hi:[0,0,0]
	v_mfma_scale_f32_16x16x128_f8f6f4 v[114:117], v[18:25], v[206:213], v[114:117], v187, v188 op_sel_hi:[0,0,0]
	v_mfma_scale_f32_16x16x128_f8f6f4 v[106:109], v[26:33], v[206:213], v[106:109], v187, v188 op_sel_hi:[0,0,0]
	v_mfma_scale_f32_16x16x128_f8f6f4 v[102:105], v[18:25], v[220:227], v[102:105], v187, v188 op_sel_hi:[0,0,0]
	v_mfma_scale_f32_16x16x128_f8f6f4 v[98:101], v[26:33], v[220:227], v[98:101], v187, v188 op_sel_hi:[0,0,0]
	s_barrier
	s_setprio 0
	s_add_i32 s26, s74, s80
	v_lshl_add_u64 v[214:215], v[176:177], 0, s[16:17]
	s_mov_b32 m0, s26
	ds_read_b128 v[190:193], v186 offset:49152
	ds_read_b128 v[194:197], v186 offset:50176
	ds_read_b128 v[198:201], v186 offset:51200
	ds_read_b128 v[202:205], v186 offset:52224
	ds_read_b128 v[206:209], v186 offset:53248
	ds_read_b128 v[210:213], v186 offset:54272
	ds_read_b128 v[220:223], v186 offset:55296
	ds_read_b128 v[224:227], v186 offset:56320
	global_load_lds_dwordx4 v[214:215], off
	v_lshl_add_u64 v[214:215], v[176:177], 0, s[18:19]
	s_add_i32 m0, s26, 0x2000
	s_add_i32 s26, s75, s80
	global_load_lds_dwordx4 v[214:215], off
	v_lshl_add_u64 v[214:215], v[176:177], 0, s[22:23]
	s_mov_b32 m0, s26
	v_lshl_add_u64 v[176:177], v[176:177], 0, s[24:25]
	global_load_lds_dwordx4 v[214:215], off
	s_add_i32 m0, s26, 0x2000
	s_nop 0
	global_load_lds_dwordx4 v[176:177], off
	v_lshl_add_u64 v[176:177], v[178:179], 0, s[20:21]
	s_mov_b32 m0, s86
	s_nop 0
	global_load_lds_dwordx4 v[176:177], off
	v_lshl_add_u64 v[176:177], v[180:181], 0, s[20:21]
	s_mov_b32 m0, s87
	s_nop 0
	global_load_lds_dwordx4 v[176:177], off
	s_setprio 1
	s_waitcnt vmcnt(8)
	s_waitcnt lgkmcnt(0)
	s_barrier
	v_mfma_scale_f32_16x16x128_f8f6f4 v[94:97], v[2:9], v[190:197], v[94:97], v187, v188 op_sel_hi:[0,0,0]
	v_mfma_scale_f32_16x16x128_f8f6f4 v[90:93], v[10:17], v[190:197], v[90:93], v187, v188 op_sel_hi:[0,0,0]
	v_mfma_scale_f32_16x16x128_f8f6f4 v[86:89], v[2:9], v[198:205], v[86:89], v187, v188 op_sel_hi:[0,0,0]
	v_mfma_scale_f32_16x16x128_f8f6f4 v[78:81], v[10:17], v[198:205], v[78:81], v187, v188 op_sel_hi:[0,0,0]
	v_mfma_scale_f32_16x16x128_f8f6f4 v[70:73], v[2:9], v[206:213], v[70:73], v187, v188 op_sel_hi:[0,0,0]
	v_mfma_scale_f32_16x16x128_f8f6f4 v[62:65], v[10:17], v[206:213], v[62:65], v187, v188 op_sel_hi:[0,0,0]
	v_mfma_scale_f32_16x16x128_f8f6f4 v[54:57], v[2:9], v[220:227], v[54:57], v187, v188 op_sel_hi:[0,0,0]
	v_mfma_scale_f32_16x16x128_f8f6f4 v[46:49], v[10:17], v[220:227], v[46:49], v187, v188 op_sel_hi:[0,0,0]
	v_mfma_scale_f32_16x16x128_f8f6f4 v[82:85], v[18:25], v[190:197], v[82:85], v187, v188 op_sel_hi:[0,0,0]
	v_mfma_scale_f32_16x16x128_f8f6f4 v[74:77], v[26:33], v[190:197], v[74:77], v187, v188 op_sel_hi:[0,0,0]
	v_mfma_scale_f32_16x16x128_f8f6f4 v[66:69], v[18:25], v[198:205], v[66:69], v187, v188 op_sel_hi:[0,0,0]
	v_mfma_scale_f32_16x16x128_f8f6f4 v[58:61], v[26:33], v[198:205], v[58:61], v187, v188 op_sel_hi:[0,0,0]
	v_mfma_scale_f32_16x16x128_f8f6f4 v[50:53], v[18:25], v[206:213], v[50:53], v187, v188 op_sel_hi:[0,0,0]
	v_mfma_scale_f32_16x16x128_f8f6f4 v[42:45], v[26:33], v[206:213], v[42:45], v187, v188 op_sel_hi:[0,0,0]
	v_mfma_scale_f32_16x16x128_f8f6f4 v[38:41], v[18:25], v[220:227], v[38:41], v187, v188 op_sel_hi:[0,0,0]
	v_mfma_scale_f32_16x16x128_f8f6f4 v[34:37], v[26:33], v[220:227], v[34:37], v187, v188 op_sel_hi:[0,0,0]
	s_barrier
	s_setprio 0
	s_add_i32 s94, s94, 2
	s_add_u32 s92, s92, 0x10000
	s_addc_u32 s93, s93, 0
	s_add_u32 s70, s70, 0x100
	s_addc_u32 s71, s71, 0
	s_cmp_gt_u32 s94, 13
	s_cbranch_scc0 .LBB0_285
	s_and_b64 vcc, exec, s[40:41]
	s_cbranch_vccz .LBB0_288
	s_barrier
	s_setprio 3

.LBB0_659:
	s_ashr_i32 s45, s44, 31
	s_lshl_b64 s[26:27], s[44:45], 20
	v_readlane_b32 s50, v254, 58
	v_readlane_b32 s51, v254, 59
	s_add_u32 s50, s50, s26
	s_addc_u32 s51, s51, s27
	s_and_b64 s[26:27], s[0:1], exec
	s_cselect_b32 s45, s51, s61
	s_cselect_b32 s72, s50, s60
	s_ashr_i32 s41, s40, 31
	s_lshl_b64 s[26:27], s[40:41], 20
	s_add_u32 s54, s3, s26
	s_addc_u32 s55, s33, s27
	s_and_b64 s[26:27], s[0:1], exec
	s_cselect_b32 s41, s55, s59
	s_cselect_b32 s73, s54, s58
	s_add_u32 s74, s58, 0x10000
	s_addc_u32 s75, s59, 0
	s_add_u32 s58, s60, 0x80080
	s_addc_u32 s59, s61, 0
	s_mov_b32 s80, -2
	ds_read_b128 v[130:133], v222
	ds_read_b128 v[134:137], v222 offset:1024
	ds_read_b128 v[138:141], v222 offset:2048
	ds_read_b128 v[142:145], v222 offset:3072
	ds_read_b128 v[146:149], v223
	ds_read_b128 v[150:153], v223 offset:1024
	ds_read_b128 v[154:157], v223 offset:2048
	ds_read_b128 v[158:161], v223 offset:3072
	s_add_u32 s26, s58, 0xfff80080
	s_addc_u32 s27, s59, -1
	s_cmp_eq_u32 s80, 28
	s_cselect_b32 s61, s45, s27
	s_cselect_b32 s60, s72, s26
	s_cselect_b32 s27, s41, s75
	s_cselect_b32 s26, s73, s74
	v_lshl_add_u64 v[208:209], s[58:59], 0, v[200:201]
	s_add_i32 m0, s57, 0xc000
	ds_read_b128 v[162:165], v224
	ds_read_b128 v[166:169], v224 offset:1024
	ds_read_b128 v[170:173], v224 offset:2048
	ds_read_b128 v[174:177], v224 offset:3072
	ds_read_b128 v[178:181], v224 offset:4096
	ds_read_b128 v[182:185], v224 offset:5120
	ds_read_b128 v[186:189], v224 offset:6144
	ds_read_b128 v[190:193], v224 offset:7168
	global_load_lds_dwordx4 v[208:209], off
	v_lshl_add_u64 v[208:209], s[58:59], 0, v[202:203]
	s_add_i32 m0, s57, 0xe000
	s_nop 0
	global_load_lds_dwordx4 v[208:209], off
	s_setprio 1
	s_waitcnt vmcnt(8)
	s_waitcnt lgkmcnt(0)
	s_barrier
	v_mfma_f32_16x16x32_bf16 v[126:129], v[130:133], v[162:165], 0
	v_mfma_f32_16x16x32_bf16 v[122:125], v[138:141], v[162:165], 0
	v_mfma_f32_16x16x32_bf16 v[118:121], v[130:133], v[170:173], 0
	v_mfma_f32_16x16x32_bf16 v[114:117], v[138:141], v[170:173], 0
	v_mfma_f32_16x16x32_bf16 v[110:113], v[130:133], v[178:181], 0
	v_mfma_f32_16x16x32_bf16 v[102:105], v[138:141], v[178:181], 0
	v_mfma_f32_16x16x32_bf16 v[94:97], v[130:133], v[186:189], 0
	v_mfma_f32_16x16x32_bf16 v[74:77], v[138:141], v[186:189], 0
	v_mfma_f32_16x16x32_bf16 v[126:129], v[134:137], v[166:169], v[126:129]
	v_mfma_f32_16x16x32_bf16 v[122:125], v[142:145], v[166:169], v[122:125]
	v_mfma_f32_16x16x32_bf16 v[118:121], v[134:137], v[174:177], v[118:121]
	v_mfma_f32_16x16x32_bf16 v[114:117], v[142:145], v[174:177], v[114:117]
	v_mfma_f32_16x16x32_bf16 v[110:113], v[134:137], v[182:185], v[110:113]
	v_mfma_f32_16x16x32_bf16 v[102:105], v[142:145], v[182:185], v[102:105]
	v_mfma_f32_16x16x32_bf16 v[94:97], v[134:137], v[190:193], v[94:97]
	v_mfma_f32_16x16x32_bf16 v[74:77], v[142:145], v[190:193], v[74:77]
	v_mfma_f32_16x16x32_bf16 v[106:109], v[146:149], v[162:165], 0
	v_mfma_f32_16x16x32_bf16 v[98:101], v[154:157], v[162:165], 0
	v_mfma_f32_16x16x32_bf16 v[90:93], v[146:149], v[170:173], 0
	v_mfma_f32_16x16x32_bf16 v[86:89], v[154:157], v[170:173], 0
	v_mfma_f32_16x16x32_bf16 v[82:85], v[146:149], v[178:181], 0
	v_mfma_f32_16x16x32_bf16 v[78:81], v[154:157], v[178:181], 0
	v_mfma_f32_16x16x32_bf16 v[70:73], v[146:149], v[186:189], 0
	v_mfma_f32_16x16x32_bf16 v[66:69], v[154:157], v[186:189], 0
	v_mfma_f32_16x16x32_bf16 v[106:109], v[150:153], v[166:169], v[106:109]
	v_mfma_f32_16x16x32_bf16 v[98:101], v[158:161], v[166:169], v[98:101]
	v_mfma_f32_16x16x32_bf16 v[90:93], v[150:153], v[174:177], v[90:93]
	v_mfma_f32_16x16x32_bf16 v[86:89], v[158:161], v[174:177], v[86:89]
	v_mfma_f32_16x16x32_bf16 v[82:85], v[150:153], v[182:185], v[82:85]
	v_mfma_f32_16x16x32_bf16 v[78:81], v[158:161], v[182:185], v[78:81]
	v_mfma_f32_16x16x32_bf16 v[70:73], v[150:153], v[190:193], v[70:73]
	v_mfma_f32_16x16x32_bf16 v[66:69], v[158:161], v[190:193], v[66:69]
	s_barrier
	s_setprio 0
	v_lshl_add_u64 v[208:209], s[26:27], 0, v[194:195]
	s_add_i32 s26, s70, s35
	s_mov_b32 m0, s26
	ds_read_b128 v[162:165], v224 offset:16384
	ds_read_b128 v[166:169], v224 offset:17408
	ds_read_b128 v[170:173], v224 offset:18432
	ds_read_b128 v[174:177], v224 offset:19456
	ds_read_b128 v[178:181], v224 offset:20480
	ds_read_b128 v[182:185], v224 offset:21504
	ds_read_b128 v[186:189], v224 offset:22528
	ds_read_b128 v[190:193], v224 offset:23552
	global_load_lds_dwordx4 v[208:209], off
	v_lshl_add_u64 v[210:211], v[208:209], 0, s[6:7]
	s_add_i32 m0, s26, 0x2000
	s_add_i32 s26, s71, s35
	global_load_lds_dwordx4 v[210:211], off
	v_lshl_add_u64 v[210:211], v[208:209], 0, s[8:9]
	s_mov_b32 m0, s26
	v_lshl_add_u64 v[212:213], s[60:61], 0, v[198:199]
	global_load_lds_dwordx4 v[210:211], off
	v_lshl_add_u64 v[210:211], v[208:209], 0, s[10:11]
	s_add_i32 m0, s26, 0x2000
	s_nop 0
	global_load_lds_dwordx4 v[210:211], off
	v_lshl_add_u64 v[210:211], s[60:61], 0, v[196:197]
	s_mov_b32 m0, s57
	s_nop 0
	global_load_lds_dwordx4 v[210:211], off
	s_mov_b32 m0, s63
	s_nop 0
	global_load_lds_dwordx4 v[212:213], off
	s_setprio 1
	s_waitcnt vmcnt(8)
	s_waitcnt lgkmcnt(0)
	s_barrier
	v_mfma_f32_16x16x32_bf16 v[62:65], v[130:133], v[162:165], 0
	v_mfma_f32_16x16x32_bf16 v[58:61], v[138:141], v[162:165], 0
	v_mfma_f32_16x16x32_bf16 v[54:57], v[130:133], v[170:173], 0
	v_mfma_f32_16x16x32_bf16 v[50:53], v[138:141], v[170:173], 0
	v_mfma_f32_16x16x32_bf16 v[46:49], v[130:133], v[178:181], 0
	v_mfma_f32_16x16x32_bf16 v[38:41], v[138:141], v[178:181], 0
	v_mfma_f32_16x16x32_bf16 v[30:33], v[130:133], v[186:189], 0
	v_mfma_f32_16x16x32_bf16 v[10:13], v[138:141], v[186:189], 0
	v_mfma_f32_16x16x32_bf16 v[62:65], v[134:137], v[166:169], v[62:65]
	v_mfma_f32_16x16x32_bf16 v[58:61], v[142:145], v[166:169], v[58:61]
	v_mfma_f32_16x16x32_bf16 v[54:57], v[134:137], v[174:177], v[54:57]
	v_mfma_f32_16x16x32_bf16 v[50:53], v[142:145], v[174:177], v[50:53]
	v_mfma_f32_16x16x32_bf16 v[46:49], v[134:137], v[182:185], v[46:49]
	v_mfma_f32_16x16x32_bf16 v[38:41], v[142:145], v[182:185], v[38:41]
	v_mfma_f32_16x16x32_bf16 v[30:33], v[134:137], v[190:193], v[30:33]
	v_mfma_f32_16x16x32_bf16 v[10:13], v[142:145], v[190:193], v[10:13]
	v_mfma_f32_16x16x32_bf16 v[42:45], v[146:149], v[162:165], 0
	v_mfma_f32_16x16x32_bf16 v[34:37], v[154:157], v[162:165], 0
	v_mfma_f32_16x16x32_bf16 v[26:29], v[146:149], v[170:173], 0
	v_mfma_f32_16x16x32_bf16 v[22:25], v[154:157], v[170:173], 0
	v_mfma_f32_16x16x32_bf16 v[18:21], v[146:149], v[178:181], 0
	v_mfma_f32_16x16x32_bf16 v[14:17], v[154:157], v[178:181], 0
	v_mfma_f32_16x16x32_bf16 v[6:9], v[146:149], v[186:189], 0
	v_mfma_f32_16x16x32_bf16 v[2:5], v[154:157], v[186:189], 0
	v_mfma_f32_16x16x32_bf16 v[42:45], v[150:153], v[166:169], v[42:45]
	v_mfma_f32_16x16x32_bf16 v[34:37], v[158:161], v[166:169], v[34:37]
	v_mfma_f32_16x16x32_bf16 v[26:29], v[150:153], v[174:177], v[26:29]
	v_mfma_f32_16x16x32_bf16 v[22:25], v[158:161], v[174:177], v[22:25]
	v_mfma_f32_16x16x32_bf16 v[18:21], v[150:153], v[182:185], v[18:21]
	v_mfma_f32_16x16x32_bf16 v[14:17], v[158:161], v[182:185], v[14:17]
	v_mfma_f32_16x16x32_bf16 v[6:9], v[150:153], v[190:193], v[6:9]
	v_mfma_f32_16x16x32_bf16 v[2:5], v[158:161], v[190:193], v[2:5]
	s_barrier
	s_setprio 0
	s_add_i32 s81, 0, 0x18000
	s_add_i32 s82, 0, 0x1c000
	v_add_u32_e32 v142, s81, v220
	v_add_u32_e32 v158, s82, v220
	ds_read_b128 v[130:133], v142
	ds_read_b128 v[134:137], v142 offset:1024
	ds_read_b128 v[138:141], v142 offset:2048
	ds_read_b128 v[142:145], v142 offset:3072
	ds_read_b128 v[146:149], v158
	ds_read_b128 v[150:153], v158 offset:1024
	ds_read_b128 v[154:157], v158 offset:2048
	ds_read_b128 v[158:161], v158 offset:3072
	s_add_u32 s26, s60, 0x80000
	s_addc_u32 s27, s61, 0
	s_mov_b32 m0, s64
	v_lshl_add_u64 v[214:215], s[26:27], 0, v[196:197]
	ds_read_b128 v[162:165], v224 offset:32768
	ds_read_b128 v[166:169], v224 offset:33792
	ds_read_b128 v[170:173], v224 offset:34816
	ds_read_b128 v[174:177], v224 offset:35840
	ds_read_b128 v[178:181], v224 offset:36864
	ds_read_b128 v[182:185], v224 offset:37888
	ds_read_b128 v[186:189], v224 offset:38912
	ds_read_b128 v[190:193], v224 offset:39936
	global_load_lds_dwordx4 v[214:215], off
	v_lshl_add_u64 v[214:215], s[26:27], 0, v[198:199]
	s_mov_b32 m0, s65
	s_nop 0
	global_load_lds_dwordx4 v[214:215], off
	s_setprio 1
	s_waitcnt vmcnt(8)
	s_waitcnt lgkmcnt(0)
	s_barrier
	v_mfma_f32_16x16x32_bf16 v[126:129], v[130:133], v[162:165], v[126:129]
	v_mfma_f32_16x16x32_bf16 v[122:125], v[138:141], v[162:165], v[122:125]
	v_mfma_f32_16x16x32_bf16 v[118:121], v[130:133], v[170:173], v[118:121]
	v_mfma_f32_16x16x32_bf16 v[114:117], v[138:141], v[170:173], v[114:117]
	v_mfma_f32_16x16x32_bf16 v[110:113], v[130:133], v[178:181], v[110:113]
	v_mfma_f32_16x16x32_bf16 v[102:105], v[138:141], v[178:181], v[102:105]
	v_mfma_f32_16x16x32_bf16 v[94:97], v[130:133], v[186:189], v[94:97]
	v_mfma_f32_16x16x32_bf16 v[74:77], v[138:141], v[186:189], v[74:77]
	v_mfma_f32_16x16x32_bf16 v[126:129], v[134:137], v[166:169], v[126:129]
	v_mfma_f32_16x16x32_bf16 v[122:125], v[142:145], v[166:169], v[122:125]
	v_mfma_f32_16x16x32_bf16 v[118:121], v[134:137], v[174:177], v[118:121]
	v_mfma_f32_16x16x32_bf16 v[114:117], v[142:145], v[174:177], v[114:117]
	v_mfma_f32_16x16x32_bf16 v[110:113], v[134:137], v[182:185], v[110:113]
	v_mfma_f32_16x16x32_bf16 v[102:105], v[142:145], v[182:185], v[102:105]
	v_mfma_f32_16x16x32_bf16 v[94:97], v[134:137], v[190:193], v[94:97]
	v_mfma_f32_16x16x32_bf16 v[74:77], v[142:145], v[190:193], v[74:77]
	v_mfma_f32_16x16x32_bf16 v[106:109], v[146:149], v[162:165], v[106:109]
	v_mfma_f32_16x16x32_bf16 v[98:101], v[154:157], v[162:165], v[98:101]
	v_mfma_f32_16x16x32_bf16 v[90:93], v[146:149], v[170:173], v[90:93]
	v_mfma_f32_16x16x32_bf16 v[86:89], v[154:157], v[170:173], v[86:89]
	v_mfma_f32_16x16x32_bf16 v[82:85], v[146:149], v[178:181], v[82:85]
	v_mfma_f32_16x16x32_bf16 v[78:81], v[154:157], v[178:181], v[78:81]
	v_mfma_f32_16x16x32_bf16 v[70:73], v[146:149], v[186:189], v[70:73]
	v_mfma_f32_16x16x32_bf16 v[66:69], v[154:157], v[186:189], v[66:69]
	v_mfma_f32_16x16x32_bf16 v[106:109], v[150:153], v[166:169], v[106:109]
	v_mfma_f32_16x16x32_bf16 v[98:101], v[158:161], v[166:169], v[98:101]
	v_mfma_f32_16x16x32_bf16 v[90:93], v[150:153], v[174:177], v[90:93]
	v_mfma_f32_16x16x32_bf16 v[86:89], v[158:161], v[174:177], v[86:89]
	v_mfma_f32_16x16x32_bf16 v[82:85], v[150:153], v[182:185], v[82:85]
	v_mfma_f32_16x16x32_bf16 v[78:81], v[158:161], v[182:185], v[78:81]
	v_mfma_f32_16x16x32_bf16 v[70:73], v[150:153], v[190:193], v[70:73]
	v_mfma_f32_16x16x32_bf16 v[66:69], v[158:161], v[190:193], v[66:69]
	s_barrier
	s_setprio 0
	s_add_i32 s26, s81, s35
	v_lshl_add_u64 v[214:215], v[208:209], 0, s[14:15]
	s_mov_b32 m0, s26
	ds_read_b128 v[162:165], v224 offset:49152
	ds_read_b128 v[166:169], v224 offset:50176
	ds_read_b128 v[170:173], v224 offset:51200
	ds_read_b128 v[174:177], v224 offset:52224
	ds_read_b128 v[178:181], v224 offset:53248
	ds_read_b128 v[182:185], v224 offset:54272
	ds_read_b128 v[186:189], v224 offset:55296
	ds_read_b128 v[190:193], v224 offset:56320
	global_load_lds_dwordx4 v[214:215], off
	v_lshl_add_u64 v[214:215], v[208:209], 0, s[16:17]
	s_add_i32 m0, s26, 0x2000
	s_add_i32 s26, s82, s35
	global_load_lds_dwordx4 v[214:215], off
	v_lshl_add_u64 v[214:215], v[208:209], 0, s[20:21]
	s_mov_b32 m0, s26
	v_lshl_add_u64 v[208:209], v[208:209], 0, s[22:23]
	global_load_lds_dwordx4 v[214:215], off
	s_add_i32 m0, s26, 0x2000
	s_nop 0
	global_load_lds_dwordx4 v[208:209], off
	v_lshl_add_u64 v[208:209], v[210:211], 0, s[18:19]
	s_mov_b32 m0, s67
	s_nop 0
	global_load_lds_dwordx4 v[208:209], off
	v_lshl_add_u64 v[208:209], v[212:213], 0, s[18:19]
	s_mov_b32 m0, s68
	s_nop 0
	global_load_lds_dwordx4 v[208:209], off
	s_setprio 1
	s_waitcnt vmcnt(8)
	s_waitcnt lgkmcnt(0)
	s_barrier
	v_mfma_f32_16x16x32_bf16 v[62:65], v[130:133], v[162:165], v[62:65]
	v_mfma_f32_16x16x32_bf16 v[58:61], v[138:141], v[162:165], v[58:61]
	v_mfma_f32_16x16x32_bf16 v[54:57], v[130:133], v[170:173], v[54:57]
	v_mfma_f32_16x16x32_bf16 v[50:53], v[138:141], v[170:173], v[50:53]
	v_mfma_f32_16x16x32_bf16 v[46:49], v[130:133], v[178:181], v[46:49]
	v_mfma_f32_16x16x32_bf16 v[38:41], v[138:141], v[178:181], v[38:41]
	v_mfma_f32_16x16x32_bf16 v[30:33], v[130:133], v[186:189], v[30:33]
	v_mfma_f32_16x16x32_bf16 v[10:13], v[138:141], v[186:189], v[10:13]
	v_mfma_f32_16x16x32_bf16 v[62:65], v[134:137], v[166:169], v[62:65]
	v_mfma_f32_16x16x32_bf16 v[58:61], v[142:145], v[166:169], v[58:61]
	v_mfma_f32_16x16x32_bf16 v[54:57], v[134:137], v[174:177], v[54:57]
	v_mfma_f32_16x16x32_bf16 v[50:53], v[142:145], v[174:177], v[50:53]
	v_mfma_f32_16x16x32_bf16 v[46:49], v[134:137], v[182:185], v[46:49]
	v_mfma_f32_16x16x32_bf16 v[38:41], v[142:145], v[182:185], v[38:41]
	v_mfma_f32_16x16x32_bf16 v[30:33], v[134:137], v[190:193], v[30:33]
	v_mfma_f32_16x16x32_bf16 v[10:13], v[142:145], v[190:193], v[10:13]
	v_mfma_f32_16x16x32_bf16 v[42:45], v[146:149], v[162:165], v[42:45]
	v_mfma_f32_16x16x32_bf16 v[34:37], v[154:157], v[162:165], v[34:37]
	v_mfma_f32_16x16x32_bf16 v[26:29], v[146:149], v[170:173], v[26:29]
	v_mfma_f32_16x16x32_bf16 v[22:25], v[154:157], v[170:173], v[22:25]
	v_mfma_f32_16x16x32_bf16 v[18:21], v[146:149], v[178:181], v[18:21]
	v_mfma_f32_16x16x32_bf16 v[14:17], v[154:157], v[178:181], v[14:17]
	v_mfma_f32_16x16x32_bf16 v[6:9], v[146:149], v[186:189], v[6:9]
	v_mfma_f32_16x16x32_bf16 v[2:5], v[154:157], v[186:189], v[2:5]
	v_mfma_f32_16x16x32_bf16 v[42:45], v[150:153], v[166:169], v[42:45]
	v_mfma_f32_16x16x32_bf16 v[34:37], v[158:161], v[166:169], v[34:37]
	v_mfma_f32_16x16x32_bf16 v[26:29], v[150:153], v[174:177], v[26:29]
	v_mfma_f32_16x16x32_bf16 v[22:25], v[158:161], v[174:177], v[22:25]
	v_mfma_f32_16x16x32_bf16 v[18:21], v[150:153], v[182:185], v[18:21]
	v_mfma_f32_16x16x32_bf16 v[14:17], v[158:161], v[182:185], v[14:17]
	v_mfma_f32_16x16x32_bf16 v[6:9], v[150:153], v[190:193], v[6:9]
	v_mfma_f32_16x16x32_bf16 v[2:5], v[158:161], v[190:193], v[2:5]
	s_barrier
	s_setprio 0
	s_add_i32 s80, s80, 2
	s_add_u32 s74, s74, 0x10000
	s_addc_u32 s75, s75, 0
	s_add_u32 s58, s58, 0x100
	s_addc_u32 s59, s59, 0
	s_cmp_gt_u32 s80, 29
.LBB0_660:
	ds_read_b128 v[130:133], v222
	ds_read_b128 v[134:137], v222 offset:1024
	ds_read_b128 v[138:141], v222 offset:2048
	ds_read_b128 v[142:145], v222 offset:3072
	ds_read_b128 v[146:149], v223
	ds_read_b128 v[150:153], v223 offset:1024
	ds_read_b128 v[154:157], v223 offset:2048
	ds_read_b128 v[158:161], v223 offset:3072
	s_add_u32 s26, s58, 0xfff80080
	s_addc_u32 s27, s59, -1
	s_cmp_eq_u32 s80, 28
	s_cselect_b32 s61, s45, s27
	s_cselect_b32 s60, s72, s26
	s_cselect_b32 s27, s41, s75
	s_cselect_b32 s26, s73, s74
	v_lshl_add_u64 v[208:209], s[58:59], 0, v[200:201]
	s_add_i32 m0, s57, 0xc000
	ds_read_b128 v[162:165], v224
	ds_read_b128 v[166:169], v224 offset:1024
	ds_read_b128 v[170:173], v224 offset:2048
	ds_read_b128 v[174:177], v224 offset:3072
	ds_read_b128 v[178:181], v224 offset:4096
	ds_read_b128 v[182:185], v224 offset:5120
	ds_read_b128 v[186:189], v224 offset:6144
	ds_read_b128 v[190:193], v224 offset:7168
	global_load_lds_dwordx4 v[208:209], off
	v_lshl_add_u64 v[208:209], s[58:59], 0, v[202:203]
	s_add_i32 m0, s57, 0xe000
	s_nop 0
	global_load_lds_dwordx4 v[208:209], off
	s_setprio 1
	s_waitcnt vmcnt(8)
	s_waitcnt lgkmcnt(0)
	s_barrier
	v_mfma_f32_16x16x32_bf16 v[126:129], v[130:133], v[162:165], v[126:129]
	v_mfma_f32_16x16x32_bf16 v[122:125], v[138:141], v[162:165], v[122:125]
	v_mfma_f32_16x16x32_bf16 v[118:121], v[130:133], v[170:173], v[118:121]
	v_mfma_f32_16x16x32_bf16 v[114:117], v[138:141], v[170:173], v[114:117]
	v_mfma_f32_16x16x32_bf16 v[110:113], v[130:133], v[178:181], v[110:113]
	v_mfma_f32_16x16x32_bf16 v[102:105], v[138:141], v[178:181], v[102:105]
	v_mfma_f32_16x16x32_bf16 v[94:97], v[130:133], v[186:189], v[94:97]
	v_mfma_f32_16x16x32_bf16 v[74:77], v[138:141], v[186:189], v[74:77]
	v_mfma_f32_16x16x32_bf16 v[126:129], v[134:137], v[166:169], v[126:129]
	v_mfma_f32_16x16x32_bf16 v[122:125], v[142:145], v[166:169], v[122:125]
	v_mfma_f32_16x16x32_bf16 v[118:121], v[134:137], v[174:177], v[118:121]
	v_mfma_f32_16x16x32_bf16 v[114:117], v[142:145], v[174:177], v[114:117]
	v_mfma_f32_16x16x32_bf16 v[110:113], v[134:137], v[182:185], v[110:113]
	v_mfma_f32_16x16x32_bf16 v[102:105], v[142:145], v[182:185], v[102:105]
	v_mfma_f32_16x16x32_bf16 v[94:97], v[134:137], v[190:193], v[94:97]
	v_mfma_f32_16x16x32_bf16 v[74:77], v[142:145], v[190:193], v[74:77]
	v_mfma_f32_16x16x32_bf16 v[106:109], v[146:149], v[162:165], v[106:109]
	v_mfma_f32_16x16x32_bf16 v[98:101], v[154:157], v[162:165], v[98:101]
	v_mfma_f32_16x16x32_bf16 v[90:93], v[146:149], v[170:173], v[90:93]
	v_mfma_f32_16x16x32_bf16 v[86:89], v[154:157], v[170:173], v[86:89]
	v_mfma_f32_16x16x32_bf16 v[82:85], v[146:149], v[178:181], v[82:85]
	v_mfma_f32_16x16x32_bf16 v[78:81], v[154:157], v[178:181], v[78:81]
	v_mfma_f32_16x16x32_bf16 v[70:73], v[146:149], v[186:189], v[70:73]
	v_mfma_f32_16x16x32_bf16 v[66:69], v[154:157], v[186:189], v[66:69]
	v_mfma_f32_16x16x32_bf16 v[106:109], v[150:153], v[166:169], v[106:109]
	v_mfma_f32_16x16x32_bf16 v[98:101], v[158:161], v[166:169], v[98:101]
	v_mfma_f32_16x16x32_bf16 v[90:93], v[150:153], v[174:177], v[90:93]
	v_mfma_f32_16x16x32_bf16 v[86:89], v[158:161], v[174:177], v[86:89]
	v_mfma_f32_16x16x32_bf16 v[82:85], v[150:153], v[182:185], v[82:85]
	v_mfma_f32_16x16x32_bf16 v[78:81], v[158:161], v[182:185], v[78:81]
	v_mfma_f32_16x16x32_bf16 v[70:73], v[150:153], v[190:193], v[70:73]
	v_mfma_f32_16x16x32_bf16 v[66:69], v[158:161], v[190:193], v[66:69]
	s_barrier
	s_setprio 0
	v_lshl_add_u64 v[208:209], s[26:27], 0, v[194:195]
	s_add_i32 s26, s70, s35
	s_mov_b32 m0, s26
	ds_read_b128 v[162:165], v224 offset:16384
	ds_read_b128 v[166:169], v224 offset:17408
	ds_read_b128 v[170:173], v224 offset:18432
	ds_read_b128 v[174:177], v224 offset:19456
	ds_read_b128 v[178:181], v224 offset:20480
	ds_read_b128 v[182:185], v224 offset:21504
	ds_read_b128 v[186:189], v224 offset:22528
	ds_read_b128 v[190:193], v224 offset:23552
	global_load_lds_dwordx4 v[208:209], off
	v_lshl_add_u64 v[210:211], v[208:209], 0, s[6:7]
	s_add_i32 m0, s26, 0x2000
	s_add_i32 s26, s71, s35
	global_load_lds_dwordx4 v[210:211], off
	v_lshl_add_u64 v[210:211], v[208:209], 0, s[8:9]
	s_mov_b32 m0, s26
	v_lshl_add_u64 v[212:213], s[60:61], 0, v[198:199]
	global_load_lds_dwordx4 v[210:211], off
	v_lshl_add_u64 v[210:211], v[208:209], 0, s[10:11]
	s_add_i32 m0, s26, 0x2000
	s_nop 0
	global_load_lds_dwordx4 v[210:211], off
	v_lshl_add_u64 v[210:211], s[60:61], 0, v[196:197]
	s_mov_b32 m0, s57
	s_nop 0
	global_load_lds_dwordx4 v[210:211], off
	s_mov_b32 m0, s63
	s_nop 0
	global_load_lds_dwordx4 v[212:213], off
	s_setprio 1
	s_waitcnt vmcnt(8)
	s_waitcnt lgkmcnt(0)
	s_barrier
	v_mfma_f32_16x16x32_bf16 v[62:65], v[130:133], v[162:165], v[62:65]
	v_mfma_f32_16x16x32_bf16 v[58:61], v[138:141], v[162:165], v[58:61]
	v_mfma_f32_16x16x32_bf16 v[54:57], v[130:133], v[170:173], v[54:57]
	v_mfma_f32_16x16x32_bf16 v[50:53], v[138:141], v[170:173], v[50:53]
	v_mfma_f32_16x16x32_bf16 v[46:49], v[130:133], v[178:181], v[46:49]
	v_mfma_f32_16x16x32_bf16 v[38:41], v[138:141], v[178:181], v[38:41]
	v_mfma_f32_16x16x32_bf16 v[30:33], v[130:133], v[186:189], v[30:33]
	v_mfma_f32_16x16x32_bf16 v[10:13], v[138:141], v[186:189], v[10:13]
	v_mfma_f32_16x16x32_bf16 v[62:65], v[134:137], v[166:169], v[62:65]
	v_mfma_f32_16x16x32_bf16 v[58:61], v[142:145], v[166:169], v[58:61]
	v_mfma_f32_16x16x32_bf16 v[54:57], v[134:137], v[174:177], v[54:57]
	v_mfma_f32_16x16x32_bf16 v[50:53], v[142:145], v[174:177], v[50:53]
	v_mfma_f32_16x16x32_bf16 v[46:49], v[134:137], v[182:185], v[46:49]
	v_mfma_f32_16x16x32_bf16 v[38:41], v[142:145], v[182:185], v[38:41]
	v_mfma_f32_16x16x32_bf16 v[30:33], v[134:137], v[190:193], v[30:33]
	v_mfma_f32_16x16x32_bf16 v[10:13], v[142:145], v[190:193], v[10:13]
	v_mfma_f32_16x16x32_bf16 v[42:45], v[146:149], v[162:165], v[42:45]
	v_mfma_f32_16x16x32_bf16 v[34:37], v[154:157], v[162:165], v[34:37]
	v_mfma_f32_16x16x32_bf16 v[26:29], v[146:149], v[170:173], v[26:29]
	v_mfma_f32_16x16x32_bf16 v[22:25], v[154:157], v[170:173], v[22:25]
	v_mfma_f32_16x16x32_bf16 v[18:21], v[146:149], v[178:181], v[18:21]
	v_mfma_f32_16x16x32_bf16 v[14:17], v[154:157], v[178:181], v[14:17]
	v_mfma_f32_16x16x32_bf16 v[6:9], v[146:149], v[186:189], v[6:9]
	v_mfma_f32_16x16x32_bf16 v[2:5], v[154:157], v[186:189], v[2:5]
	v_mfma_f32_16x16x32_bf16 v[42:45], v[150:153], v[166:169], v[42:45]
	v_mfma_f32_16x16x32_bf16 v[34:37], v[158:161], v[166:169], v[34:37]
	v_mfma_f32_16x16x32_bf16 v[26:29], v[150:153], v[174:177], v[26:29]
	v_mfma_f32_16x16x32_bf16 v[22:25], v[158:161], v[174:177], v[22:25]
	v_mfma_f32_16x16x32_bf16 v[18:21], v[150:153], v[182:185], v[18:21]
	v_mfma_f32_16x16x32_bf16 v[14:17], v[158:161], v[182:185], v[14:17]
	v_mfma_f32_16x16x32_bf16 v[6:9], v[150:153], v[190:193], v[6:9]
	v_mfma_f32_16x16x32_bf16 v[2:5], v[158:161], v[190:193], v[2:5]
	s_barrier
	s_setprio 0
	s_add_i32 s81, 0, 0x18000
	s_add_i32 s82, 0, 0x1c000
	v_add_u32_e32 v142, s81, v220
	v_add_u32_e32 v158, s82, v220
	ds_read_b128 v[130:133], v142
	ds_read_b128 v[134:137], v142 offset:1024
	ds_read_b128 v[138:141], v142 offset:2048
	ds_read_b128 v[142:145], v142 offset:3072
	ds_read_b128 v[146:149], v158
	ds_read_b128 v[150:153], v158 offset:1024
	ds_read_b128 v[154:157], v158 offset:2048
	ds_read_b128 v[158:161], v158 offset:3072
	s_add_u32 s26, s60, 0x80000
	s_addc_u32 s27, s61, 0
	s_mov_b32 m0, s64
	v_lshl_add_u64 v[214:215], s[26:27], 0, v[196:197]
	ds_read_b128 v[162:165], v224 offset:32768
	ds_read_b128 v[166:169], v224 offset:33792
	ds_read_b128 v[170:173], v224 offset:34816
	ds_read_b128 v[174:177], v224 offset:35840
	ds_read_b128 v[178:181], v224 offset:36864
	ds_read_b128 v[182:185], v224 offset:37888
	ds_read_b128 v[186:189], v224 offset:38912
	ds_read_b128 v[190:193], v224 offset:39936
	global_load_lds_dwordx4 v[214:215], off
	v_lshl_add_u64 v[214:215], s[26:27], 0, v[198:199]
	s_mov_b32 m0, s65
	s_nop 0
	global_load_lds_dwordx4 v[214:215], off
	s_setprio 1
	s_waitcnt vmcnt(8)
	s_waitcnt lgkmcnt(0)
	s_barrier
	v_mfma_f32_16x16x32_bf16 v[126:129], v[130:133], v[162:165], v[126:129]
	v_mfma_f32_16x16x32_bf16 v[122:125], v[138:141], v[162:165], v[122:125]
	v_mfma_f32_16x16x32_bf16 v[118:121], v[130:133], v[170:173], v[118:121]
	v_mfma_f32_16x16x32_bf16 v[114:117], v[138:141], v[170:173], v[114:117]
	v_mfma_f32_16x16x32_bf16 v[110:113], v[130:133], v[178:181], v[110:113]
	v_mfma_f32_16x16x32_bf16 v[102:105], v[138:141], v[178:181], v[102:105]
	v_mfma_f32_16x16x32_bf16 v[94:97], v[130:133], v[186:189], v[94:97]
	v_mfma_f32_16x16x32_bf16 v[74:77], v[138:141], v[186:189], v[74:77]
	v_mfma_f32_16x16x32_bf16 v[126:129], v[134:137], v[166:169], v[126:129]
	v_mfma_f32_16x16x32_bf16 v[122:125], v[142:145], v[166:169], v[122:125]
	v_mfma_f32_16x16x32_bf16 v[118:121], v[134:137], v[174:177], v[118:121]
	v_mfma_f32_16x16x32_bf16 v[114:117], v[142:145], v[174:177], v[114:117]
	v_mfma_f32_16x16x32_bf16 v[110:113], v[134:137], v[182:185], v[110:113]
	v_mfma_f32_16x16x32_bf16 v[102:105], v[142:145], v[182:185], v[102:105]
	v_mfma_f32_16x16x32_bf16 v[94:97], v[134:137], v[190:193], v[94:97]
	v_mfma_f32_16x16x32_bf16 v[74:77], v[142:145], v[190:193], v[74:77]
	v_mfma_f32_16x16x32_bf16 v[106:109], v[146:149], v[162:165], v[106:109]
	v_mfma_f32_16x16x32_bf16 v[98:101], v[154:157], v[162:165], v[98:101]
	v_mfma_f32_16x16x32_bf16 v[90:93], v[146:149], v[170:173], v[90:93]
	v_mfma_f32_16x16x32_bf16 v[86:89], v[154:157], v[170:173], v[86:89]
	v_mfma_f32_16x16x32_bf16 v[82:85], v[146:149], v[178:181], v[82:85]
	v_mfma_f32_16x16x32_bf16 v[78:81], v[154:157], v[178:181], v[78:81]
	v_mfma_f32_16x16x32_bf16 v[70:73], v[146:149], v[186:189], v[70:73]
	v_mfma_f32_16x16x32_bf16 v[66:69], v[154:157], v[186:189], v[66:69]
	v_mfma_f32_16x16x32_bf16 v[106:109], v[150:153], v[166:169], v[106:109]
	v_mfma_f32_16x16x32_bf16 v[98:101], v[158:161], v[166:169], v[98:101]
	v_mfma_f32_16x16x32_bf16 v[90:93], v[150:153], v[174:177], v[90:93]
	v_mfma_f32_16x16x32_bf16 v[86:89], v[158:161], v[174:177], v[86:89]
	v_mfma_f32_16x16x32_bf16 v[82:85], v[150:153], v[182:185], v[82:85]
	v_mfma_f32_16x16x32_bf16 v[78:81], v[158:161], v[182:185], v[78:81]
	v_mfma_f32_16x16x32_bf16 v[70:73], v[150:153], v[190:193], v[70:73]
	v_mfma_f32_16x16x32_bf16 v[66:69], v[158:161], v[190:193], v[66:69]
	s_barrier
	s_setprio 0
	s_add_i32 s26, s81, s35
	v_lshl_add_u64 v[214:215], v[208:209], 0, s[14:15]
	s_mov_b32 m0, s26
	ds_read_b128 v[162:165], v224 offset:49152
	ds_read_b128 v[166:169], v224 offset:50176
	ds_read_b128 v[170:173], v224 offset:51200
	ds_read_b128 v[174:177], v224 offset:52224
	ds_read_b128 v[178:181], v224 offset:53248
	ds_read_b128 v[182:185], v224 offset:54272
	ds_read_b128 v[186:189], v224 offset:55296
	ds_read_b128 v[190:193], v224 offset:56320
	global_load_lds_dwordx4 v[214:215], off
	v_lshl_add_u64 v[214:215], v[208:209], 0, s[16:17]
	s_add_i32 m0, s26, 0x2000
	s_add_i32 s26, s82, s35
	global_load_lds_dwordx4 v[214:215], off
	v_lshl_add_u64 v[214:215], v[208:209], 0, s[20:21]
	s_mov_b32 m0, s26
	v_lshl_add_u64 v[208:209], v[208:209], 0, s[22:23]
	global_load_lds_dwordx4 v[214:215], off
	s_add_i32 m0, s26, 0x2000
	s_nop 0
	global_load_lds_dwordx4 v[208:209], off
	v_lshl_add_u64 v[208:209], v[210:211], 0, s[18:19]
	s_mov_b32 m0, s67
	s_nop 0
	global_load_lds_dwordx4 v[208:209], off
	v_lshl_add_u64 v[208:209], v[212:213], 0, s[18:19]
	s_mov_b32 m0, s68
	s_nop 0
	global_load_lds_dwordx4 v[208:209], off
	s_setprio 1
	s_waitcnt vmcnt(8)
	s_waitcnt lgkmcnt(0)
	s_barrier
	v_mfma_f32_16x16x32_bf16 v[62:65], v[130:133], v[162:165], v[62:65]
	v_mfma_f32_16x16x32_bf16 v[58:61], v[138:141], v[162:165], v[58:61]
	v_mfma_f32_16x16x32_bf16 v[54:57], v[130:133], v[170:173], v[54:57]
	v_mfma_f32_16x16x32_bf16 v[50:53], v[138:141], v[170:173], v[50:53]
	v_mfma_f32_16x16x32_bf16 v[46:49], v[130:133], v[178:181], v[46:49]
	v_mfma_f32_16x16x32_bf16 v[38:41], v[138:141], v[178:181], v[38:41]
	v_mfma_f32_16x16x32_bf16 v[30:33], v[130:133], v[186:189], v[30:33]
	v_mfma_f32_16x16x32_bf16 v[10:13], v[138:141], v[186:189], v[10:13]
	v_mfma_f32_16x16x32_bf16 v[62:65], v[134:137], v[166:169], v[62:65]
	v_mfma_f32_16x16x32_bf16 v[58:61], v[142:145], v[166:169], v[58:61]
	v_mfma_f32_16x16x32_bf16 v[54:57], v[134:137], v[174:177], v[54:57]
	v_mfma_f32_16x16x32_bf16 v[50:53], v[142:145], v[174:177], v[50:53]
	v_mfma_f32_16x16x32_bf16 v[46:49], v[134:137], v[182:185], v[46:49]
	v_mfma_f32_16x16x32_bf16 v[38:41], v[142:145], v[182:185], v[38:41]
	v_mfma_f32_16x16x32_bf16 v[30:33], v[134:137], v[190:193], v[30:33]
	v_mfma_f32_16x16x32_bf16 v[10:13], v[142:145], v[190:193], v[10:13]
	v_mfma_f32_16x16x32_bf16 v[42:45], v[146:149], v[162:165], v[42:45]
	v_mfma_f32_16x16x32_bf16 v[34:37], v[154:157], v[162:165], v[34:37]
	v_mfma_f32_16x16x32_bf16 v[26:29], v[146:149], v[170:173], v[26:29]
	v_mfma_f32_16x16x32_bf16 v[22:25], v[154:157], v[170:173], v[22:25]
	v_mfma_f32_16x16x32_bf16 v[18:21], v[146:149], v[178:181], v[18:21]
	v_mfma_f32_16x16x32_bf16 v[14:17], v[154:157], v[178:181], v[14:17]
	v_mfma_f32_16x16x32_bf16 v[6:9], v[146:149], v[186:189], v[6:9]
	v_mfma_f32_16x16x32_bf16 v[2:5], v[154:157], v[186:189], v[2:5]
	v_mfma_f32_16x16x32_bf16 v[42:45], v[150:153], v[166:169], v[42:45]
	v_mfma_f32_16x16x32_bf16 v[34:37], v[158:161], v[166:169], v[34:37]
	v_mfma_f32_16x16x32_bf16 v[26:29], v[150:153], v[174:177], v[26:29]
	v_mfma_f32_16x16x32_bf16 v[22:25], v[158:161], v[174:177], v[22:25]
	v_mfma_f32_16x16x32_bf16 v[18:21], v[150:153], v[182:185], v[18:21]
	v_mfma_f32_16x16x32_bf16 v[14:17], v[158:161], v[182:185], v[14:17]
	v_mfma_f32_16x16x32_bf16 v[6:9], v[150:153], v[190:193], v[6:9]
	v_mfma_f32_16x16x32_bf16 v[2:5], v[158:161], v[190:193], v[2:5]
	s_barrier
	s_setprio 0
	s_add_i32 s80, s80, 2
	s_add_u32 s74, s74, 0x10000
	s_addc_u32 s75, s75, 0
	s_add_u32 s58, s58, 0x100
	s_addc_u32 s59, s59, 0
	s_cmp_gt_u32 s80, 29
	s_cbranch_scc0 .LBB0_660
	s_and_b64 vcc, exec, s[24:25]
	s_cbranch_vccz .LBB0_663
	s_barrier
	s_setprio 3

.LBB0_782:
	s_ashr_i32 s55, s54, 31
	s_lshl_b64 s[26:27], s[54:55], 20
	v_readlane_b32 s56, v254, 56
	v_readlane_b32 s57, v254, 57
	s_add_u32 s56, s56, s26
	s_addc_u32 s57, s57, s27
	s_and_b64 s[26:27], s[0:1], exec
	s_cselect_b32 s55, s57, s65
	s_cselect_b32 s81, s56, s64
	s_ashr_i32 s53, s52, 31
	s_lshl_b64 s[26:27], s[52:53], 20
	s_add_u32 s58, s3, s26
	s_addc_u32 s59, s33, s27
	s_and_b64 s[26:27], s[0:1], exec
	s_cselect_b32 s53, s59, s63
	s_cselect_b32 s82, s58, s62
	s_add_u32 s83, s62, 0x10000
	s_addc_u32 s84, s63, 0
	s_add_u32 s62, s64, 0x80080
	s_addc_u32 s63, s65, 0
	s_mov_b32 s85, -2
	ds_read_b128 v[144:147], v151
	ds_read_b128 v[156:159], v151 offset:1024
	ds_read_b128 v[160:163], v151 offset:2048
	ds_read_b128 v[164:167], v151 offset:3072
	ds_read_b128 v[168:171], v152
	ds_read_b128 v[172:175], v152 offset:1024
	ds_read_b128 v[176:179], v152 offset:2048
	ds_read_b128 v[180:183], v152 offset:3072
	s_add_u32 s26, s62, 0xfff80080
	s_addc_u32 s27, s63, -1
	s_cmp_eq_u32 s85, 28
	s_cselect_b32 s65, s55, s27
	s_cselect_b32 s64, s81, s26
	s_cselect_b32 s27, s53, s84
	s_cselect_b32 s26, s82, s83
	v_lshl_add_u64 v[216:217], s[62:63], 0, v[136:137]
	s_add_i32 m0, s61, 0xc000
	ds_read_b128 v[184:187], v153
	ds_read_b128 v[188:191], v153 offset:1024
	ds_read_b128 v[192:195], v153 offset:2048
	ds_read_b128 v[196:199], v153 offset:3072
	ds_read_b128 v[200:203], v153 offset:4096
	ds_read_b128 v[204:207], v153 offset:5120
	ds_read_b128 v[208:211], v153 offset:6144
	ds_read_b128 v[212:215], v153 offset:7168
	global_load_lds_dwordx4 v[216:217], off
	v_lshl_add_u64 v[216:217], s[62:63], 0, v[138:139]
	s_add_i32 m0, s61, 0xe000
	s_nop 0
	global_load_lds_dwordx4 v[216:217], off
	s_setprio 1
	s_waitcnt vmcnt(16)
	s_waitcnt lgkmcnt(0)
	s_barrier
	v_mfma_f32_16x16x32_bf16 v[126:129], v[144:147], v[184:187], 0
	v_mfma_f32_16x16x32_bf16 v[118:121], v[160:163], v[184:187], 0
	v_mfma_f32_16x16x32_bf16 v[110:113], v[144:147], v[192:195], 0
	v_mfma_f32_16x16x32_bf16 v[102:105], v[160:163], v[192:195], 0
	v_mfma_f32_16x16x32_bf16 v[94:97], v[144:147], v[200:203], 0
	v_mfma_f32_16x16x32_bf16 v[86:89], v[160:163], v[200:203], 0
	v_mfma_f32_16x16x32_bf16 v[78:81], v[144:147], v[208:211], 0
	v_mfma_f32_16x16x32_bf16 v[70:73], v[160:163], v[208:211], 0
	v_mfma_f32_16x16x32_bf16 v[126:129], v[156:159], v[188:191], v[126:129]
	v_mfma_f32_16x16x32_bf16 v[118:121], v[164:167], v[188:191], v[118:121]
	v_mfma_f32_16x16x32_bf16 v[110:113], v[156:159], v[196:199], v[110:113]
	v_mfma_f32_16x16x32_bf16 v[102:105], v[164:167], v[196:199], v[102:105]
	v_mfma_f32_16x16x32_bf16 v[94:97], v[156:159], v[204:207], v[94:97]
	v_mfma_f32_16x16x32_bf16 v[86:89], v[164:167], v[204:207], v[86:89]
	v_mfma_f32_16x16x32_bf16 v[78:81], v[156:159], v[212:215], v[78:81]
	v_mfma_f32_16x16x32_bf16 v[70:73], v[164:167], v[212:215], v[70:73]
	v_mfma_f32_16x16x32_bf16 v[122:125], v[168:171], v[184:187], 0
	v_mfma_f32_16x16x32_bf16 v[114:117], v[176:179], v[184:187], 0
	v_mfma_f32_16x16x32_bf16 v[106:109], v[168:171], v[192:195], 0
	v_mfma_f32_16x16x32_bf16 v[98:101], v[176:179], v[192:195], 0
	v_mfma_f32_16x16x32_bf16 v[90:93], v[168:171], v[200:203], 0
	v_mfma_f32_16x16x32_bf16 v[82:85], v[176:179], v[200:203], 0
	v_mfma_f32_16x16x32_bf16 v[74:77], v[168:171], v[208:211], 0
	v_mfma_f32_16x16x32_bf16 v[66:69], v[176:179], v[208:211], 0
	v_mfma_f32_16x16x32_bf16 v[122:125], v[172:175], v[188:191], v[122:125]
	v_mfma_f32_16x16x32_bf16 v[114:117], v[180:183], v[188:191], v[114:117]
	v_mfma_f32_16x16x32_bf16 v[106:109], v[172:175], v[196:199], v[106:109]
	v_mfma_f32_16x16x32_bf16 v[98:101], v[180:183], v[196:199], v[98:101]
	v_mfma_f32_16x16x32_bf16 v[90:93], v[172:175], v[204:207], v[90:93]
	v_mfma_f32_16x16x32_bf16 v[82:85], v[180:183], v[204:207], v[82:85]
	v_mfma_f32_16x16x32_bf16 v[74:77], v[172:175], v[212:215], v[74:77]
	v_mfma_f32_16x16x32_bf16 v[66:69], v[180:183], v[212:215], v[66:69]
	s_barrier
	s_setprio 0
	v_lshl_add_u64 v[216:217], s[26:27], 0, v[130:131]
	s_add_i32 s26, s73, s35
	s_mov_b32 m0, s26
	ds_read_b128 v[184:187], v153 offset:16384
	ds_read_b128 v[188:191], v153 offset:17408
	ds_read_b128 v[192:195], v153 offset:18432
	ds_read_b128 v[196:199], v153 offset:19456
	ds_read_b128 v[200:203], v153 offset:20480
	ds_read_b128 v[204:207], v153 offset:21504
	ds_read_b128 v[208:211], v153 offset:22528
	ds_read_b128 v[212:215], v153 offset:23552
	global_load_lds_dwordx4 v[216:217], off
	v_lshl_add_u64 v[220:221], v[216:217], 0, s[6:7]
	s_add_i32 m0, s26, 0x2000
	s_add_i32 s26, s74, s35
	global_load_lds_dwordx4 v[220:221], off
	v_lshl_add_u64 v[220:221], v[216:217], 0, s[8:9]
	s_mov_b32 m0, s26
	v_lshl_add_u64 v[222:223], s[64:65], 0, v[134:135]
	global_load_lds_dwordx4 v[220:221], off
	v_lshl_add_u64 v[220:221], v[216:217], 0, s[10:11]
	s_add_i32 m0, s26, 0x2000
	s_nop 0
	global_load_lds_dwordx4 v[220:221], off
	v_lshl_add_u64 v[220:221], s[64:65], 0, v[132:133]
	s_mov_b32 m0, s61
	s_nop 0
	global_load_lds_dwordx4 v[220:221], off
	s_mov_b32 m0, s66
	s_nop 0
	global_load_lds_dwordx4 v[222:223], off
	s_setprio 1
	s_waitcnt vmcnt(16)
	s_waitcnt lgkmcnt(0)
	s_barrier
	v_mfma_f32_16x16x32_bf16 v[62:65], v[144:147], v[184:187], 0
	v_mfma_f32_16x16x32_bf16 v[54:57], v[160:163], v[184:187], 0
	v_mfma_f32_16x16x32_bf16 v[46:49], v[144:147], v[192:195], 0
	v_mfma_f32_16x16x32_bf16 v[38:41], v[160:163], v[192:195], 0
	v_mfma_f32_16x16x32_bf16 v[30:33], v[144:147], v[200:203], 0
	v_mfma_f32_16x16x32_bf16 v[22:25], v[160:163], v[200:203], 0
	v_mfma_f32_16x16x32_bf16 v[14:17], v[144:147], v[208:211], 0
	v_mfma_f32_16x16x32_bf16 v[6:9], v[160:163], v[208:211], 0
	v_mfma_f32_16x16x32_bf16 v[62:65], v[156:159], v[188:191], v[62:65]
	v_mfma_f32_16x16x32_bf16 v[54:57], v[164:167], v[188:191], v[54:57]
	v_mfma_f32_16x16x32_bf16 v[46:49], v[156:159], v[196:199], v[46:49]
	v_mfma_f32_16x16x32_bf16 v[38:41], v[164:167], v[196:199], v[38:41]
	v_mfma_f32_16x16x32_bf16 v[30:33], v[156:159], v[204:207], v[30:33]
	v_mfma_f32_16x16x32_bf16 v[22:25], v[164:167], v[204:207], v[22:25]
	v_mfma_f32_16x16x32_bf16 v[14:17], v[156:159], v[212:215], v[14:17]
	v_mfma_f32_16x16x32_bf16 v[6:9], v[164:167], v[212:215], v[6:9]
	v_mfma_f32_16x16x32_bf16 v[58:61], v[168:171], v[184:187], 0
	v_mfma_f32_16x16x32_bf16 v[50:53], v[176:179], v[184:187], 0
	v_mfma_f32_16x16x32_bf16 v[42:45], v[168:171], v[192:195], 0
	v_mfma_f32_16x16x32_bf16 v[34:37], v[176:179], v[192:195], 0
	v_mfma_f32_16x16x32_bf16 v[26:29], v[168:171], v[200:203], 0
	v_mfma_f32_16x16x32_bf16 v[18:21], v[176:179], v[200:203], 0
	v_mfma_f32_16x16x32_bf16 v[10:13], v[168:171], v[208:211], 0
	v_mfma_f32_16x16x32_bf16 v[2:5], v[176:179], v[208:211], 0
	v_mfma_f32_16x16x32_bf16 v[58:61], v[172:175], v[188:191], v[58:61]
	v_mfma_f32_16x16x32_bf16 v[50:53], v[180:183], v[188:191], v[50:53]
	v_mfma_f32_16x16x32_bf16 v[42:45], v[172:175], v[196:199], v[42:45]
	v_mfma_f32_16x16x32_bf16 v[34:37], v[180:183], v[196:199], v[34:37]
	v_mfma_f32_16x16x32_bf16 v[26:29], v[172:175], v[204:207], v[26:29]
	v_mfma_f32_16x16x32_bf16 v[18:21], v[180:183], v[204:207], v[18:21]
	v_mfma_f32_16x16x32_bf16 v[10:13], v[172:175], v[212:215], v[10:13]
	v_mfma_f32_16x16x32_bf16 v[2:5], v[180:183], v[212:215], v[2:5]
	s_barrier
	s_setprio 0
	s_add_i32 s86, 0, 0x18000
	v_add_u32_e32 v155, s86, v149
	s_add_i32 s87, 0, 0x1c000
	ds_read_b128 v[144:147], v155
	ds_read_b128 v[156:159], v155 offset:1024
	ds_read_b128 v[160:163], v155 offset:2048
	ds_read_b128 v[164:167], v155 offset:3072
	v_add_u32_e32 v155, s87, v149
	ds_read_b128 v[168:171], v155
	ds_read_b128 v[172:175], v155 offset:1024
	ds_read_b128 v[176:179], v155 offset:2048
	ds_read_b128 v[180:183], v155 offset:3072
	s_add_u32 s26, s64, 0x80000
	s_addc_u32 s27, s65, 0
	s_mov_b32 m0, s67
	v_lshl_add_u64 v[224:225], s[26:27], 0, v[132:133]
	ds_read_b128 v[184:187], v153 offset:32768
	ds_read_b128 v[188:191], v153 offset:33792
	ds_read_b128 v[192:195], v153 offset:34816
	ds_read_b128 v[196:199], v153 offset:35840
	ds_read_b128 v[200:203], v153 offset:36864
	ds_read_b128 v[204:207], v153 offset:37888
	ds_read_b128 v[208:211], v153 offset:38912
	ds_read_b128 v[212:215], v153 offset:39936
	global_load_lds_dwordx4 v[224:225], off
	v_lshl_add_u64 v[224:225], s[26:27], 0, v[134:135]
	s_mov_b32 m0, s68
	s_nop 0
	global_load_lds_dwordx4 v[224:225], off
	s_setprio 1
	s_waitcnt vmcnt(8)
	s_waitcnt lgkmcnt(0)
	s_barrier
	v_mfma_f32_16x16x32_bf16 v[126:129], v[144:147], v[184:187], v[126:129]
	v_mfma_f32_16x16x32_bf16 v[118:121], v[160:163], v[184:187], v[118:121]
	v_mfma_f32_16x16x32_bf16 v[110:113], v[144:147], v[192:195], v[110:113]
	v_mfma_f32_16x16x32_bf16 v[102:105], v[160:163], v[192:195], v[102:105]
	v_mfma_f32_16x16x32_bf16 v[94:97], v[144:147], v[200:203], v[94:97]
	v_mfma_f32_16x16x32_bf16 v[86:89], v[160:163], v[200:203], v[86:89]
	v_mfma_f32_16x16x32_bf16 v[78:81], v[144:147], v[208:211], v[78:81]
	v_mfma_f32_16x16x32_bf16 v[70:73], v[160:163], v[208:211], v[70:73]
	v_mfma_f32_16x16x32_bf16 v[126:129], v[156:159], v[188:191], v[126:129]
	v_mfma_f32_16x16x32_bf16 v[118:121], v[164:167], v[188:191], v[118:121]
	v_mfma_f32_16x16x32_bf16 v[110:113], v[156:159], v[196:199], v[110:113]
	v_mfma_f32_16x16x32_bf16 v[102:105], v[164:167], v[196:199], v[102:105]
	v_mfma_f32_16x16x32_bf16 v[94:97], v[156:159], v[204:207], v[94:97]
	v_mfma_f32_16x16x32_bf16 v[86:89], v[164:167], v[204:207], v[86:89]
	v_mfma_f32_16x16x32_bf16 v[78:81], v[156:159], v[212:215], v[78:81]
	v_mfma_f32_16x16x32_bf16 v[70:73], v[164:167], v[212:215], v[70:73]
	v_mfma_f32_16x16x32_bf16 v[122:125], v[168:171], v[184:187], v[122:125]
	v_mfma_f32_16x16x32_bf16 v[114:117], v[176:179], v[184:187], v[114:117]
	v_mfma_f32_16x16x32_bf16 v[106:109], v[168:171], v[192:195], v[106:109]
	v_mfma_f32_16x16x32_bf16 v[98:101], v[176:179], v[192:195], v[98:101]
	v_mfma_f32_16x16x32_bf16 v[90:93], v[168:171], v[200:203], v[90:93]
	v_mfma_f32_16x16x32_bf16 v[82:85], v[176:179], v[200:203], v[82:85]
	v_mfma_f32_16x16x32_bf16 v[74:77], v[168:171], v[208:211], v[74:77]
	v_mfma_f32_16x16x32_bf16 v[66:69], v[176:179], v[208:211], v[66:69]
	v_mfma_f32_16x16x32_bf16 v[122:125], v[172:175], v[188:191], v[122:125]
	v_mfma_f32_16x16x32_bf16 v[114:117], v[180:183], v[188:191], v[114:117]
	v_mfma_f32_16x16x32_bf16 v[106:109], v[172:175], v[196:199], v[106:109]
	v_mfma_f32_16x16x32_bf16 v[98:101], v[180:183], v[196:199], v[98:101]
	v_mfma_f32_16x16x32_bf16 v[90:93], v[172:175], v[204:207], v[90:93]
	v_mfma_f32_16x16x32_bf16 v[82:85], v[180:183], v[204:207], v[82:85]
	v_mfma_f32_16x16x32_bf16 v[74:77], v[172:175], v[212:215], v[74:77]
	v_mfma_f32_16x16x32_bf16 v[66:69], v[180:183], v[212:215], v[66:69]
	s_barrier
	s_setprio 0
	s_add_i32 s26, s86, s35
	v_lshl_add_u64 v[224:225], v[216:217], 0, s[16:17]
	s_mov_b32 m0, s26
	ds_read_b128 v[184:187], v153 offset:49152
	ds_read_b128 v[188:191], v153 offset:50176
	ds_read_b128 v[192:195], v153 offset:51200
	ds_read_b128 v[196:199], v153 offset:52224
	ds_read_b128 v[200:203], v153 offset:53248
	ds_read_b128 v[204:207], v153 offset:54272
	ds_read_b128 v[208:211], v153 offset:55296
	ds_read_b128 v[212:215], v153 offset:56320
	global_load_lds_dwordx4 v[224:225], off
	v_lshl_add_u64 v[224:225], v[216:217], 0, s[18:19]
	s_add_i32 m0, s26, 0x2000
	s_add_i32 s26, s87, s35
	global_load_lds_dwordx4 v[224:225], off
	v_lshl_add_u64 v[224:225], v[216:217], 0, s[22:23]
	s_mov_b32 m0, s26
	v_lshl_add_u64 v[216:217], v[216:217], 0, s[24:25]
	global_load_lds_dwordx4 v[224:225], off
	s_add_i32 m0, s26, 0x2000
	s_nop 0
	global_load_lds_dwordx4 v[216:217], off
	v_lshl_add_u64 v[216:217], v[220:221], 0, s[20:21]
	s_mov_b32 m0, s70
	s_nop 0
	global_load_lds_dwordx4 v[216:217], off
	v_lshl_add_u64 v[216:217], v[222:223], 0, s[20:21]
	s_mov_b32 m0, s71
	s_nop 0
	global_load_lds_dwordx4 v[216:217], off
	s_setprio 1
	s_waitcnt vmcnt(8)
	s_waitcnt lgkmcnt(0)
	s_barrier
	v_mfma_f32_16x16x32_bf16 v[62:65], v[144:147], v[184:187], v[62:65]
	v_mfma_f32_16x16x32_bf16 v[54:57], v[160:163], v[184:187], v[54:57]
	v_mfma_f32_16x16x32_bf16 v[46:49], v[144:147], v[192:195], v[46:49]
	v_mfma_f32_16x16x32_bf16 v[38:41], v[160:163], v[192:195], v[38:41]
	v_mfma_f32_16x16x32_bf16 v[30:33], v[144:147], v[200:203], v[30:33]
	v_mfma_f32_16x16x32_bf16 v[22:25], v[160:163], v[200:203], v[22:25]
	v_mfma_f32_16x16x32_bf16 v[14:17], v[144:147], v[208:211], v[14:17]
	v_mfma_f32_16x16x32_bf16 v[6:9], v[160:163], v[208:211], v[6:9]
	v_mfma_f32_16x16x32_bf16 v[62:65], v[156:159], v[188:191], v[62:65]
	v_mfma_f32_16x16x32_bf16 v[54:57], v[164:167], v[188:191], v[54:57]
	v_mfma_f32_16x16x32_bf16 v[46:49], v[156:159], v[196:199], v[46:49]
	v_mfma_f32_16x16x32_bf16 v[38:41], v[164:167], v[196:199], v[38:41]
	v_mfma_f32_16x16x32_bf16 v[30:33], v[156:159], v[204:207], v[30:33]
	v_mfma_f32_16x16x32_bf16 v[22:25], v[164:167], v[204:207], v[22:25]
	v_mfma_f32_16x16x32_bf16 v[14:17], v[156:159], v[212:215], v[14:17]
	v_mfma_f32_16x16x32_bf16 v[6:9], v[164:167], v[212:215], v[6:9]
	v_mfma_f32_16x16x32_bf16 v[58:61], v[168:171], v[184:187], v[58:61]
	v_mfma_f32_16x16x32_bf16 v[50:53], v[176:179], v[184:187], v[50:53]
	v_mfma_f32_16x16x32_bf16 v[42:45], v[168:171], v[192:195], v[42:45]
	v_mfma_f32_16x16x32_bf16 v[34:37], v[176:179], v[192:195], v[34:37]
	v_mfma_f32_16x16x32_bf16 v[26:29], v[168:171], v[200:203], v[26:29]
	v_mfma_f32_16x16x32_bf16 v[18:21], v[176:179], v[200:203], v[18:21]
	v_mfma_f32_16x16x32_bf16 v[10:13], v[168:171], v[208:211], v[10:13]
	v_mfma_f32_16x16x32_bf16 v[2:5], v[176:179], v[208:211], v[2:5]
	v_mfma_f32_16x16x32_bf16 v[58:61], v[172:175], v[188:191], v[58:61]
	v_mfma_f32_16x16x32_bf16 v[50:53], v[180:183], v[188:191], v[50:53]
	v_mfma_f32_16x16x32_bf16 v[42:45], v[172:175], v[196:199], v[42:45]
	v_mfma_f32_16x16x32_bf16 v[34:37], v[180:183], v[196:199], v[34:37]
	v_mfma_f32_16x16x32_bf16 v[26:29], v[172:175], v[204:207], v[26:29]
	v_mfma_f32_16x16x32_bf16 v[18:21], v[180:183], v[204:207], v[18:21]
	v_mfma_f32_16x16x32_bf16 v[10:13], v[172:175], v[212:215], v[10:13]
	v_mfma_f32_16x16x32_bf16 v[2:5], v[180:183], v[212:215], v[2:5]
	s_barrier
	s_setprio 0
	s_add_i32 s85, s85, 2
	s_add_u32 s83, s83, 0x10000
	s_addc_u32 s84, s84, 0
	s_add_u32 s62, s62, 0x100
	s_addc_u32 s63, s63, 0
	s_cmp_gt_u32 s85, 29
.LBB0_783:
	ds_read_b128 v[144:147], v151
	ds_read_b128 v[156:159], v151 offset:1024
	ds_read_b128 v[160:163], v151 offset:2048
	ds_read_b128 v[164:167], v151 offset:3072
	ds_read_b128 v[168:171], v152
	ds_read_b128 v[172:175], v152 offset:1024
	ds_read_b128 v[176:179], v152 offset:2048
	ds_read_b128 v[180:183], v152 offset:3072
	s_add_u32 s26, s62, 0xfff80080
	s_addc_u32 s27, s63, -1
	s_cmp_eq_u32 s85, 28
	s_cselect_b32 s65, s55, s27
	s_cselect_b32 s64, s81, s26
	s_cselect_b32 s27, s53, s84
	s_cselect_b32 s26, s82, s83
	v_lshl_add_u64 v[216:217], s[62:63], 0, v[136:137]
	s_add_i32 m0, s61, 0xc000
	ds_read_b128 v[184:187], v153
	ds_read_b128 v[188:191], v153 offset:1024
	ds_read_b128 v[192:195], v153 offset:2048
	ds_read_b128 v[196:199], v153 offset:3072
	ds_read_b128 v[200:203], v153 offset:4096
	ds_read_b128 v[204:207], v153 offset:5120
	ds_read_b128 v[208:211], v153 offset:6144
	ds_read_b128 v[212:215], v153 offset:7168
	global_load_lds_dwordx4 v[216:217], off
	v_lshl_add_u64 v[216:217], s[62:63], 0, v[138:139]
	s_add_i32 m0, s61, 0xe000
	s_nop 0
	global_load_lds_dwordx4 v[216:217], off
	s_setprio 1
	s_waitcnt vmcnt(8)
	s_waitcnt lgkmcnt(0)
	s_barrier
	v_mfma_f32_16x16x32_bf16 v[126:129], v[144:147], v[184:187], v[126:129]
	v_mfma_f32_16x16x32_bf16 v[118:121], v[160:163], v[184:187], v[118:121]
	v_mfma_f32_16x16x32_bf16 v[110:113], v[144:147], v[192:195], v[110:113]
	v_mfma_f32_16x16x32_bf16 v[102:105], v[160:163], v[192:195], v[102:105]
	v_mfma_f32_16x16x32_bf16 v[94:97], v[144:147], v[200:203], v[94:97]
	v_mfma_f32_16x16x32_bf16 v[86:89], v[160:163], v[200:203], v[86:89]
	v_mfma_f32_16x16x32_bf16 v[78:81], v[144:147], v[208:211], v[78:81]
	v_mfma_f32_16x16x32_bf16 v[70:73], v[160:163], v[208:211], v[70:73]
	v_mfma_f32_16x16x32_bf16 v[126:129], v[156:159], v[188:191], v[126:129]
	v_mfma_f32_16x16x32_bf16 v[118:121], v[164:167], v[188:191], v[118:121]
	v_mfma_f32_16x16x32_bf16 v[110:113], v[156:159], v[196:199], v[110:113]
	v_mfma_f32_16x16x32_bf16 v[102:105], v[164:167], v[196:199], v[102:105]
	v_mfma_f32_16x16x32_bf16 v[94:97], v[156:159], v[204:207], v[94:97]
	v_mfma_f32_16x16x32_bf16 v[86:89], v[164:167], v[204:207], v[86:89]
	v_mfma_f32_16x16x32_bf16 v[78:81], v[156:159], v[212:215], v[78:81]
	v_mfma_f32_16x16x32_bf16 v[70:73], v[164:167], v[212:215], v[70:73]
	v_mfma_f32_16x16x32_bf16 v[122:125], v[168:171], v[184:187], v[122:125]
	v_mfma_f32_16x16x32_bf16 v[114:117], v[176:179], v[184:187], v[114:117]
	v_mfma_f32_16x16x32_bf16 v[106:109], v[168:171], v[192:195], v[106:109]
	v_mfma_f32_16x16x32_bf16 v[98:101], v[176:179], v[192:195], v[98:101]
	v_mfma_f32_16x16x32_bf16 v[90:93], v[168:171], v[200:203], v[90:93]
	v_mfma_f32_16x16x32_bf16 v[82:85], v[176:179], v[200:203], v[82:85]
	v_mfma_f32_16x16x32_bf16 v[74:77], v[168:171], v[208:211], v[74:77]
	v_mfma_f32_16x16x32_bf16 v[66:69], v[176:179], v[208:211], v[66:69]
	v_mfma_f32_16x16x32_bf16 v[122:125], v[172:175], v[188:191], v[122:125]
	v_mfma_f32_16x16x32_bf16 v[114:117], v[180:183], v[188:191], v[114:117]
	v_mfma_f32_16x16x32_bf16 v[106:109], v[172:175], v[196:199], v[106:109]
	v_mfma_f32_16x16x32_bf16 v[98:101], v[180:183], v[196:199], v[98:101]
	v_mfma_f32_16x16x32_bf16 v[90:93], v[172:175], v[204:207], v[90:93]
	v_mfma_f32_16x16x32_bf16 v[82:85], v[180:183], v[204:207], v[82:85]
	v_mfma_f32_16x16x32_bf16 v[74:77], v[172:175], v[212:215], v[74:77]
	v_mfma_f32_16x16x32_bf16 v[66:69], v[180:183], v[212:215], v[66:69]
	s_barrier
	s_setprio 0
	v_lshl_add_u64 v[216:217], s[26:27], 0, v[130:131]
	s_add_i32 s26, s73, s35
	s_mov_b32 m0, s26
	ds_read_b128 v[184:187], v153 offset:16384
	ds_read_b128 v[188:191], v153 offset:17408
	ds_read_b128 v[192:195], v153 offset:18432
	ds_read_b128 v[196:199], v153 offset:19456
	ds_read_b128 v[200:203], v153 offset:20480
	ds_read_b128 v[204:207], v153 offset:21504
	ds_read_b128 v[208:211], v153 offset:22528
	ds_read_b128 v[212:215], v153 offset:23552
	global_load_lds_dwordx4 v[216:217], off
	v_lshl_add_u64 v[220:221], v[216:217], 0, s[6:7]
	s_add_i32 m0, s26, 0x2000
	s_add_i32 s26, s74, s35
	global_load_lds_dwordx4 v[220:221], off
	v_lshl_add_u64 v[220:221], v[216:217], 0, s[8:9]
	s_mov_b32 m0, s26
	v_lshl_add_u64 v[222:223], s[64:65], 0, v[134:135]
	global_load_lds_dwordx4 v[220:221], off
	v_lshl_add_u64 v[220:221], v[216:217], 0, s[10:11]
	s_add_i32 m0, s26, 0x2000
	s_nop 0
	global_load_lds_dwordx4 v[220:221], off
	v_lshl_add_u64 v[220:221], s[64:65], 0, v[132:133]
	s_mov_b32 m0, s61
	s_nop 0
	global_load_lds_dwordx4 v[220:221], off
	s_mov_b32 m0, s66
	s_nop 0
	global_load_lds_dwordx4 v[222:223], off
	s_setprio 1
	s_waitcnt vmcnt(8)
	s_waitcnt lgkmcnt(0)
	s_barrier
	v_mfma_f32_16x16x32_bf16 v[62:65], v[144:147], v[184:187], v[62:65]
	v_mfma_f32_16x16x32_bf16 v[54:57], v[160:163], v[184:187], v[54:57]
	v_mfma_f32_16x16x32_bf16 v[46:49], v[144:147], v[192:195], v[46:49]
	v_mfma_f32_16x16x32_bf16 v[38:41], v[160:163], v[192:195], v[38:41]
	v_mfma_f32_16x16x32_bf16 v[30:33], v[144:147], v[200:203], v[30:33]
	v_mfma_f32_16x16x32_bf16 v[22:25], v[160:163], v[200:203], v[22:25]
	v_mfma_f32_16x16x32_bf16 v[14:17], v[144:147], v[208:211], v[14:17]
	v_mfma_f32_16x16x32_bf16 v[6:9], v[160:163], v[208:211], v[6:9]
	v_mfma_f32_16x16x32_bf16 v[62:65], v[156:159], v[188:191], v[62:65]
	v_mfma_f32_16x16x32_bf16 v[54:57], v[164:167], v[188:191], v[54:57]
	v_mfma_f32_16x16x32_bf16 v[46:49], v[156:159], v[196:199], v[46:49]
	v_mfma_f32_16x16x32_bf16 v[38:41], v[164:167], v[196:199], v[38:41]
	v_mfma_f32_16x16x32_bf16 v[30:33], v[156:159], v[204:207], v[30:33]
	v_mfma_f32_16x16x32_bf16 v[22:25], v[164:167], v[204:207], v[22:25]
	v_mfma_f32_16x16x32_bf16 v[14:17], v[156:159], v[212:215], v[14:17]
	v_mfma_f32_16x16x32_bf16 v[6:9], v[164:167], v[212:215], v[6:9]
	v_mfma_f32_16x16x32_bf16 v[58:61], v[168:171], v[184:187], v[58:61]
	v_mfma_f32_16x16x32_bf16 v[50:53], v[176:179], v[184:187], v[50:53]
	v_mfma_f32_16x16x32_bf16 v[42:45], v[168:171], v[192:195], v[42:45]
	v_mfma_f32_16x16x32_bf16 v[34:37], v[176:179], v[192:195], v[34:37]
	v_mfma_f32_16x16x32_bf16 v[26:29], v[168:171], v[200:203], v[26:29]
	v_mfma_f32_16x16x32_bf16 v[18:21], v[176:179], v[200:203], v[18:21]
	v_mfma_f32_16x16x32_bf16 v[10:13], v[168:171], v[208:211], v[10:13]
	v_mfma_f32_16x16x32_bf16 v[2:5], v[176:179], v[208:211], v[2:5]
	v_mfma_f32_16x16x32_bf16 v[58:61], v[172:175], v[188:191], v[58:61]
	v_mfma_f32_16x16x32_bf16 v[50:53], v[180:183], v[188:191], v[50:53]
	v_mfma_f32_16x16x32_bf16 v[42:45], v[172:175], v[196:199], v[42:45]
	v_mfma_f32_16x16x32_bf16 v[34:37], v[180:183], v[196:199], v[34:37]
	v_mfma_f32_16x16x32_bf16 v[26:29], v[172:175], v[204:207], v[26:29]
	v_mfma_f32_16x16x32_bf16 v[18:21], v[180:183], v[204:207], v[18:21]
	v_mfma_f32_16x16x32_bf16 v[10:13], v[172:175], v[212:215], v[10:13]
	v_mfma_f32_16x16x32_bf16 v[2:5], v[180:183], v[212:215], v[2:5]
	s_barrier
	s_setprio 0
	s_add_i32 s86, 0, 0x18000
	v_add_u32_e32 v155, s86, v149
	s_add_i32 s87, 0, 0x1c000
	ds_read_b128 v[144:147], v155
	ds_read_b128 v[156:159], v155 offset:1024
	ds_read_b128 v[160:163], v155 offset:2048
	ds_read_b128 v[164:167], v155 offset:3072
	v_add_u32_e32 v155, s87, v149
	ds_read_b128 v[168:171], v155
	ds_read_b128 v[172:175], v155 offset:1024
	ds_read_b128 v[176:179], v155 offset:2048
	ds_read_b128 v[180:183], v155 offset:3072
	s_add_u32 s26, s64, 0x80000
	s_addc_u32 s27, s65, 0
	s_mov_b32 m0, s67
	v_lshl_add_u64 v[224:225], s[26:27], 0, v[132:133]
	ds_read_b128 v[184:187], v153 offset:32768
	ds_read_b128 v[188:191], v153 offset:33792
	ds_read_b128 v[192:195], v153 offset:34816
	ds_read_b128 v[196:199], v153 offset:35840
	ds_read_b128 v[200:203], v153 offset:36864
	ds_read_b128 v[204:207], v153 offset:37888
	ds_read_b128 v[208:211], v153 offset:38912
	ds_read_b128 v[212:215], v153 offset:39936
	global_load_lds_dwordx4 v[224:225], off
	v_lshl_add_u64 v[224:225], s[26:27], 0, v[134:135]
	s_mov_b32 m0, s68
	s_nop 0
	global_load_lds_dwordx4 v[224:225], off
	s_setprio 1
	s_waitcnt vmcnt(8)
	s_waitcnt lgkmcnt(0)
	s_barrier
	v_mfma_f32_16x16x32_bf16 v[126:129], v[144:147], v[184:187], v[126:129]
	v_mfma_f32_16x16x32_bf16 v[118:121], v[160:163], v[184:187], v[118:121]
	v_mfma_f32_16x16x32_bf16 v[110:113], v[144:147], v[192:195], v[110:113]
	v_mfma_f32_16x16x32_bf16 v[102:105], v[160:163], v[192:195], v[102:105]
	v_mfma_f32_16x16x32_bf16 v[94:97], v[144:147], v[200:203], v[94:97]
	v_mfma_f32_16x16x32_bf16 v[86:89], v[160:163], v[200:203], v[86:89]
	v_mfma_f32_16x16x32_bf16 v[78:81], v[144:147], v[208:211], v[78:81]
	v_mfma_f32_16x16x32_bf16 v[70:73], v[160:163], v[208:211], v[70:73]
	v_mfma_f32_16x16x32_bf16 v[126:129], v[156:159], v[188:191], v[126:129]
	v_mfma_f32_16x16x32_bf16 v[118:121], v[164:167], v[188:191], v[118:121]
	v_mfma_f32_16x16x32_bf16 v[110:113], v[156:159], v[196:199], v[110:113]
	v_mfma_f32_16x16x32_bf16 v[102:105], v[164:167], v[196:199], v[102:105]
	v_mfma_f32_16x16x32_bf16 v[94:97], v[156:159], v[204:207], v[94:97]
	v_mfma_f32_16x16x32_bf16 v[86:89], v[164:167], v[204:207], v[86:89]
	v_mfma_f32_16x16x32_bf16 v[78:81], v[156:159], v[212:215], v[78:81]
	v_mfma_f32_16x16x32_bf16 v[70:73], v[164:167], v[212:215], v[70:73]
	v_mfma_f32_16x16x32_bf16 v[122:125], v[168:171], v[184:187], v[122:125]
	v_mfma_f32_16x16x32_bf16 v[114:117], v[176:179], v[184:187], v[114:117]
	v_mfma_f32_16x16x32_bf16 v[106:109], v[168:171], v[192:195], v[106:109]
	v_mfma_f32_16x16x32_bf16 v[98:101], v[176:179], v[192:195], v[98:101]
	v_mfma_f32_16x16x32_bf16 v[90:93], v[168:171], v[200:203], v[90:93]
	v_mfma_f32_16x16x32_bf16 v[82:85], v[176:179], v[200:203], v[82:85]
	v_mfma_f32_16x16x32_bf16 v[74:77], v[168:171], v[208:211], v[74:77]
	v_mfma_f32_16x16x32_bf16 v[66:69], v[176:179], v[208:211], v[66:69]
	v_mfma_f32_16x16x32_bf16 v[122:125], v[172:175], v[188:191], v[122:125]
	v_mfma_f32_16x16x32_bf16 v[114:117], v[180:183], v[188:191], v[114:117]
	v_mfma_f32_16x16x32_bf16 v[106:109], v[172:175], v[196:199], v[106:109]
	v_mfma_f32_16x16x32_bf16 v[98:101], v[180:183], v[196:199], v[98:101]
	v_mfma_f32_16x16x32_bf16 v[90:93], v[172:175], v[204:207], v[90:93]
	v_mfma_f32_16x16x32_bf16 v[82:85], v[180:183], v[204:207], v[82:85]
	v_mfma_f32_16x16x32_bf16 v[74:77], v[172:175], v[212:215], v[74:77]
	v_mfma_f32_16x16x32_bf16 v[66:69], v[180:183], v[212:215], v[66:69]
	s_barrier
	s_setprio 0
	s_add_i32 s26, s86, s35
	v_lshl_add_u64 v[224:225], v[216:217], 0, s[16:17]
	s_mov_b32 m0, s26
	ds_read_b128 v[184:187], v153 offset:49152
	ds_read_b128 v[188:191], v153 offset:50176
	ds_read_b128 v[192:195], v153 offset:51200
	ds_read_b128 v[196:199], v153 offset:52224
	ds_read_b128 v[200:203], v153 offset:53248
	ds_read_b128 v[204:207], v153 offset:54272
	ds_read_b128 v[208:211], v153 offset:55296
	ds_read_b128 v[212:215], v153 offset:56320
	global_load_lds_dwordx4 v[224:225], off
	v_lshl_add_u64 v[224:225], v[216:217], 0, s[18:19]
	s_add_i32 m0, s26, 0x2000
	s_add_i32 s26, s87, s35
	global_load_lds_dwordx4 v[224:225], off
	v_lshl_add_u64 v[224:225], v[216:217], 0, s[22:23]
	s_mov_b32 m0, s26
	v_lshl_add_u64 v[216:217], v[216:217], 0, s[24:25]
	global_load_lds_dwordx4 v[224:225], off
	s_add_i32 m0, s26, 0x2000
	s_nop 0
	global_load_lds_dwordx4 v[216:217], off
	v_lshl_add_u64 v[216:217], v[220:221], 0, s[20:21]
	s_mov_b32 m0, s70
	s_nop 0
	global_load_lds_dwordx4 v[216:217], off
	v_lshl_add_u64 v[216:217], v[222:223], 0, s[20:21]
	s_mov_b32 m0, s71
	s_nop 0
	global_load_lds_dwordx4 v[216:217], off
	s_setprio 1
	s_waitcnt vmcnt(8)
	s_waitcnt lgkmcnt(0)
	s_barrier
	v_mfma_f32_16x16x32_bf16 v[62:65], v[144:147], v[184:187], v[62:65]
	v_mfma_f32_16x16x32_bf16 v[54:57], v[160:163], v[184:187], v[54:57]
	v_mfma_f32_16x16x32_bf16 v[46:49], v[144:147], v[192:195], v[46:49]
	v_mfma_f32_16x16x32_bf16 v[38:41], v[160:163], v[192:195], v[38:41]
	v_mfma_f32_16x16x32_bf16 v[30:33], v[144:147], v[200:203], v[30:33]
	v_mfma_f32_16x16x32_bf16 v[22:25], v[160:163], v[200:203], v[22:25]
	v_mfma_f32_16x16x32_bf16 v[14:17], v[144:147], v[208:211], v[14:17]
	v_mfma_f32_16x16x32_bf16 v[6:9], v[160:163], v[208:211], v[6:9]
	v_mfma_f32_16x16x32_bf16 v[62:65], v[156:159], v[188:191], v[62:65]
	v_mfma_f32_16x16x32_bf16 v[54:57], v[164:167], v[188:191], v[54:57]
	v_mfma_f32_16x16x32_bf16 v[46:49], v[156:159], v[196:199], v[46:49]
	v_mfma_f32_16x16x32_bf16 v[38:41], v[164:167], v[196:199], v[38:41]
	v_mfma_f32_16x16x32_bf16 v[30:33], v[156:159], v[204:207], v[30:33]
	v_mfma_f32_16x16x32_bf16 v[22:25], v[164:167], v[204:207], v[22:25]
	v_mfma_f32_16x16x32_bf16 v[14:17], v[156:159], v[212:215], v[14:17]
	v_mfma_f32_16x16x32_bf16 v[6:9], v[164:167], v[212:215], v[6:9]
	v_mfma_f32_16x16x32_bf16 v[58:61], v[168:171], v[184:187], v[58:61]
	v_mfma_f32_16x16x32_bf16 v[50:53], v[176:179], v[184:187], v[50:53]
	v_mfma_f32_16x16x32_bf16 v[42:45], v[168:171], v[192:195], v[42:45]
	v_mfma_f32_16x16x32_bf16 v[34:37], v[176:179], v[192:195], v[34:37]
	v_mfma_f32_16x16x32_bf16 v[26:29], v[168:171], v[200:203], v[26:29]
	v_mfma_f32_16x16x32_bf16 v[18:21], v[176:179], v[200:203], v[18:21]
	v_mfma_f32_16x16x32_bf16 v[10:13], v[168:171], v[208:211], v[10:13]
	v_mfma_f32_16x16x32_bf16 v[2:5], v[176:179], v[208:211], v[2:5]
	v_mfma_f32_16x16x32_bf16 v[58:61], v[172:175], v[188:191], v[58:61]
	v_mfma_f32_16x16x32_bf16 v[50:53], v[180:183], v[188:191], v[50:53]
	v_mfma_f32_16x16x32_bf16 v[42:45], v[172:175], v[196:199], v[42:45]
	v_mfma_f32_16x16x32_bf16 v[34:37], v[180:183], v[196:199], v[34:37]
	v_mfma_f32_16x16x32_bf16 v[26:29], v[172:175], v[204:207], v[26:29]
	v_mfma_f32_16x16x32_bf16 v[18:21], v[180:183], v[204:207], v[18:21]
	v_mfma_f32_16x16x32_bf16 v[10:13], v[172:175], v[212:215], v[10:13]
	v_mfma_f32_16x16x32_bf16 v[2:5], v[180:183], v[212:215], v[2:5]
	s_barrier
	s_setprio 0
	s_add_i32 s85, s85, 2
	s_add_u32 s83, s83, 0x10000
	s_addc_u32 s84, s84, 0
	s_add_u32 s62, s62, 0x100
	s_addc_u32 s63, s63, 0
	s_cmp_gt_u32 s85, 29
	s_cbranch_scc0 .LBB0_783
	s_and_b64 vcc, exec, s[40:41]
	s_cbranch_vccz .LBB0_786
	s_barrier
	s_setprio 3

.LBB0_857:
	s_add_u32 s72, s50, 0x10000
	s_addc_u32 s73, s51, 0
	s_add_u32 s50, s52, 0xb0080
	s_addc_u32 s51, s53, 0
	s_mov_b32 s74, -2
	ds_read_b128 v[26:29], v185
	ds_read_b128 v[30:33], v185 offset:1024
	ds_read_b128 v[18:21], v185 offset:2048
	ds_read_b128 v[22:25], v185 offset:3072
	ds_read_b128 v[10:13], v186
	ds_read_b128 v[14:17], v186 offset:1024
	ds_read_b128 v[2:5], v186 offset:2048
	ds_read_b128 v[6:9], v186 offset:3072
	s_add_u32 s26, s50, 0xfff50080
	s_addc_u32 s27, s51, -1
	s_cmp_eq_u32 s74, 40
	s_cselect_b32 s53, s5, s27
	s_cselect_b32 s52, s4, s26
	s_cselect_b32 s55, s45, s73
	s_cselect_b32 s54, s44, s72
	v_lshl_add_u64 v[176:177], s[50:51], 0, v[168:169]
	s_add_i32 m0, s59, 0xc000
	ds_read_b128 v[190:193], v187
	ds_read_b128 v[194:197], v187 offset:1024
	ds_read_b128 v[198:201], v187 offset:2048
	ds_read_b128 v[202:205], v187 offset:3072
	ds_read_b128 v[206:209], v187 offset:4096
	ds_read_b128 v[210:213], v187 offset:5120
	ds_read_b128 v[220:223], v187 offset:6144
	ds_read_b128 v[224:227], v187 offset:7168
	global_load_lds_dwordx4 v[176:177], off
	v_lshl_add_u64 v[176:177], s[50:51], 0, v[170:171]
	s_add_i32 m0, s59, 0xe000
	s_nop 0
	global_load_lds_dwordx4 v[176:177], off
	s_setprio 1
	s_waitcnt vmcnt(8)
	s_waitcnt lgkmcnt(0)
	s_barrier
	v_mfma_scale_f32_16x16x128_f8f6f4 v[158:161], v[26:33], v[190:197], 0, v188, v189 op_sel_hi:[0,0,0]
	v_mfma_scale_f32_16x16x128_f8f6f4 v[154:157], v[18:25], v[190:197], 0, v188, v189 op_sel_hi:[0,0,0]
	v_mfma_scale_f32_16x16x128_f8f6f4 v[150:153], v[26:33], v[198:205], 0, v188, v189 op_sel_hi:[0,0,0]
	v_mfma_scale_f32_16x16x128_f8f6f4 v[146:149], v[18:25], v[198:205], 0, v188, v189 op_sel_hi:[0,0,0]
	v_mfma_scale_f32_16x16x128_f8f6f4 v[138:141], v[26:33], v[206:213], 0, v188, v189 op_sel_hi:[0,0,0]
	v_mfma_scale_f32_16x16x128_f8f6f4 v[130:133], v[18:25], v[206:213], 0, v188, v189 op_sel_hi:[0,0,0]
	v_mfma_scale_f32_16x16x128_f8f6f4 v[122:125], v[26:33], v[220:227], 0, v188, v189 op_sel_hi:[0,0,0]
	v_mfma_scale_f32_16x16x128_f8f6f4 v[114:117], v[18:25], v[220:227], 0, v188, v189 op_sel_hi:[0,0,0]
	v_mfma_scale_f32_16x16x128_f8f6f4 v[142:145], v[10:17], v[190:197], 0, v188, v189 op_sel_hi:[0,0,0]
	v_mfma_scale_f32_16x16x128_f8f6f4 v[134:137], v[2:9], v[190:197], 0, v188, v189 op_sel_hi:[0,0,0]
	v_mfma_scale_f32_16x16x128_f8f6f4 v[126:129], v[10:17], v[198:205], 0, v188, v189 op_sel_hi:[0,0,0]
	v_mfma_scale_f32_16x16x128_f8f6f4 v[118:121], v[2:9], v[198:205], 0, v188, v189 op_sel_hi:[0,0,0]
	v_mfma_scale_f32_16x16x128_f8f6f4 v[110:113], v[10:17], v[206:213], 0, v188, v189 op_sel_hi:[0,0,0]
	v_mfma_scale_f32_16x16x128_f8f6f4 v[106:109], v[2:9], v[206:213], 0, v188, v189 op_sel_hi:[0,0,0]
	v_mfma_scale_f32_16x16x128_f8f6f4 v[102:105], v[10:17], v[220:227], 0, v188, v189 op_sel_hi:[0,0,0]
	v_mfma_scale_f32_16x16x128_f8f6f4 v[98:101], v[2:9], v[220:227], 0, v188, v189 op_sel_hi:[0,0,0]
	s_barrier
	s_setprio 0
	s_add_i32 s26, s67, s57
	v_lshl_add_u64 v[176:177], s[54:55], 0, v[162:163]
	s_mov_b32 m0, s26
	ds_read_b128 v[190:193], v187 offset:16384
	ds_read_b128 v[194:197], v187 offset:17408
	ds_read_b128 v[198:201], v187 offset:18432
	ds_read_b128 v[202:205], v187 offset:19456
	ds_read_b128 v[206:209], v187 offset:20480
	ds_read_b128 v[210:213], v187 offset:21504
	ds_read_b128 v[220:223], v187 offset:22528
	ds_read_b128 v[224:227], v187 offset:23552
	global_load_lds_dwordx4 v[176:177], off
	v_lshl_add_u64 v[178:179], v[176:177], 0, s[8:9]
	s_add_i32 m0, s26, 0x2000
	s_add_i32 s26, s68, s57
	global_load_lds_dwordx4 v[178:179], off
	v_lshl_add_u64 v[178:179], v[176:177], 0, s[10:11]
	s_mov_b32 m0, s26
	v_lshl_add_u64 v[180:181], s[52:53], 0, v[166:167]
	global_load_lds_dwordx4 v[178:179], off
	v_lshl_add_u64 v[178:179], v[176:177], 0, s[12:13]
	s_add_i32 m0, s26, 0x2000
	s_nop 0
	global_load_lds_dwordx4 v[178:179], off
	v_lshl_add_u64 v[178:179], s[52:53], 0, v[164:165]
	s_mov_b32 m0, s59
	s_nop 0
	global_load_lds_dwordx4 v[178:179], off
	s_mov_b32 m0, s60
	s_nop 0
	global_load_lds_dwordx4 v[180:181], off
	s_setprio 1
	s_waitcnt vmcnt(8)
	s_waitcnt lgkmcnt(0)
	s_barrier
	v_mfma_scale_f32_16x16x128_f8f6f4 v[94:97], v[26:33], v[190:197], 0, v188, v189 op_sel_hi:[0,0,0]
	v_mfma_scale_f32_16x16x128_f8f6f4 v[90:93], v[18:25], v[190:197], 0, v188, v189 op_sel_hi:[0,0,0]
	v_mfma_scale_f32_16x16x128_f8f6f4 v[86:89], v[26:33], v[198:205], 0, v188, v189 op_sel_hi:[0,0,0]
	v_mfma_scale_f32_16x16x128_f8f6f4 v[78:81], v[18:25], v[198:205], 0, v188, v189 op_sel_hi:[0,0,0]
	v_mfma_scale_f32_16x16x128_f8f6f4 v[70:73], v[26:33], v[206:213], 0, v188, v189 op_sel_hi:[0,0,0]
	v_mfma_scale_f32_16x16x128_f8f6f4 v[62:65], v[18:25], v[206:213], 0, v188, v189 op_sel_hi:[0,0,0]
	v_mfma_scale_f32_16x16x128_f8f6f4 v[54:57], v[26:33], v[220:227], 0, v188, v189 op_sel_hi:[0,0,0]
	v_mfma_scale_f32_16x16x128_f8f6f4 v[46:49], v[18:25], v[220:227], 0, v188, v189 op_sel_hi:[0,0,0]
	v_mfma_scale_f32_16x16x128_f8f6f4 v[82:85], v[10:17], v[190:197], 0, v188, v189 op_sel_hi:[0,0,0]
	v_mfma_scale_f32_16x16x128_f8f6f4 v[74:77], v[2:9], v[190:197], 0, v188, v189 op_sel_hi:[0,0,0]
	v_mfma_scale_f32_16x16x128_f8f6f4 v[66:69], v[10:17], v[198:205], 0, v188, v189 op_sel_hi:[0,0,0]
	v_mfma_scale_f32_16x16x128_f8f6f4 v[58:61], v[2:9], v[198:205], 0, v188, v189 op_sel_hi:[0,0,0]
	v_mfma_scale_f32_16x16x128_f8f6f4 v[50:53], v[10:17], v[206:213], 0, v188, v189 op_sel_hi:[0,0,0]
	v_mfma_scale_f32_16x16x128_f8f6f4 v[42:45], v[2:9], v[206:213], 0, v188, v189 op_sel_hi:[0,0,0]
	v_mfma_scale_f32_16x16x128_f8f6f4 v[38:41], v[10:17], v[220:227], 0, v188, v189 op_sel_hi:[0,0,0]
	v_mfma_scale_f32_16x16x128_f8f6f4 v[34:37], v[2:9], v[220:227], 0, v188, v189 op_sel_hi:[0,0,0]
	s_barrier
	s_setprio 0
	s_add_i32 s54, 0, 0x18000
	s_add_i32 s55, 0, 0x1c000
	v_add_u32_e32 v14, s54, v183
	v_add_u32_e32 v30, s55, v183
	ds_read_b128 v[2:5], v14
	ds_read_b128 v[6:9], v14 offset:1024
	ds_read_b128 v[10:13], v14 offset:2048
	ds_read_b128 v[14:17], v14 offset:3072
	ds_read_b128 v[18:21], v30
	ds_read_b128 v[22:25], v30 offset:1024
	ds_read_b128 v[26:29], v30 offset:2048
	ds_read_b128 v[30:33], v30 offset:3072
	s_add_u32 s26, s52, 0xb0000
	s_addc_u32 s27, s53, 0
	s_mov_b32 m0, s61
	v_lshl_add_u64 v[214:215], s[26:27], 0, v[164:165]
	ds_read_b128 v[190:193], v187 offset:32768
	ds_read_b128 v[194:197], v187 offset:33792
	ds_read_b128 v[198:201], v187 offset:34816
	ds_read_b128 v[202:205], v187 offset:35840
	ds_read_b128 v[206:209], v187 offset:36864
	ds_read_b128 v[210:213], v187 offset:37888
	ds_read_b128 v[220:223], v187 offset:38912
	ds_read_b128 v[224:227], v187 offset:39936
	global_load_lds_dwordx4 v[214:215], off
	v_lshl_add_u64 v[214:215], s[26:27], 0, v[166:167]
	s_mov_b32 m0, s62
	s_nop 0
	global_load_lds_dwordx4 v[214:215], off
	s_setprio 1
	s_waitcnt vmcnt(8)
	s_waitcnt lgkmcnt(0)
	s_barrier
	v_mfma_scale_f32_16x16x128_f8f6f4 v[158:161], v[2:9], v[190:197], v[158:161], v188, v189 op_sel_hi:[0,0,0]
	v_mfma_scale_f32_16x16x128_f8f6f4 v[154:157], v[10:17], v[190:197], v[154:157], v188, v189 op_sel_hi:[0,0,0]
	v_mfma_scale_f32_16x16x128_f8f6f4 v[150:153], v[2:9], v[198:205], v[150:153], v188, v189 op_sel_hi:[0,0,0]
	v_mfma_scale_f32_16x16x128_f8f6f4 v[146:149], v[10:17], v[198:205], v[146:149], v188, v189 op_sel_hi:[0,0,0]
	v_mfma_scale_f32_16x16x128_f8f6f4 v[138:141], v[2:9], v[206:213], v[138:141], v188, v189 op_sel_hi:[0,0,0]
	v_mfma_scale_f32_16x16x128_f8f6f4 v[130:133], v[10:17], v[206:213], v[130:133], v188, v189 op_sel_hi:[0,0,0]
	v_mfma_scale_f32_16x16x128_f8f6f4 v[122:125], v[2:9], v[220:227], v[122:125], v188, v189 op_sel_hi:[0,0,0]
	v_mfma_scale_f32_16x16x128_f8f6f4 v[114:117], v[10:17], v[220:227], v[114:117], v188, v189 op_sel_hi:[0,0,0]
	v_mfma_scale_f32_16x16x128_f8f6f4 v[142:145], v[18:25], v[190:197], v[142:145], v188, v189 op_sel_hi:[0,0,0]
	v_mfma_scale_f32_16x16x128_f8f6f4 v[134:137], v[26:33], v[190:197], v[134:137], v188, v189 op_sel_hi:[0,0,0]
	v_mfma_scale_f32_16x16x128_f8f6f4 v[126:129], v[18:25], v[198:205], v[126:129], v188, v189 op_sel_hi:[0,0,0]
	v_mfma_scale_f32_16x16x128_f8f6f4 v[118:121], v[26:33], v[198:205], v[118:121], v188, v189 op_sel_hi:[0,0,0]
	v_mfma_scale_f32_16x16x128_f8f6f4 v[110:113], v[18:25], v[206:213], v[110:113], v188, v189 op_sel_hi:[0,0,0]
	v_mfma_scale_f32_16x16x128_f8f6f4 v[106:109], v[26:33], v[206:213], v[106:109], v188, v189 op_sel_hi:[0,0,0]
	v_mfma_scale_f32_16x16x128_f8f6f4 v[102:105], v[18:25], v[220:227], v[102:105], v188, v189 op_sel_hi:[0,0,0]
	v_mfma_scale_f32_16x16x128_f8f6f4 v[98:101], v[26:33], v[220:227], v[98:101], v188, v189 op_sel_hi:[0,0,0]
	s_barrier
	s_setprio 0
	s_add_i32 s26, s54, s57
	v_lshl_add_u64 v[214:215], v[176:177], 0, s[16:17]
	s_mov_b32 m0, s26
	ds_read_b128 v[190:193], v187 offset:49152
	ds_read_b128 v[194:197], v187 offset:50176
	ds_read_b128 v[198:201], v187 offset:51200
	ds_read_b128 v[202:205], v187 offset:52224
	ds_read_b128 v[206:209], v187 offset:53248
	ds_read_b128 v[210:213], v187 offset:54272
	ds_read_b128 v[220:223], v187 offset:55296
	ds_read_b128 v[224:227], v187 offset:56320
	global_load_lds_dwordx4 v[214:215], off
	v_lshl_add_u64 v[214:215], v[176:177], 0, s[18:19]
	s_add_i32 m0, s26, 0x2000
	s_add_i32 s26, s55, s57
	global_load_lds_dwordx4 v[214:215], off
	v_lshl_add_u64 v[214:215], v[176:177], 0, s[22:23]
	s_mov_b32 m0, s26
	v_lshl_add_u64 v[176:177], v[176:177], 0, s[24:25]
	global_load_lds_dwordx4 v[214:215], off
	s_add_i32 m0, s26, 0x2000
	s_nop 0
	global_load_lds_dwordx4 v[176:177], off
	v_lshl_add_u64 v[176:177], v[178:179], 0, s[20:21]
	s_mov_b32 m0, s64
	s_nop 0
	global_load_lds_dwordx4 v[176:177], off
	v_lshl_add_u64 v[176:177], v[180:181], 0, s[20:21]
	s_mov_b32 m0, s65
	s_nop 0
	global_load_lds_dwordx4 v[176:177], off
	s_setprio 1
	s_waitcnt vmcnt(8)
	s_waitcnt lgkmcnt(0)
	s_barrier
	v_mfma_scale_f32_16x16x128_f8f6f4 v[94:97], v[2:9], v[190:197], v[94:97], v188, v189 op_sel_hi:[0,0,0]
	v_mfma_scale_f32_16x16x128_f8f6f4 v[90:93], v[10:17], v[190:197], v[90:93], v188, v189 op_sel_hi:[0,0,0]
	v_mfma_scale_f32_16x16x128_f8f6f4 v[86:89], v[2:9], v[198:205], v[86:89], v188, v189 op_sel_hi:[0,0,0]
	v_mfma_scale_f32_16x16x128_f8f6f4 v[78:81], v[10:17], v[198:205], v[78:81], v188, v189 op_sel_hi:[0,0,0]
	v_mfma_scale_f32_16x16x128_f8f6f4 v[70:73], v[2:9], v[206:213], v[70:73], v188, v189 op_sel_hi:[0,0,0]
	v_mfma_scale_f32_16x16x128_f8f6f4 v[62:65], v[10:17], v[206:213], v[62:65], v188, v189 op_sel_hi:[0,0,0]
	v_mfma_scale_f32_16x16x128_f8f6f4 v[54:57], v[2:9], v[220:227], v[54:57], v188, v189 op_sel_hi:[0,0,0]
	v_mfma_scale_f32_16x16x128_f8f6f4 v[46:49], v[10:17], v[220:227], v[46:49], v188, v189 op_sel_hi:[0,0,0]
	v_mfma_scale_f32_16x16x128_f8f6f4 v[82:85], v[18:25], v[190:197], v[82:85], v188, v189 op_sel_hi:[0,0,0]
	v_mfma_scale_f32_16x16x128_f8f6f4 v[74:77], v[26:33], v[190:197], v[74:77], v188, v189 op_sel_hi:[0,0,0]
	v_mfma_scale_f32_16x16x128_f8f6f4 v[66:69], v[18:25], v[198:205], v[66:69], v188, v189 op_sel_hi:[0,0,0]
	v_mfma_scale_f32_16x16x128_f8f6f4 v[58:61], v[26:33], v[198:205], v[58:61], v188, v189 op_sel_hi:[0,0,0]
	v_mfma_scale_f32_16x16x128_f8f6f4 v[50:53], v[18:25], v[206:213], v[50:53], v188, v189 op_sel_hi:[0,0,0]
	v_mfma_scale_f32_16x16x128_f8f6f4 v[42:45], v[26:33], v[206:213], v[42:45], v188, v189 op_sel_hi:[0,0,0]
	v_mfma_scale_f32_16x16x128_f8f6f4 v[38:41], v[18:25], v[220:227], v[38:41], v188, v189 op_sel_hi:[0,0,0]
	v_mfma_scale_f32_16x16x128_f8f6f4 v[34:37], v[26:33], v[220:227], v[34:37], v188, v189 op_sel_hi:[0,0,0]
	s_barrier
	s_setprio 0
	s_add_i32 s74, s74, 2
	s_add_u32 s72, s72, 0x10000
	s_addc_u32 s73, s73, 0
	s_add_u32 s50, s50, 0x100
	s_addc_u32 s51, s51, 0
	s_cmp_gt_u32 s74, 41
.LBB0_858:
	ds_read_b128 v[26:29], v185
	ds_read_b128 v[30:33], v185 offset:1024
	ds_read_b128 v[18:21], v185 offset:2048
	ds_read_b128 v[22:25], v185 offset:3072
	ds_read_b128 v[10:13], v186
	ds_read_b128 v[14:17], v186 offset:1024
	ds_read_b128 v[2:5], v186 offset:2048
	ds_read_b128 v[6:9], v186 offset:3072
	s_add_u32 s26, s50, 0xfff50080
	s_addc_u32 s27, s51, -1
	s_cmp_eq_u32 s74, 40
	s_cselect_b32 s53, s5, s27
	s_cselect_b32 s52, s4, s26
	s_cselect_b32 s55, s45, s73
	s_cselect_b32 s54, s44, s72
	v_lshl_add_u64 v[176:177], s[50:51], 0, v[168:169]
	s_add_i32 m0, s59, 0xc000
	ds_read_b128 v[190:193], v187
	ds_read_b128 v[194:197], v187 offset:1024
	ds_read_b128 v[198:201], v187 offset:2048
	ds_read_b128 v[202:205], v187 offset:3072
	ds_read_b128 v[206:209], v187 offset:4096
	ds_read_b128 v[210:213], v187 offset:5120
	ds_read_b128 v[220:223], v187 offset:6144
	ds_read_b128 v[224:227], v187 offset:7168
	global_load_lds_dwordx4 v[176:177], off
	v_lshl_add_u64 v[176:177], s[50:51], 0, v[170:171]
	s_add_i32 m0, s59, 0xe000
	s_nop 0
	global_load_lds_dwordx4 v[176:177], off
	s_setprio 1
	s_waitcnt vmcnt(8)
	s_waitcnt lgkmcnt(0)
	s_barrier
	v_mfma_scale_f32_16x16x128_f8f6f4 v[158:161], v[26:33], v[190:197], v[158:161], v188, v189 op_sel_hi:[0,0,0]
	v_mfma_scale_f32_16x16x128_f8f6f4 v[154:157], v[18:25], v[190:197], v[154:157], v188, v189 op_sel_hi:[0,0,0]
	v_mfma_scale_f32_16x16x128_f8f6f4 v[150:153], v[26:33], v[198:205], v[150:153], v188, v189 op_sel_hi:[0,0,0]
	v_mfma_scale_f32_16x16x128_f8f6f4 v[146:149], v[18:25], v[198:205], v[146:149], v188, v189 op_sel_hi:[0,0,0]
	v_mfma_scale_f32_16x16x128_f8f6f4 v[138:141], v[26:33], v[206:213], v[138:141], v188, v189 op_sel_hi:[0,0,0]
	v_mfma_scale_f32_16x16x128_f8f6f4 v[130:133], v[18:25], v[206:213], v[130:133], v188, v189 op_sel_hi:[0,0,0]
	v_mfma_scale_f32_16x16x128_f8f6f4 v[122:125], v[26:33], v[220:227], v[122:125], v188, v189 op_sel_hi:[0,0,0]
	v_mfma_scale_f32_16x16x128_f8f6f4 v[114:117], v[18:25], v[220:227], v[114:117], v188, v189 op_sel_hi:[0,0,0]
	v_mfma_scale_f32_16x16x128_f8f6f4 v[142:145], v[10:17], v[190:197], v[142:145], v188, v189 op_sel_hi:[0,0,0]
	v_mfma_scale_f32_16x16x128_f8f6f4 v[134:137], v[2:9], v[190:197], v[134:137], v188, v189 op_sel_hi:[0,0,0]
	v_mfma_scale_f32_16x16x128_f8f6f4 v[126:129], v[10:17], v[198:205], v[126:129], v188, v189 op_sel_hi:[0,0,0]
	v_mfma_scale_f32_16x16x128_f8f6f4 v[118:121], v[2:9], v[198:205], v[118:121], v188, v189 op_sel_hi:[0,0,0]
	v_mfma_scale_f32_16x16x128_f8f6f4 v[110:113], v[10:17], v[206:213], v[110:113], v188, v189 op_sel_hi:[0,0,0]
	v_mfma_scale_f32_16x16x128_f8f6f4 v[106:109], v[2:9], v[206:213], v[106:109], v188, v189 op_sel_hi:[0,0,0]
	v_mfma_scale_f32_16x16x128_f8f6f4 v[102:105], v[10:17], v[220:227], v[102:105], v188, v189 op_sel_hi:[0,0,0]
	v_mfma_scale_f32_16x16x128_f8f6f4 v[98:101], v[2:9], v[220:227], v[98:101], v188, v189 op_sel_hi:[0,0,0]
	s_barrier
	s_setprio 0
	s_add_i32 s26, s67, s57
	v_lshl_add_u64 v[176:177], s[54:55], 0, v[162:163]
	s_mov_b32 m0, s26
	ds_read_b128 v[190:193], v187 offset:16384
	ds_read_b128 v[194:197], v187 offset:17408
	ds_read_b128 v[198:201], v187 offset:18432
	ds_read_b128 v[202:205], v187 offset:19456
	ds_read_b128 v[206:209], v187 offset:20480
	ds_read_b128 v[210:213], v187 offset:21504
	ds_read_b128 v[220:223], v187 offset:22528
	ds_read_b128 v[224:227], v187 offset:23552
	global_load_lds_dwordx4 v[176:177], off
	v_lshl_add_u64 v[178:179], v[176:177], 0, s[8:9]
	s_add_i32 m0, s26, 0x2000
	s_add_i32 s26, s68, s57
	global_load_lds_dwordx4 v[178:179], off
	v_lshl_add_u64 v[178:179], v[176:177], 0, s[10:11]
	s_mov_b32 m0, s26
	v_lshl_add_u64 v[180:181], s[52:53], 0, v[166:167]
	global_load_lds_dwordx4 v[178:179], off
	v_lshl_add_u64 v[178:179], v[176:177], 0, s[12:13]
	s_add_i32 m0, s26, 0x2000
	s_nop 0
	global_load_lds_dwordx4 v[178:179], off
	v_lshl_add_u64 v[178:179], s[52:53], 0, v[164:165]
	s_mov_b32 m0, s59
	s_nop 0
	global_load_lds_dwordx4 v[178:179], off
	s_mov_b32 m0, s60
	s_nop 0
	global_load_lds_dwordx4 v[180:181], off
	s_setprio 1
	s_waitcnt vmcnt(8)
	s_waitcnt lgkmcnt(0)
	s_barrier
	v_mfma_scale_f32_16x16x128_f8f6f4 v[94:97], v[26:33], v[190:197], v[94:97], v188, v189 op_sel_hi:[0,0,0]
	v_mfma_scale_f32_16x16x128_f8f6f4 v[90:93], v[18:25], v[190:197], v[90:93], v188, v189 op_sel_hi:[0,0,0]
	v_mfma_scale_f32_16x16x128_f8f6f4 v[86:89], v[26:33], v[198:205], v[86:89], v188, v189 op_sel_hi:[0,0,0]
	v_mfma_scale_f32_16x16x128_f8f6f4 v[78:81], v[18:25], v[198:205], v[78:81], v188, v189 op_sel_hi:[0,0,0]
	v_mfma_scale_f32_16x16x128_f8f6f4 v[70:73], v[26:33], v[206:213], v[70:73], v188, v189 op_sel_hi:[0,0,0]
	v_mfma_scale_f32_16x16x128_f8f6f4 v[62:65], v[18:25], v[206:213], v[62:65], v188, v189 op_sel_hi:[0,0,0]
	v_mfma_scale_f32_16x16x128_f8f6f4 v[54:57], v[26:33], v[220:227], v[54:57], v188, v189 op_sel_hi:[0,0,0]
	v_mfma_scale_f32_16x16x128_f8f6f4 v[46:49], v[18:25], v[220:227], v[46:49], v188, v189 op_sel_hi:[0,0,0]
	v_mfma_scale_f32_16x16x128_f8f6f4 v[82:85], v[10:17], v[190:197], v[82:85], v188, v189 op_sel_hi:[0,0,0]
	v_mfma_scale_f32_16x16x128_f8f6f4 v[74:77], v[2:9], v[190:197], v[74:77], v188, v189 op_sel_hi:[0,0,0]
	v_mfma_scale_f32_16x16x128_f8f6f4 v[66:69], v[10:17], v[198:205], v[66:69], v188, v189 op_sel_hi:[0,0,0]
	v_mfma_scale_f32_16x16x128_f8f6f4 v[58:61], v[2:9], v[198:205], v[58:61], v188, v189 op_sel_hi:[0,0,0]
	v_mfma_scale_f32_16x16x128_f8f6f4 v[50:53], v[10:17], v[206:213], v[50:53], v188, v189 op_sel_hi:[0,0,0]
	v_mfma_scale_f32_16x16x128_f8f6f4 v[42:45], v[2:9], v[206:213], v[42:45], v188, v189 op_sel_hi:[0,0,0]
	v_mfma_scale_f32_16x16x128_f8f6f4 v[38:41], v[10:17], v[220:227], v[38:41], v188, v189 op_sel_hi:[0,0,0]
	v_mfma_scale_f32_16x16x128_f8f6f4 v[34:37], v[2:9], v[220:227], v[34:37], v188, v189 op_sel_hi:[0,0,0]
	s_barrier
	s_setprio 0
	s_add_i32 s54, 0, 0x18000
	s_add_i32 s55, 0, 0x1c000
	v_add_u32_e32 v14, s54, v183
	v_add_u32_e32 v30, s55, v183
	ds_read_b128 v[2:5], v14
	ds_read_b128 v[6:9], v14 offset:1024
	ds_read_b128 v[10:13], v14 offset:2048
	ds_read_b128 v[14:17], v14 offset:3072
	ds_read_b128 v[18:21], v30
	ds_read_b128 v[22:25], v30 offset:1024
	ds_read_b128 v[26:29], v30 offset:2048
	ds_read_b128 v[30:33], v30 offset:3072
	s_add_u32 s26, s52, 0xb0000
	s_addc_u32 s27, s53, 0
	s_mov_b32 m0, s61
	v_lshl_add_u64 v[214:215], s[26:27], 0, v[164:165]
	ds_read_b128 v[190:193], v187 offset:32768
	ds_read_b128 v[194:197], v187 offset:33792
	ds_read_b128 v[198:201], v187 offset:34816
	ds_read_b128 v[202:205], v187 offset:35840
	ds_read_b128 v[206:209], v187 offset:36864
	ds_read_b128 v[210:213], v187 offset:37888
	ds_read_b128 v[220:223], v187 offset:38912
	ds_read_b128 v[224:227], v187 offset:39936
	global_load_lds_dwordx4 v[214:215], off
	v_lshl_add_u64 v[214:215], s[26:27], 0, v[166:167]
	s_mov_b32 m0, s62
	s_nop 0
	global_load_lds_dwordx4 v[214:215], off
	s_setprio 1
	s_waitcnt vmcnt(8)
	s_waitcnt lgkmcnt(0)
	s_barrier
	v_mfma_scale_f32_16x16x128_f8f6f4 v[158:161], v[2:9], v[190:197], v[158:161], v188, v189 op_sel_hi:[0,0,0]
	v_mfma_scale_f32_16x16x128_f8f6f4 v[154:157], v[10:17], v[190:197], v[154:157], v188, v189 op_sel_hi:[0,0,0]
	v_mfma_scale_f32_16x16x128_f8f6f4 v[150:153], v[2:9], v[198:205], v[150:153], v188, v189 op_sel_hi:[0,0,0]
	v_mfma_scale_f32_16x16x128_f8f6f4 v[146:149], v[10:17], v[198:205], v[146:149], v188, v189 op_sel_hi:[0,0,0]
	v_mfma_scale_f32_16x16x128_f8f6f4 v[138:141], v[2:9], v[206:213], v[138:141], v188, v189 op_sel_hi:[0,0,0]
	v_mfma_scale_f32_16x16x128_f8f6f4 v[130:133], v[10:17], v[206:213], v[130:133], v188, v189 op_sel_hi:[0,0,0]
	v_mfma_scale_f32_16x16x128_f8f6f4 v[122:125], v[2:9], v[220:227], v[122:125], v188, v189 op_sel_hi:[0,0,0]
	v_mfma_scale_f32_16x16x128_f8f6f4 v[114:117], v[10:17], v[220:227], v[114:117], v188, v189 op_sel_hi:[0,0,0]
	v_mfma_scale_f32_16x16x128_f8f6f4 v[142:145], v[18:25], v[190:197], v[142:145], v188, v189 op_sel_hi:[0,0,0]
	v_mfma_scale_f32_16x16x128_f8f6f4 v[134:137], v[26:33], v[190:197], v[134:137], v188, v189 op_sel_hi:[0,0,0]
	v_mfma_scale_f32_16x16x128_f8f6f4 v[126:129], v[18:25], v[198:205], v[126:129], v188, v189 op_sel_hi:[0,0,0]
	v_mfma_scale_f32_16x16x128_f8f6f4 v[118:121], v[26:33], v[198:205], v[118:121], v188, v189 op_sel_hi:[0,0,0]
	v_mfma_scale_f32_16x16x128_f8f6f4 v[110:113], v[18:25], v[206:213], v[110:113], v188, v189 op_sel_hi:[0,0,0]
	v_mfma_scale_f32_16x16x128_f8f6f4 v[106:109], v[26:33], v[206:213], v[106:109], v188, v189 op_sel_hi:[0,0,0]
	v_mfma_scale_f32_16x16x128_f8f6f4 v[102:105], v[18:25], v[220:227], v[102:105], v188, v189 op_sel_hi:[0,0,0]
	v_mfma_scale_f32_16x16x128_f8f6f4 v[98:101], v[26:33], v[220:227], v[98:101], v188, v189 op_sel_hi:[0,0,0]
	s_barrier
	s_setprio 0
	s_add_i32 s26, s54, s57
	v_lshl_add_u64 v[214:215], v[176:177], 0, s[16:17]
	s_mov_b32 m0, s26
	ds_read_b128 v[190:193], v187 offset:49152
	ds_read_b128 v[194:197], v187 offset:50176
	ds_read_b128 v[198:201], v187 offset:51200
	ds_read_b128 v[202:205], v187 offset:52224
	ds_read_b128 v[206:209], v187 offset:53248
	ds_read_b128 v[210:213], v187 offset:54272
	ds_read_b128 v[220:223], v187 offset:55296
	ds_read_b128 v[224:227], v187 offset:56320
	global_load_lds_dwordx4 v[214:215], off
	v_lshl_add_u64 v[214:215], v[176:177], 0, s[18:19]
	s_add_i32 m0, s26, 0x2000
	s_add_i32 s26, s55, s57
	global_load_lds_dwordx4 v[214:215], off
	v_lshl_add_u64 v[214:215], v[176:177], 0, s[22:23]
	s_mov_b32 m0, s26
	v_lshl_add_u64 v[176:177], v[176:177], 0, s[24:25]
	global_load_lds_dwordx4 v[214:215], off
	s_add_i32 m0, s26, 0x2000
	s_nop 0
	global_load_lds_dwordx4 v[176:177], off
	v_lshl_add_u64 v[176:177], v[178:179], 0, s[20:21]
	s_mov_b32 m0, s64
	s_nop 0
	global_load_lds_dwordx4 v[176:177], off
	v_lshl_add_u64 v[176:177], v[180:181], 0, s[20:21]
	s_mov_b32 m0, s65
	s_nop 0
	global_load_lds_dwordx4 v[176:177], off
	s_setprio 1
	s_waitcnt vmcnt(8)
	s_waitcnt lgkmcnt(0)
	s_barrier
	v_mfma_scale_f32_16x16x128_f8f6f4 v[94:97], v[2:9], v[190:197], v[94:97], v188, v189 op_sel_hi:[0,0,0]
	v_mfma_scale_f32_16x16x128_f8f6f4 v[90:93], v[10:17], v[190:197], v[90:93], v188, v189 op_sel_hi:[0,0,0]
	v_mfma_scale_f32_16x16x128_f8f6f4 v[86:89], v[2:9], v[198:205], v[86:89], v188, v189 op_sel_hi:[0,0,0]
	v_mfma_scale_f32_16x16x128_f8f6f4 v[78:81], v[10:17], v[198:205], v[78:81], v188, v189 op_sel_hi:[0,0,0]
	v_mfma_scale_f32_16x16x128_f8f6f4 v[70:73], v[2:9], v[206:213], v[70:73], v188, v189 op_sel_hi:[0,0,0]
	v_mfma_scale_f32_16x16x128_f8f6f4 v[62:65], v[10:17], v[206:213], v[62:65], v188, v189 op_sel_hi:[0,0,0]
	v_mfma_scale_f32_16x16x128_f8f6f4 v[54:57], v[2:9], v[220:227], v[54:57], v188, v189 op_sel_hi:[0,0,0]
	v_mfma_scale_f32_16x16x128_f8f6f4 v[46:49], v[10:17], v[220:227], v[46:49], v188, v189 op_sel_hi:[0,0,0]
	v_mfma_scale_f32_16x16x128_f8f6f4 v[82:85], v[18:25], v[190:197], v[82:85], v188, v189 op_sel_hi:[0,0,0]
	v_mfma_scale_f32_16x16x128_f8f6f4 v[74:77], v[26:33], v[190:197], v[74:77], v188, v189 op_sel_hi:[0,0,0]
	v_mfma_scale_f32_16x16x128_f8f6f4 v[66:69], v[18:25], v[198:205], v[66:69], v188, v189 op_sel_hi:[0,0,0]
	v_mfma_scale_f32_16x16x128_f8f6f4 v[58:61], v[26:33], v[198:205], v[58:61], v188, v189 op_sel_hi:[0,0,0]
	v_mfma_scale_f32_16x16x128_f8f6f4 v[50:53], v[18:25], v[206:213], v[50:53], v188, v189 op_sel_hi:[0,0,0]
	v_mfma_scale_f32_16x16x128_f8f6f4 v[42:45], v[26:33], v[206:213], v[42:45], v188, v189 op_sel_hi:[0,0,0]
	v_mfma_scale_f32_16x16x128_f8f6f4 v[38:41], v[18:25], v[220:227], v[38:41], v188, v189 op_sel_hi:[0,0,0]
	v_mfma_scale_f32_16x16x128_f8f6f4 v[34:37], v[26:33], v[220:227], v[34:37], v188, v189 op_sel_hi:[0,0,0]
	s_barrier
	s_setprio 0
	s_add_i32 s74, s74, 2
	s_add_u32 s72, s72, 0x10000
	s_addc_u32 s73, s73, 0
	s_add_u32 s50, s50, 0x100
	s_addc_u32 s51, s51, 0
	s_cmp_gt_u32 s74, 41
	s_cbranch_scc0 .LBB0_858
	s_and_b64 vcc, exec, s[40:41]
	s_cbranch_vccz .LBB0_861
	s_barrier
	s_setprio 3

.LBB0_984:
	s_ashr_i32 s45, s44, 31
	s_lshl_b64 s[26:27], s[44:45], 19
	v_readlane_b32 s50, v254, 56
	v_readlane_b32 s51, v254, 57
	s_add_u32 s50, s50, s26
	s_addc_u32 s51, s51, s27
	s_and_b64 s[26:27], s[0:1], exec
	s_cselect_b32 s45, s51, s59
	s_cselect_b32 s72, s50, s58
	s_ashr_i32 s41, s40, 31
	s_lshl_b64 s[26:27], s[40:41], 19
	s_add_u32 s52, s3, s26
	s_addc_u32 s53, s33, s27
	s_and_b64 s[26:27], s[0:1], exec
	s_cselect_b32 s41, s53, s57
	s_cselect_b32 s73, s52, s56
	s_add_u32 s74, s56, 0x10000
	s_addc_u32 s75, s57, 0
	s_add_u32 s56, s58, 0x40080
	s_addc_u32 s57, s59, 0
	s_mov_b32 s80, -2
	ds_read_b128 v[26:29], v185
	ds_read_b128 v[30:33], v185 offset:1024
	ds_read_b128 v[18:21], v185 offset:2048
	ds_read_b128 v[22:25], v185 offset:3072
	ds_read_b128 v[10:13], v186
	ds_read_b128 v[14:17], v186 offset:1024
	ds_read_b128 v[2:5], v186 offset:2048
	ds_read_b128 v[6:9], v186 offset:3072
	s_add_u32 s26, s56, 0xfffc0080
	s_addc_u32 s27, s57, -1
	s_cmp_eq_u32 s80, 12
	s_cselect_b32 s59, s45, s27
	s_cselect_b32 s58, s72, s26
	s_cselect_b32 s61, s41, s75
	s_cselect_b32 s60, s73, s74
	v_lshl_add_u64 v[176:177], s[56:57], 0, v[168:169]
	s_add_i32 m0, s55, 0xc000
	ds_read_b128 v[192:195], v187
	ds_read_b128 v[196:199], v187 offset:1024
	ds_read_b128 v[200:203], v187 offset:2048
	ds_read_b128 v[204:207], v187 offset:3072
	ds_read_b128 v[208:211], v187 offset:4096
	ds_read_b128 v[212:215], v187 offset:5120
	ds_read_b128 v[220:223], v187 offset:6144
	ds_read_b128 v[224:227], v187 offset:7168
	global_load_lds_dwordx4 v[176:177], off
	v_lshl_add_u64 v[176:177], s[56:57], 0, v[170:171]
	s_add_i32 m0, s55, 0xe000
	s_nop 0
	global_load_lds_dwordx4 v[176:177], off
	s_setprio 1
	s_waitcnt vmcnt(24)
	s_waitcnt lgkmcnt(0)
	s_barrier
	v_mfma_scale_f32_16x16x128_f8f6f4 v[158:161], v[26:33], v[192:199], 0, v188, v189 op_sel_hi:[0,0,0]
	v_mfma_scale_f32_16x16x128_f8f6f4 v[154:157], v[18:25], v[192:199], 0, v188, v189 op_sel_hi:[0,0,0]
	v_mfma_scale_f32_16x16x128_f8f6f4 v[146:149], v[26:33], v[200:207], 0, v188, v189 op_sel_hi:[0,0,0]
	v_mfma_scale_f32_16x16x128_f8f6f4 v[138:141], v[18:25], v[200:207], 0, v188, v189 op_sel_hi:[0,0,0]
	v_mfma_scale_f32_16x16x128_f8f6f4 v[130:133], v[26:33], v[208:215], 0, v188, v189 op_sel_hi:[0,0,0]
	v_mfma_scale_f32_16x16x128_f8f6f4 v[122:125], v[18:25], v[208:215], 0, v188, v189 op_sel_hi:[0,0,0]
	v_mfma_scale_f32_16x16x128_f8f6f4 v[114:117], v[26:33], v[220:227], 0, v188, v189 op_sel_hi:[0,0,0]
	v_mfma_scale_f32_16x16x128_f8f6f4 v[106:109], v[18:25], v[220:227], 0, v188, v189 op_sel_hi:[0,0,0]
	v_mfma_scale_f32_16x16x128_f8f6f4 v[150:153], v[10:17], v[192:199], 0, v188, v189 op_sel_hi:[0,0,0]
	v_mfma_scale_f32_16x16x128_f8f6f4 v[142:145], v[2:9], v[192:199], 0, v188, v189 op_sel_hi:[0,0,0]
	v_mfma_scale_f32_16x16x128_f8f6f4 v[134:137], v[10:17], v[200:207], 0, v188, v189 op_sel_hi:[0,0,0]
	v_mfma_scale_f32_16x16x128_f8f6f4 v[126:129], v[2:9], v[200:207], 0, v188, v189 op_sel_hi:[0,0,0]
	v_mfma_scale_f32_16x16x128_f8f6f4 v[118:121], v[10:17], v[208:215], 0, v188, v189 op_sel_hi:[0,0,0]
	v_mfma_scale_f32_16x16x128_f8f6f4 v[110:113], v[2:9], v[208:215], 0, v188, v189 op_sel_hi:[0,0,0]
	v_mfma_scale_f32_16x16x128_f8f6f4 v[102:105], v[10:17], v[220:227], 0, v188, v189 op_sel_hi:[0,0,0]
	v_mfma_scale_f32_16x16x128_f8f6f4 v[98:101], v[2:9], v[220:227], 0, v188, v189 op_sel_hi:[0,0,0]
	s_barrier
	s_setprio 0
	s_add_i32 s26, s70, s35
	v_lshl_add_u64 v[176:177], s[60:61], 0, v[162:163]
	s_mov_b32 m0, s26
	ds_read_b128 v[192:195], v187 offset:16384
	ds_read_b128 v[196:199], v187 offset:17408
	ds_read_b128 v[200:203], v187 offset:18432
	ds_read_b128 v[204:207], v187 offset:19456
	ds_read_b128 v[208:211], v187 offset:20480
	ds_read_b128 v[212:215], v187 offset:21504
	ds_read_b128 v[220:223], v187 offset:22528
	ds_read_b128 v[224:227], v187 offset:23552
	global_load_lds_dwordx4 v[176:177], off
	v_lshl_add_u64 v[178:179], v[176:177], 0, s[6:7]
	s_add_i32 m0, s26, 0x2000
	s_add_i32 s26, s71, s35
	global_load_lds_dwordx4 v[178:179], off
	v_lshl_add_u64 v[178:179], v[176:177], 0, s[8:9]
	s_mov_b32 m0, s26
	v_lshl_add_u64 v[180:181], s[58:59], 0, v[166:167]
	global_load_lds_dwordx4 v[178:179], off
	v_lshl_add_u64 v[178:179], v[176:177], 0, s[10:11]
	s_add_i32 m0, s26, 0x2000
	s_nop 0
	global_load_lds_dwordx4 v[178:179], off
	v_lshl_add_u64 v[178:179], s[58:59], 0, v[164:165]
	s_mov_b32 m0, s55
	s_nop 0
	global_load_lds_dwordx4 v[178:179], off
	s_mov_b32 m0, s63
	s_nop 0
	global_load_lds_dwordx4 v[180:181], off
	s_setprio 1
	s_waitcnt vmcnt(24)
	s_waitcnt lgkmcnt(0)
	s_barrier
	v_mfma_scale_f32_16x16x128_f8f6f4 v[94:97], v[26:33], v[192:199], 0, v188, v189 op_sel_hi:[0,0,0]
	v_mfma_scale_f32_16x16x128_f8f6f4 v[90:93], v[18:25], v[192:199], 0, v188, v189 op_sel_hi:[0,0,0]
	v_mfma_scale_f32_16x16x128_f8f6f4 v[82:85], v[26:33], v[200:207], 0, v188, v189 op_sel_hi:[0,0,0]
	v_mfma_scale_f32_16x16x128_f8f6f4 v[74:77], v[18:25], v[200:207], 0, v188, v189 op_sel_hi:[0,0,0]
	v_mfma_scale_f32_16x16x128_f8f6f4 v[66:69], v[26:33], v[208:215], 0, v188, v189 op_sel_hi:[0,0,0]
	v_mfma_scale_f32_16x16x128_f8f6f4 v[58:61], v[18:25], v[208:215], 0, v188, v189 op_sel_hi:[0,0,0]
	v_mfma_scale_f32_16x16x128_f8f6f4 v[50:53], v[26:33], v[220:227], 0, v188, v189 op_sel_hi:[0,0,0]
	v_mfma_scale_f32_16x16x128_f8f6f4 v[42:45], v[18:25], v[220:227], 0, v188, v189 op_sel_hi:[0,0,0]
	v_mfma_scale_f32_16x16x128_f8f6f4 v[86:89], v[10:17], v[192:199], 0, v188, v189 op_sel_hi:[0,0,0]
	v_mfma_scale_f32_16x16x128_f8f6f4 v[78:81], v[2:9], v[192:199], 0, v188, v189 op_sel_hi:[0,0,0]
	v_mfma_scale_f32_16x16x128_f8f6f4 v[70:73], v[10:17], v[200:207], 0, v188, v189 op_sel_hi:[0,0,0]
	v_mfma_scale_f32_16x16x128_f8f6f4 v[62:65], v[2:9], v[200:207], 0, v188, v189 op_sel_hi:[0,0,0]
	v_mfma_scale_f32_16x16x128_f8f6f4 v[54:57], v[10:17], v[208:215], 0, v188, v189 op_sel_hi:[0,0,0]
	v_mfma_scale_f32_16x16x128_f8f6f4 v[46:49], v[2:9], v[208:215], 0, v188, v189 op_sel_hi:[0,0,0]
	v_mfma_scale_f32_16x16x128_f8f6f4 v[38:41], v[10:17], v[220:227], 0, v188, v189 op_sel_hi:[0,0,0]
	v_mfma_scale_f32_16x16x128_f8f6f4 v[34:37], v[2:9], v[220:227], 0, v188, v189 op_sel_hi:[0,0,0]
	s_barrier
	s_setprio 0
	s_add_i32 s60, 0, 0x18000
	s_add_i32 s61, 0, 0x1c000
	v_add_u32_e32 v14, s60, v183
	v_add_u32_e32 v30, s61, v183
	ds_read_b128 v[2:5], v14
	ds_read_b128 v[6:9], v14 offset:1024
	ds_read_b128 v[10:13], v14 offset:2048
	ds_read_b128 v[14:17], v14 offset:3072
	ds_read_b128 v[18:21], v30
	ds_read_b128 v[22:25], v30 offset:1024
	ds_read_b128 v[26:29], v30 offset:2048
	ds_read_b128 v[30:33], v30 offset:3072
	s_add_u32 s26, s58, 0x40000
	s_addc_u32 s27, s59, 0
	s_mov_b32 m0, s64
	v_lshl_add_u64 v[216:217], s[26:27], 0, v[164:165]
	ds_read_b128 v[192:195], v187 offset:32768
	ds_read_b128 v[196:199], v187 offset:33792
	ds_read_b128 v[200:203], v187 offset:34816
	ds_read_b128 v[204:207], v187 offset:35840
	ds_read_b128 v[208:211], v187 offset:36864
	ds_read_b128 v[212:215], v187 offset:37888
	ds_read_b128 v[220:223], v187 offset:38912
	ds_read_b128 v[224:227], v187 offset:39936
	global_load_lds_dwordx4 v[216:217], off
	v_lshl_add_u64 v[216:217], s[26:27], 0, v[166:167]
	s_mov_b32 m0, s65
	s_nop 0
	global_load_lds_dwordx4 v[216:217], off
	s_setprio 1
	s_waitcnt vmcnt(8)
	s_waitcnt lgkmcnt(0)
	s_barrier
	v_mfma_scale_f32_16x16x128_f8f6f4 v[158:161], v[2:9], v[192:199], v[158:161], v188, v189 op_sel_hi:[0,0,0]
	v_mfma_scale_f32_16x16x128_f8f6f4 v[154:157], v[10:17], v[192:199], v[154:157], v188, v189 op_sel_hi:[0,0,0]
	v_mfma_scale_f32_16x16x128_f8f6f4 v[146:149], v[2:9], v[200:207], v[146:149], v188, v189 op_sel_hi:[0,0,0]
	v_mfma_scale_f32_16x16x128_f8f6f4 v[138:141], v[10:17], v[200:207], v[138:141], v188, v189 op_sel_hi:[0,0,0]
	v_mfma_scale_f32_16x16x128_f8f6f4 v[130:133], v[2:9], v[208:215], v[130:133], v188, v189 op_sel_hi:[0,0,0]
	v_mfma_scale_f32_16x16x128_f8f6f4 v[122:125], v[10:17], v[208:215], v[122:125], v188, v189 op_sel_hi:[0,0,0]
	v_mfma_scale_f32_16x16x128_f8f6f4 v[114:117], v[2:9], v[220:227], v[114:117], v188, v189 op_sel_hi:[0,0,0]
	v_mfma_scale_f32_16x16x128_f8f6f4 v[106:109], v[10:17], v[220:227], v[106:109], v188, v189 op_sel_hi:[0,0,0]
	v_mfma_scale_f32_16x16x128_f8f6f4 v[150:153], v[18:25], v[192:199], v[150:153], v188, v189 op_sel_hi:[0,0,0]
	v_mfma_scale_f32_16x16x128_f8f6f4 v[142:145], v[26:33], v[192:199], v[142:145], v188, v189 op_sel_hi:[0,0,0]
	v_mfma_scale_f32_16x16x128_f8f6f4 v[134:137], v[18:25], v[200:207], v[134:137], v188, v189 op_sel_hi:[0,0,0]
	v_mfma_scale_f32_16x16x128_f8f6f4 v[126:129], v[26:33], v[200:207], v[126:129], v188, v189 op_sel_hi:[0,0,0]
	v_mfma_scale_f32_16x16x128_f8f6f4 v[118:121], v[18:25], v[208:215], v[118:121], v188, v189 op_sel_hi:[0,0,0]
	v_mfma_scale_f32_16x16x128_f8f6f4 v[110:113], v[26:33], v[208:215], v[110:113], v188, v189 op_sel_hi:[0,0,0]
	v_mfma_scale_f32_16x16x128_f8f6f4 v[102:105], v[18:25], v[220:227], v[102:105], v188, v189 op_sel_hi:[0,0,0]
	v_mfma_scale_f32_16x16x128_f8f6f4 v[98:101], v[26:33], v[220:227], v[98:101], v188, v189 op_sel_hi:[0,0,0]
	s_barrier
	s_setprio 0
	s_add_i32 s26, s60, s35
	v_lshl_add_u64 v[216:217], v[176:177], 0, s[14:15]
	s_mov_b32 m0, s26
	ds_read_b128 v[192:195], v187 offset:49152
	ds_read_b128 v[196:199], v187 offset:50176
	ds_read_b128 v[200:203], v187 offset:51200
	ds_read_b128 v[204:207], v187 offset:52224
	ds_read_b128 v[208:211], v187 offset:53248
	ds_read_b128 v[212:215], v187 offset:54272
	ds_read_b128 v[220:223], v187 offset:55296
	ds_read_b128 v[224:227], v187 offset:56320
	global_load_lds_dwordx4 v[216:217], off
	v_lshl_add_u64 v[216:217], v[176:177], 0, s[16:17]
	s_add_i32 m0, s26, 0x2000
	s_add_i32 s26, s61, s35
	global_load_lds_dwordx4 v[216:217], off
	v_lshl_add_u64 v[216:217], v[176:177], 0, s[20:21]
	s_mov_b32 m0, s26
	v_lshl_add_u64 v[176:177], v[176:177], 0, s[22:23]
	global_load_lds_dwordx4 v[216:217], off
	s_add_i32 m0, s26, 0x2000
	s_nop 0
	global_load_lds_dwordx4 v[176:177], off
	v_lshl_add_u64 v[176:177], v[178:179], 0, s[18:19]
	s_mov_b32 m0, s67
	s_nop 0
	global_load_lds_dwordx4 v[176:177], off
	v_lshl_add_u64 v[176:177], v[180:181], 0, s[18:19]
	s_mov_b32 m0, s68
	s_nop 0
	global_load_lds_dwordx4 v[176:177], off
	s_setprio 1
	s_waitcnt vmcnt(8)
	s_waitcnt lgkmcnt(0)
	s_barrier
	v_mfma_scale_f32_16x16x128_f8f6f4 v[94:97], v[2:9], v[192:199], v[94:97], v188, v189 op_sel_hi:[0,0,0]
	v_mfma_scale_f32_16x16x128_f8f6f4 v[90:93], v[10:17], v[192:199], v[90:93], v188, v189 op_sel_hi:[0,0,0]
	v_mfma_scale_f32_16x16x128_f8f6f4 v[82:85], v[2:9], v[200:207], v[82:85], v188, v189 op_sel_hi:[0,0,0]
	v_mfma_scale_f32_16x16x128_f8f6f4 v[74:77], v[10:17], v[200:207], v[74:77], v188, v189 op_sel_hi:[0,0,0]
	v_mfma_scale_f32_16x16x128_f8f6f4 v[66:69], v[2:9], v[208:215], v[66:69], v188, v189 op_sel_hi:[0,0,0]
	v_mfma_scale_f32_16x16x128_f8f6f4 v[58:61], v[10:17], v[208:215], v[58:61], v188, v189 op_sel_hi:[0,0,0]
	v_mfma_scale_f32_16x16x128_f8f6f4 v[50:53], v[2:9], v[220:227], v[50:53], v188, v189 op_sel_hi:[0,0,0]
	v_mfma_scale_f32_16x16x128_f8f6f4 v[42:45], v[10:17], v[220:227], v[42:45], v188, v189 op_sel_hi:[0,0,0]
	v_mfma_scale_f32_16x16x128_f8f6f4 v[86:89], v[18:25], v[192:199], v[86:89], v188, v189 op_sel_hi:[0,0,0]
	v_mfma_scale_f32_16x16x128_f8f6f4 v[78:81], v[26:33], v[192:199], v[78:81], v188, v189 op_sel_hi:[0,0,0]
	v_mfma_scale_f32_16x16x128_f8f6f4 v[70:73], v[18:25], v[200:207], v[70:73], v188, v189 op_sel_hi:[0,0,0]
	v_mfma_scale_f32_16x16x128_f8f6f4 v[62:65], v[26:33], v[200:207], v[62:65], v188, v189 op_sel_hi:[0,0,0]
	v_mfma_scale_f32_16x16x128_f8f6f4 v[54:57], v[18:25], v[208:215], v[54:57], v188, v189 op_sel_hi:[0,0,0]
	v_mfma_scale_f32_16x16x128_f8f6f4 v[46:49], v[26:33], v[208:215], v[46:49], v188, v189 op_sel_hi:[0,0,0]
	v_mfma_scale_f32_16x16x128_f8f6f4 v[38:41], v[18:25], v[220:227], v[38:41], v188, v189 op_sel_hi:[0,0,0]
	v_mfma_scale_f32_16x16x128_f8f6f4 v[34:37], v[26:33], v[220:227], v[34:37], v188, v189 op_sel_hi:[0,0,0]
	s_barrier
	s_setprio 0
	s_add_i32 s80, s80, 2
	s_add_u32 s74, s74, 0x10000
	s_addc_u32 s75, s75, 0
	s_add_u32 s56, s56, 0x100
	s_addc_u32 s57, s57, 0
	s_cmp_gt_u32 s80, 13
.LBB0_985:
	ds_read_b128 v[26:29], v185
	ds_read_b128 v[30:33], v185 offset:1024
	ds_read_b128 v[18:21], v185 offset:2048
	ds_read_b128 v[22:25], v185 offset:3072
	ds_read_b128 v[10:13], v186
	ds_read_b128 v[14:17], v186 offset:1024
	ds_read_b128 v[2:5], v186 offset:2048
	ds_read_b128 v[6:9], v186 offset:3072
	s_add_u32 s26, s56, 0xfffc0080
	s_addc_u32 s27, s57, -1
	s_cmp_eq_u32 s80, 12
	s_cselect_b32 s59, s45, s27
	s_cselect_b32 s58, s72, s26
	s_cselect_b32 s61, s41, s75
	s_cselect_b32 s60, s73, s74
	v_lshl_add_u64 v[176:177], s[56:57], 0, v[168:169]
	s_add_i32 m0, s55, 0xc000
	ds_read_b128 v[192:195], v187
	ds_read_b128 v[196:199], v187 offset:1024
	ds_read_b128 v[200:203], v187 offset:2048
	ds_read_b128 v[204:207], v187 offset:3072
	ds_read_b128 v[208:211], v187 offset:4096
	ds_read_b128 v[212:215], v187 offset:5120
	ds_read_b128 v[220:223], v187 offset:6144
	ds_read_b128 v[224:227], v187 offset:7168
	global_load_lds_dwordx4 v[176:177], off
	v_lshl_add_u64 v[176:177], s[56:57], 0, v[170:171]
	s_add_i32 m0, s55, 0xe000
	s_nop 0
	global_load_lds_dwordx4 v[176:177], off
	s_setprio 1
	s_waitcnt vmcnt(8)
	s_waitcnt lgkmcnt(0)
	s_barrier
	v_mfma_scale_f32_16x16x128_f8f6f4 v[158:161], v[26:33], v[192:199], v[158:161], v188, v189 op_sel_hi:[0,0,0]
	v_mfma_scale_f32_16x16x128_f8f6f4 v[154:157], v[18:25], v[192:199], v[154:157], v188, v189 op_sel_hi:[0,0,0]
	v_mfma_scale_f32_16x16x128_f8f6f4 v[146:149], v[26:33], v[200:207], v[146:149], v188, v189 op_sel_hi:[0,0,0]
	v_mfma_scale_f32_16x16x128_f8f6f4 v[138:141], v[18:25], v[200:207], v[138:141], v188, v189 op_sel_hi:[0,0,0]
	v_mfma_scale_f32_16x16x128_f8f6f4 v[130:133], v[26:33], v[208:215], v[130:133], v188, v189 op_sel_hi:[0,0,0]
	v_mfma_scale_f32_16x16x128_f8f6f4 v[122:125], v[18:25], v[208:215], v[122:125], v188, v189 op_sel_hi:[0,0,0]
	v_mfma_scale_f32_16x16x128_f8f6f4 v[114:117], v[26:33], v[220:227], v[114:117], v188, v189 op_sel_hi:[0,0,0]
	v_mfma_scale_f32_16x16x128_f8f6f4 v[106:109], v[18:25], v[220:227], v[106:109], v188, v189 op_sel_hi:[0,0,0]
	v_mfma_scale_f32_16x16x128_f8f6f4 v[150:153], v[10:17], v[192:199], v[150:153], v188, v189 op_sel_hi:[0,0,0]
	v_mfma_scale_f32_16x16x128_f8f6f4 v[142:145], v[2:9], v[192:199], v[142:145], v188, v189 op_sel_hi:[0,0,0]
	v_mfma_scale_f32_16x16x128_f8f6f4 v[134:137], v[10:17], v[200:207], v[134:137], v188, v189 op_sel_hi:[0,0,0]
	v_mfma_scale_f32_16x16x128_f8f6f4 v[126:129], v[2:9], v[200:207], v[126:129], v188, v189 op_sel_hi:[0,0,0]
	v_mfma_scale_f32_16x16x128_f8f6f4 v[118:121], v[10:17], v[208:215], v[118:121], v188, v189 op_sel_hi:[0,0,0]
	v_mfma_scale_f32_16x16x128_f8f6f4 v[110:113], v[2:9], v[208:215], v[110:113], v188, v189 op_sel_hi:[0,0,0]
	v_mfma_scale_f32_16x16x128_f8f6f4 v[102:105], v[10:17], v[220:227], v[102:105], v188, v189 op_sel_hi:[0,0,0]
	v_mfma_scale_f32_16x16x128_f8f6f4 v[98:101], v[2:9], v[220:227], v[98:101], v188, v189 op_sel_hi:[0,0,0]
	s_barrier
	s_setprio 0
	s_add_i32 s26, s70, s35
	v_lshl_add_u64 v[176:177], s[60:61], 0, v[162:163]
	s_mov_b32 m0, s26
	ds_read_b128 v[192:195], v187 offset:16384
	ds_read_b128 v[196:199], v187 offset:17408
	ds_read_b128 v[200:203], v187 offset:18432
	ds_read_b128 v[204:207], v187 offset:19456
	ds_read_b128 v[208:211], v187 offset:20480
	ds_read_b128 v[212:215], v187 offset:21504
	ds_read_b128 v[220:223], v187 offset:22528
	ds_read_b128 v[224:227], v187 offset:23552
	global_load_lds_dwordx4 v[176:177], off
	v_lshl_add_u64 v[178:179], v[176:177], 0, s[6:7]
	s_add_i32 m0, s26, 0x2000
	s_add_i32 s26, s71, s35
	global_load_lds_dwordx4 v[178:179], off
	v_lshl_add_u64 v[178:179], v[176:177], 0, s[8:9]
	s_mov_b32 m0, s26
	v_lshl_add_u64 v[180:181], s[58:59], 0, v[166:167]
	global_load_lds_dwordx4 v[178:179], off
	v_lshl_add_u64 v[178:179], v[176:177], 0, s[10:11]
	s_add_i32 m0, s26, 0x2000
	s_nop 0
	global_load_lds_dwordx4 v[178:179], off
	v_lshl_add_u64 v[178:179], s[58:59], 0, v[164:165]
	s_mov_b32 m0, s55
	s_nop 0
	global_load_lds_dwordx4 v[178:179], off
	s_mov_b32 m0, s63
	s_nop 0
	global_load_lds_dwordx4 v[180:181], off
	s_setprio 1
	s_waitcnt vmcnt(8)
	s_waitcnt lgkmcnt(0)
	s_barrier
	v_mfma_scale_f32_16x16x128_f8f6f4 v[94:97], v[26:33], v[192:199], v[94:97], v188, v189 op_sel_hi:[0,0,0]
	v_mfma_scale_f32_16x16x128_f8f6f4 v[90:93], v[18:25], v[192:199], v[90:93], v188, v189 op_sel_hi:[0,0,0]
	v_mfma_scale_f32_16x16x128_f8f6f4 v[82:85], v[26:33], v[200:207], v[82:85], v188, v189 op_sel_hi:[0,0,0]
	v_mfma_scale_f32_16x16x128_f8f6f4 v[74:77], v[18:25], v[200:207], v[74:77], v188, v189 op_sel_hi:[0,0,0]
	v_mfma_scale_f32_16x16x128_f8f6f4 v[66:69], v[26:33], v[208:215], v[66:69], v188, v189 op_sel_hi:[0,0,0]
	v_mfma_scale_f32_16x16x128_f8f6f4 v[58:61], v[18:25], v[208:215], v[58:61], v188, v189 op_sel_hi:[0,0,0]
	v_mfma_scale_f32_16x16x128_f8f6f4 v[50:53], v[26:33], v[220:227], v[50:53], v188, v189 op_sel_hi:[0,0,0]
	v_mfma_scale_f32_16x16x128_f8f6f4 v[42:45], v[18:25], v[220:227], v[42:45], v188, v189 op_sel_hi:[0,0,0]
	v_mfma_scale_f32_16x16x128_f8f6f4 v[86:89], v[10:17], v[192:199], v[86:89], v188, v189 op_sel_hi:[0,0,0]
	v_mfma_scale_f32_16x16x128_f8f6f4 v[78:81], v[2:9], v[192:199], v[78:81], v188, v189 op_sel_hi:[0,0,0]
	v_mfma_scale_f32_16x16x128_f8f6f4 v[70:73], v[10:17], v[200:207], v[70:73], v188, v189 op_sel_hi:[0,0,0]
	v_mfma_scale_f32_16x16x128_f8f6f4 v[62:65], v[2:9], v[200:207], v[62:65], v188, v189 op_sel_hi:[0,0,0]
	v_mfma_scale_f32_16x16x128_f8f6f4 v[54:57], v[10:17], v[208:215], v[54:57], v188, v189 op_sel_hi:[0,0,0]
	v_mfma_scale_f32_16x16x128_f8f6f4 v[46:49], v[2:9], v[208:215], v[46:49], v188, v189 op_sel_hi:[0,0,0]
	v_mfma_scale_f32_16x16x128_f8f6f4 v[38:41], v[10:17], v[220:227], v[38:41], v188, v189 op_sel_hi:[0,0,0]
	v_mfma_scale_f32_16x16x128_f8f6f4 v[34:37], v[2:9], v[220:227], v[34:37], v188, v189 op_sel_hi:[0,0,0]
	s_barrier
	s_setprio 0
	s_add_i32 s60, 0, 0x18000
	s_add_i32 s61, 0, 0x1c000
	v_add_u32_e32 v14, s60, v183
	v_add_u32_e32 v30, s61, v183
	ds_read_b128 v[2:5], v14
	ds_read_b128 v[6:9], v14 offset:1024
	ds_read_b128 v[10:13], v14 offset:2048
	ds_read_b128 v[14:17], v14 offset:3072
	ds_read_b128 v[18:21], v30
	ds_read_b128 v[22:25], v30 offset:1024
	ds_read_b128 v[26:29], v30 offset:2048
	ds_read_b128 v[30:33], v30 offset:3072
	s_add_u32 s26, s58, 0x40000
	s_addc_u32 s27, s59, 0
	s_mov_b32 m0, s64
	v_lshl_add_u64 v[216:217], s[26:27], 0, v[164:165]
	ds_read_b128 v[192:195], v187 offset:32768
	ds_read_b128 v[196:199], v187 offset:33792
	ds_read_b128 v[200:203], v187 offset:34816
	ds_read_b128 v[204:207], v187 offset:35840
	ds_read_b128 v[208:211], v187 offset:36864
	ds_read_b128 v[212:215], v187 offset:37888
	ds_read_b128 v[220:223], v187 offset:38912
	ds_read_b128 v[224:227], v187 offset:39936
	global_load_lds_dwordx4 v[216:217], off
	v_lshl_add_u64 v[216:217], s[26:27], 0, v[166:167]
	s_mov_b32 m0, s65
	s_nop 0
	global_load_lds_dwordx4 v[216:217], off
	s_setprio 1
	s_waitcnt vmcnt(8)
	s_waitcnt lgkmcnt(0)
	s_barrier
	v_mfma_scale_f32_16x16x128_f8f6f4 v[158:161], v[2:9], v[192:199], v[158:161], v188, v189 op_sel_hi:[0,0,0]
	v_mfma_scale_f32_16x16x128_f8f6f4 v[154:157], v[10:17], v[192:199], v[154:157], v188, v189 op_sel_hi:[0,0,0]
	v_mfma_scale_f32_16x16x128_f8f6f4 v[146:149], v[2:9], v[200:207], v[146:149], v188, v189 op_sel_hi:[0,0,0]
	v_mfma_scale_f32_16x16x128_f8f6f4 v[138:141], v[10:17], v[200:207], v[138:141], v188, v189 op_sel_hi:[0,0,0]
	v_mfma_scale_f32_16x16x128_f8f6f4 v[130:133], v[2:9], v[208:215], v[130:133], v188, v189 op_sel_hi:[0,0,0]
	v_mfma_scale_f32_16x16x128_f8f6f4 v[122:125], v[10:17], v[208:215], v[122:125], v188, v189 op_sel_hi:[0,0,0]
	v_mfma_scale_f32_16x16x128_f8f6f4 v[114:117], v[2:9], v[220:227], v[114:117], v188, v189 op_sel_hi:[0,0,0]
	v_mfma_scale_f32_16x16x128_f8f6f4 v[106:109], v[10:17], v[220:227], v[106:109], v188, v189 op_sel_hi:[0,0,0]
	v_mfma_scale_f32_16x16x128_f8f6f4 v[150:153], v[18:25], v[192:199], v[150:153], v188, v189 op_sel_hi:[0,0,0]
	v_mfma_scale_f32_16x16x128_f8f6f4 v[142:145], v[26:33], v[192:199], v[142:145], v188, v189 op_sel_hi:[0,0,0]
	v_mfma_scale_f32_16x16x128_f8f6f4 v[134:137], v[18:25], v[200:207], v[134:137], v188, v189 op_sel_hi:[0,0,0]
	v_mfma_scale_f32_16x16x128_f8f6f4 v[126:129], v[26:33], v[200:207], v[126:129], v188, v189 op_sel_hi:[0,0,0]
	v_mfma_scale_f32_16x16x128_f8f6f4 v[118:121], v[18:25], v[208:215], v[118:121], v188, v189 op_sel_hi:[0,0,0]
	v_mfma_scale_f32_16x16x128_f8f6f4 v[110:113], v[26:33], v[208:215], v[110:113], v188, v189 op_sel_hi:[0,0,0]
	v_mfma_scale_f32_16x16x128_f8f6f4 v[102:105], v[18:25], v[220:227], v[102:105], v188, v189 op_sel_hi:[0,0,0]
	v_mfma_scale_f32_16x16x128_f8f6f4 v[98:101], v[26:33], v[220:227], v[98:101], v188, v189 op_sel_hi:[0,0,0]
	s_barrier
	s_setprio 0
	s_add_i32 s26, s60, s35
	v_lshl_add_u64 v[216:217], v[176:177], 0, s[14:15]
	s_mov_b32 m0, s26
	ds_read_b128 v[192:195], v187 offset:49152
	ds_read_b128 v[196:199], v187 offset:50176
	ds_read_b128 v[200:203], v187 offset:51200
	ds_read_b128 v[204:207], v187 offset:52224
	ds_read_b128 v[208:211], v187 offset:53248
	ds_read_b128 v[212:215], v187 offset:54272
	ds_read_b128 v[220:223], v187 offset:55296
	ds_read_b128 v[224:227], v187 offset:56320
	global_load_lds_dwordx4 v[216:217], off
	v_lshl_add_u64 v[216:217], v[176:177], 0, s[16:17]
	s_add_i32 m0, s26, 0x2000
	s_add_i32 s26, s61, s35
	global_load_lds_dwordx4 v[216:217], off
	v_lshl_add_u64 v[216:217], v[176:177], 0, s[20:21]
	s_mov_b32 m0, s26
	v_lshl_add_u64 v[176:177], v[176:177], 0, s[22:23]
	global_load_lds_dwordx4 v[216:217], off
	s_add_i32 m0, s26, 0x2000
	s_nop 0
	global_load_lds_dwordx4 v[176:177], off
	v_lshl_add_u64 v[176:177], v[178:179], 0, s[18:19]
	s_mov_b32 m0, s67
	s_nop 0
	global_load_lds_dwordx4 v[176:177], off
	v_lshl_add_u64 v[176:177], v[180:181], 0, s[18:19]
	s_mov_b32 m0, s68
	s_nop 0
	global_load_lds_dwordx4 v[176:177], off
	s_setprio 1
	s_waitcnt vmcnt(8)
	s_waitcnt lgkmcnt(0)
	s_barrier
	v_mfma_scale_f32_16x16x128_f8f6f4 v[94:97], v[2:9], v[192:199], v[94:97], v188, v189 op_sel_hi:[0,0,0]
	v_mfma_scale_f32_16x16x128_f8f6f4 v[90:93], v[10:17], v[192:199], v[90:93], v188, v189 op_sel_hi:[0,0,0]
	v_mfma_scale_f32_16x16x128_f8f6f4 v[82:85], v[2:9], v[200:207], v[82:85], v188, v189 op_sel_hi:[0,0,0]
	v_mfma_scale_f32_16x16x128_f8f6f4 v[74:77], v[10:17], v[200:207], v[74:77], v188, v189 op_sel_hi:[0,0,0]
	v_mfma_scale_f32_16x16x128_f8f6f4 v[66:69], v[2:9], v[208:215], v[66:69], v188, v189 op_sel_hi:[0,0,0]
	v_mfma_scale_f32_16x16x128_f8f6f4 v[58:61], v[10:17], v[208:215], v[58:61], v188, v189 op_sel_hi:[0,0,0]
	v_mfma_scale_f32_16x16x128_f8f6f4 v[50:53], v[2:9], v[220:227], v[50:53], v188, v189 op_sel_hi:[0,0,0]
	v_mfma_scale_f32_16x16x128_f8f6f4 v[42:45], v[10:17], v[220:227], v[42:45], v188, v189 op_sel_hi:[0,0,0]
	v_mfma_scale_f32_16x16x128_f8f6f4 v[86:89], v[18:25], v[192:199], v[86:89], v188, v189 op_sel_hi:[0,0,0]
	v_mfma_scale_f32_16x16x128_f8f6f4 v[78:81], v[26:33], v[192:199], v[78:81], v188, v189 op_sel_hi:[0,0,0]
	v_mfma_scale_f32_16x16x128_f8f6f4 v[70:73], v[18:25], v[200:207], v[70:73], v188, v189 op_sel_hi:[0,0,0]
	v_mfma_scale_f32_16x16x128_f8f6f4 v[62:65], v[26:33], v[200:207], v[62:65], v188, v189 op_sel_hi:[0,0,0]
	v_mfma_scale_f32_16x16x128_f8f6f4 v[54:57], v[18:25], v[208:215], v[54:57], v188, v189 op_sel_hi:[0,0,0]
	v_mfma_scale_f32_16x16x128_f8f6f4 v[46:49], v[26:33], v[208:215], v[46:49], v188, v189 op_sel_hi:[0,0,0]
	v_mfma_scale_f32_16x16x128_f8f6f4 v[38:41], v[18:25], v[220:227], v[38:41], v188, v189 op_sel_hi:[0,0,0]
	v_mfma_scale_f32_16x16x128_f8f6f4 v[34:37], v[26:33], v[220:227], v[34:37], v188, v189 op_sel_hi:[0,0,0]
	s_barrier
	s_setprio 0
	s_add_i32 s80, s80, 2
	s_add_u32 s74, s74, 0x10000
	s_addc_u32 s75, s75, 0
	s_add_u32 s56, s56, 0x100
	s_addc_u32 s57, s57, 0
	s_cmp_gt_u32 s80, 13
	s_cbranch_scc0 .LBB0_985
	s_and_b64 vcc, exec, s[24:25]
	s_cbranch_vccz .LBB0_988
	s_barrier
	s_setprio 3

.LBB0_1191:
	s_ashr_i32 s45, s44, 31
	s_lshl_b64 s[26:27], s[44:45], 19
	s_add_u32 s50, s4, s26
	s_addc_u32 s51, s5, s27
	s_and_b64 s[26:27], s[0:1], exec
	s_cselect_b32 s45, s51, s59
	s_cselect_b32 s69, s50, s58
	s_ashr_i32 s41, s40, 31
	s_lshl_b64 s[26:27], s[40:41], 19
	s_add_u32 s52, s3, s26
	s_addc_u32 s53, s33, s27
	s_and_b64 s[26:27], s[0:1], exec
	s_cselect_b32 s41, s53, s57
	s_cselect_b32 s70, s52, s56
	s_add_u32 s71, s56, 0x10000
	s_addc_u32 s72, s57, 0
	s_add_u32 s56, s58, 0x40080
	s_addc_u32 s57, s59, 0
	s_mov_b32 s73, -2
	ds_read_b128 v[66:69], v199
	ds_read_b128 v[70:73], v199 offset:1024
	ds_read_b128 v[82:85], v199 offset:2048
	ds_read_b128 v[86:89], v199 offset:3072
	ds_read_b128 v[146:149], v200
	ds_read_b128 v[150:153], v200 offset:1024
	ds_read_b128 v[154:157], v200 offset:2048
	ds_read_b128 v[158:161], v200 offset:3072
	s_add_u32 s26, s56, 0xfffc0080
	s_addc_u32 s27, s57, -1
	s_cmp_eq_u32 s73, 12
	s_cselect_b32 s59, s45, s27
	s_cselect_b32 s58, s69, s26
	s_cselect_b32 s27, s41, s72
	s_cselect_b32 s26, s70, s71
	v_lshl_add_u64 v[214:215], s[56:57], 0, v[176:177]
	s_add_i32 m0, s55, 0xc000
	ds_read_b128 v[162:165], v201
	ds_read_b128 v[166:169], v201 offset:1024
	ds_read_b128 v[184:187], v201 offset:2048
	ds_read_b128 v[188:191], v201 offset:3072
	ds_read_b128 v[192:195], v201 offset:4096
	ds_read_b128 v[202:205], v201 offset:5120
	ds_read_b128 v[206:209], v201 offset:6144
	ds_read_b128 v[210:213], v201 offset:7168
	global_load_lds_dwordx4 v[214:215], off
	v_lshl_add_u64 v[214:215], s[56:57], 0, v[178:179]
	s_add_i32 m0, s55, 0xe000
	s_nop 0
	global_load_lds_dwordx4 v[214:215], off
	s_setprio 1
	s_waitcnt vmcnt(8)
	s_waitcnt lgkmcnt(0)
	s_barrier
	v_mfma_f32_16x16x32_bf16 v[142:145], v[66:69], v[162:165], 0
	v_mfma_f32_16x16x32_bf16 v[138:141], v[82:85], v[162:165], 0
	v_mfma_f32_16x16x32_bf16 v[126:129], v[66:69], v[184:187], 0
	v_mfma_f32_16x16x32_bf16 v[122:125], v[82:85], v[184:187], 0
	v_mfma_f32_16x16x32_bf16 v[110:113], v[66:69], v[192:195], 0
	v_mfma_f32_16x16x32_bf16 v[106:109], v[82:85], v[192:195], 0
	v_mfma_f32_16x16x32_bf16 v[94:97], v[66:69], v[206:209], 0
	v_mfma_f32_16x16x32_bf16 v[90:93], v[82:85], v[206:209], 0
	v_mfma_f32_16x16x32_bf16 v[142:145], v[70:73], v[166:169], v[142:145]
	v_mfma_f32_16x16x32_bf16 v[138:141], v[86:89], v[166:169], v[138:141]
	v_mfma_f32_16x16x32_bf16 v[126:129], v[70:73], v[188:191], v[126:129]
	v_mfma_f32_16x16x32_bf16 v[122:125], v[86:89], v[188:191], v[122:125]
	v_mfma_f32_16x16x32_bf16 v[110:113], v[70:73], v[202:205], v[110:113]
	v_mfma_f32_16x16x32_bf16 v[106:109], v[86:89], v[202:205], v[106:109]
	v_mfma_f32_16x16x32_bf16 v[94:97], v[70:73], v[210:213], v[94:97]
	v_mfma_f32_16x16x32_bf16 v[90:93], v[86:89], v[210:213], v[90:93]
	v_mfma_f32_16x16x32_bf16 v[134:137], v[146:149], v[162:165], 0
	v_mfma_f32_16x16x32_bf16 v[130:133], v[154:157], v[162:165], 0
	v_mfma_f32_16x16x32_bf16 v[118:121], v[146:149], v[184:187], 0
	v_mfma_f32_16x16x32_bf16 v[114:117], v[154:157], v[184:187], 0
	v_mfma_f32_16x16x32_bf16 v[102:105], v[146:149], v[192:195], 0
	v_mfma_f32_16x16x32_bf16 v[98:101], v[154:157], v[192:195], 0
	v_mfma_f32_16x16x32_bf16 v[78:81], v[146:149], v[206:209], 0
	v_mfma_f32_16x16x32_bf16 v[74:77], v[154:157], v[206:209], 0
	v_mfma_f32_16x16x32_bf16 v[134:137], v[150:153], v[166:169], v[134:137]
	v_mfma_f32_16x16x32_bf16 v[130:133], v[158:161], v[166:169], v[130:133]
	v_mfma_f32_16x16x32_bf16 v[118:121], v[150:153], v[188:191], v[118:121]
	v_mfma_f32_16x16x32_bf16 v[114:117], v[158:161], v[188:191], v[114:117]
	v_mfma_f32_16x16x32_bf16 v[102:105], v[150:153], v[202:205], v[102:105]
	v_mfma_f32_16x16x32_bf16 v[98:101], v[158:161], v[202:205], v[98:101]
	v_mfma_f32_16x16x32_bf16 v[78:81], v[150:153], v[210:213], v[78:81]
	v_mfma_f32_16x16x32_bf16 v[74:77], v[158:161], v[210:213], v[74:77]
	s_barrier
	s_setprio 0
	v_lshl_add_u64 v[214:215], s[26:27], 0, v[170:171]
	s_add_i32 s26, s67, s35
	s_mov_b32 m0, s26
	ds_read_b128 v[162:165], v201 offset:16384
	ds_read_b128 v[166:169], v201 offset:17408
	ds_read_b128 v[184:187], v201 offset:18432
	ds_read_b128 v[188:191], v201 offset:19456
	ds_read_b128 v[192:195], v201 offset:20480
	ds_read_b128 v[202:205], v201 offset:21504
	ds_read_b128 v[206:209], v201 offset:22528
	ds_read_b128 v[210:213], v201 offset:23552
	global_load_lds_dwordx4 v[214:215], off
	v_lshl_add_u64 v[216:217], v[214:215], 0, s[6:7]
	s_add_i32 m0, s26, 0x2000
	s_add_i32 s26, s68, s35
	global_load_lds_dwordx4 v[216:217], off
	v_lshl_add_u64 v[216:217], v[214:215], 0, s[10:11]
	s_mov_b32 m0, s26
	v_lshl_add_u64 v[220:221], s[58:59], 0, v[174:175]
	global_load_lds_dwordx4 v[216:217], off
	v_lshl_add_u64 v[216:217], v[214:215], 0, s[12:13]
	s_add_i32 m0, s26, 0x2000
	s_nop 0
	global_load_lds_dwordx4 v[216:217], off
	v_lshl_add_u64 v[216:217], s[58:59], 0, v[172:173]
	s_mov_b32 m0, s55
	s_nop 0
	global_load_lds_dwordx4 v[216:217], off
	s_mov_b32 m0, s60
	s_nop 0
	global_load_lds_dwordx4 v[220:221], off
	s_setprio 1
	s_waitcnt vmcnt(8)
	s_waitcnt lgkmcnt(0)
	s_barrier
	v_mfma_f32_16x16x32_bf16 v[62:65], v[66:69], v[162:165], 0
	v_mfma_f32_16x16x32_bf16 v[58:61], v[82:85], v[162:165], 0
	v_mfma_f32_16x16x32_bf16 v[46:49], v[66:69], v[184:187], 0
	v_mfma_f32_16x16x32_bf16 v[42:45], v[82:85], v[184:187], 0
	v_mfma_f32_16x16x32_bf16 v[30:33], v[66:69], v[192:195], 0
	v_mfma_f32_16x16x32_bf16 v[26:29], v[82:85], v[192:195], 0
	v_mfma_f32_16x16x32_bf16 v[14:17], v[66:69], v[206:209], 0
	v_mfma_f32_16x16x32_bf16 v[10:13], v[82:85], v[206:209], 0
	v_mfma_f32_16x16x32_bf16 v[62:65], v[70:73], v[166:169], v[62:65]
	v_mfma_f32_16x16x32_bf16 v[58:61], v[86:89], v[166:169], v[58:61]
	v_mfma_f32_16x16x32_bf16 v[46:49], v[70:73], v[188:191], v[46:49]
	v_mfma_f32_16x16x32_bf16 v[42:45], v[86:89], v[188:191], v[42:45]
	v_mfma_f32_16x16x32_bf16 v[30:33], v[70:73], v[202:205], v[30:33]
	v_mfma_f32_16x16x32_bf16 v[26:29], v[86:89], v[202:205], v[26:29]
	v_mfma_f32_16x16x32_bf16 v[14:17], v[70:73], v[210:213], v[14:17]
	v_mfma_f32_16x16x32_bf16 v[10:13], v[86:89], v[210:213], v[10:13]
	v_mfma_f32_16x16x32_bf16 v[54:57], v[146:149], v[162:165], 0
	v_mfma_f32_16x16x32_bf16 v[50:53], v[154:157], v[162:165], 0
	v_mfma_f32_16x16x32_bf16 v[38:41], v[146:149], v[184:187], 0
	v_mfma_f32_16x16x32_bf16 v[34:37], v[154:157], v[184:187], 0
	v_mfma_f32_16x16x32_bf16 v[22:25], v[146:149], v[192:195], 0
	v_mfma_f32_16x16x32_bf16 v[18:21], v[154:157], v[192:195], 0
	v_mfma_f32_16x16x32_bf16 v[6:9], v[146:149], v[206:209], 0
	v_mfma_f32_16x16x32_bf16 v[2:5], v[154:157], v[206:209], 0
	v_mfma_f32_16x16x32_bf16 v[54:57], v[150:153], v[166:169], v[54:57]
	v_mfma_f32_16x16x32_bf16 v[50:53], v[158:161], v[166:169], v[50:53]
	v_mfma_f32_16x16x32_bf16 v[38:41], v[150:153], v[188:191], v[38:41]
	v_mfma_f32_16x16x32_bf16 v[34:37], v[158:161], v[188:191], v[34:37]
	v_mfma_f32_16x16x32_bf16 v[22:25], v[150:153], v[202:205], v[22:25]
	v_mfma_f32_16x16x32_bf16 v[18:21], v[158:161], v[202:205], v[18:21]
	v_mfma_f32_16x16x32_bf16 v[6:9], v[150:153], v[210:213], v[6:9]
	v_mfma_f32_16x16x32_bf16 v[2:5], v[158:161], v[210:213], v[2:5]
	s_barrier
	s_setprio 0
	s_add_i32 s74, 0, 0x18000
	s_add_i32 s75, 0, 0x1c000
	v_add_u32_e32 v86, s74, v197
	v_add_u32_e32 v158, s75, v197
	ds_read_b128 v[66:69], v86
	ds_read_b128 v[70:73], v86 offset:1024
	ds_read_b128 v[82:85], v86 offset:2048
	ds_read_b128 v[86:89], v86 offset:3072
	ds_read_b128 v[146:149], v158
	ds_read_b128 v[150:153], v158 offset:1024
	ds_read_b128 v[154:157], v158 offset:2048
	ds_read_b128 v[158:161], v158 offset:3072
	s_add_u32 s26, s58, 0x40000
	s_addc_u32 s27, s59, 0
	s_mov_b32 m0, s61
	v_lshl_add_u64 v[222:223], s[26:27], 0, v[172:173]
	ds_read_b128 v[162:165], v201 offset:32768
	ds_read_b128 v[166:169], v201 offset:33792
	ds_read_b128 v[184:187], v201 offset:34816
	ds_read_b128 v[188:191], v201 offset:35840
	ds_read_b128 v[192:195], v201 offset:36864
	ds_read_b128 v[202:205], v201 offset:37888
	ds_read_b128 v[206:209], v201 offset:38912
	ds_read_b128 v[210:213], v201 offset:39936
	global_load_lds_dwordx4 v[222:223], off
	v_lshl_add_u64 v[222:223], s[26:27], 0, v[174:175]
	s_mov_b32 m0, s62
	s_nop 0
	global_load_lds_dwordx4 v[222:223], off
	s_setprio 1
	s_waitcnt vmcnt(8)
	s_waitcnt lgkmcnt(0)
	s_barrier
	v_mfma_f32_16x16x32_bf16 v[142:145], v[66:69], v[162:165], v[142:145]
	v_mfma_f32_16x16x32_bf16 v[138:141], v[82:85], v[162:165], v[138:141]
	v_mfma_f32_16x16x32_bf16 v[126:129], v[66:69], v[184:187], v[126:129]
	v_mfma_f32_16x16x32_bf16 v[122:125], v[82:85], v[184:187], v[122:125]
	v_mfma_f32_16x16x32_bf16 v[110:113], v[66:69], v[192:195], v[110:113]
	v_mfma_f32_16x16x32_bf16 v[106:109], v[82:85], v[192:195], v[106:109]
	v_mfma_f32_16x16x32_bf16 v[94:97], v[66:69], v[206:209], v[94:97]
	v_mfma_f32_16x16x32_bf16 v[90:93], v[82:85], v[206:209], v[90:93]
	v_mfma_f32_16x16x32_bf16 v[142:145], v[70:73], v[166:169], v[142:145]
	v_mfma_f32_16x16x32_bf16 v[138:141], v[86:89], v[166:169], v[138:141]
	v_mfma_f32_16x16x32_bf16 v[126:129], v[70:73], v[188:191], v[126:129]
	v_mfma_f32_16x16x32_bf16 v[122:125], v[86:89], v[188:191], v[122:125]
	v_mfma_f32_16x16x32_bf16 v[110:113], v[70:73], v[202:205], v[110:113]
	v_mfma_f32_16x16x32_bf16 v[106:109], v[86:89], v[202:205], v[106:109]
	v_mfma_f32_16x16x32_bf16 v[94:97], v[70:73], v[210:213], v[94:97]
	v_mfma_f32_16x16x32_bf16 v[90:93], v[86:89], v[210:213], v[90:93]
	v_mfma_f32_16x16x32_bf16 v[134:137], v[146:149], v[162:165], v[134:137]
	v_mfma_f32_16x16x32_bf16 v[130:133], v[154:157], v[162:165], v[130:133]
	v_mfma_f32_16x16x32_bf16 v[118:121], v[146:149], v[184:187], v[118:121]
	v_mfma_f32_16x16x32_bf16 v[114:117], v[154:157], v[184:187], v[114:117]
	v_mfma_f32_16x16x32_bf16 v[102:105], v[146:149], v[192:195], v[102:105]
	v_mfma_f32_16x16x32_bf16 v[98:101], v[154:157], v[192:195], v[98:101]
	v_mfma_f32_16x16x32_bf16 v[78:81], v[146:149], v[206:209], v[78:81]
	v_mfma_f32_16x16x32_bf16 v[74:77], v[154:157], v[206:209], v[74:77]
	v_mfma_f32_16x16x32_bf16 v[134:137], v[150:153], v[166:169], v[134:137]
	v_mfma_f32_16x16x32_bf16 v[130:133], v[158:161], v[166:169], v[130:133]
	v_mfma_f32_16x16x32_bf16 v[118:121], v[150:153], v[188:191], v[118:121]
	v_mfma_f32_16x16x32_bf16 v[114:117], v[158:161], v[188:191], v[114:117]
	v_mfma_f32_16x16x32_bf16 v[102:105], v[150:153], v[202:205], v[102:105]
	v_mfma_f32_16x16x32_bf16 v[98:101], v[158:161], v[202:205], v[98:101]
	v_mfma_f32_16x16x32_bf16 v[78:81], v[150:153], v[210:213], v[78:81]
	v_mfma_f32_16x16x32_bf16 v[74:77], v[158:161], v[210:213], v[74:77]
	s_barrier
	s_setprio 0
	s_add_i32 s26, s74, s35
	v_lshl_add_u64 v[222:223], v[214:215], 0, s[16:17]
	s_mov_b32 m0, s26
	ds_read_b128 v[162:165], v201 offset:49152
	ds_read_b128 v[166:169], v201 offset:50176
	ds_read_b128 v[184:187], v201 offset:51200
	ds_read_b128 v[188:191], v201 offset:52224
	ds_read_b128 v[192:195], v201 offset:53248
	ds_read_b128 v[202:205], v201 offset:54272
	ds_read_b128 v[206:209], v201 offset:55296
	ds_read_b128 v[210:213], v201 offset:56320
	global_load_lds_dwordx4 v[222:223], off
	v_lshl_add_u64 v[222:223], v[214:215], 0, s[18:19]
	s_add_i32 m0, s26, 0x2000
	s_add_i32 s26, s75, s35
	global_load_lds_dwordx4 v[222:223], off
	v_lshl_add_u64 v[222:223], v[214:215], 0, s[22:23]
	s_mov_b32 m0, s26
	v_lshl_add_u64 v[214:215], v[214:215], 0, s[24:25]
	global_load_lds_dwordx4 v[222:223], off
	s_add_i32 m0, s26, 0x2000
	s_nop 0
	global_load_lds_dwordx4 v[214:215], off
	v_lshl_add_u64 v[214:215], v[216:217], 0, s[20:21]
	s_mov_b32 m0, s64
	s_nop 0
	global_load_lds_dwordx4 v[214:215], off
	v_lshl_add_u64 v[214:215], v[220:221], 0, s[20:21]
	s_mov_b32 m0, s65
	s_nop 0
	global_load_lds_dwordx4 v[214:215], off
	s_setprio 1
	s_waitcnt vmcnt(8)
	s_waitcnt lgkmcnt(0)
	s_barrier
	v_mfma_f32_16x16x32_bf16 v[62:65], v[66:69], v[162:165], v[62:65]
	v_mfma_f32_16x16x32_bf16 v[58:61], v[82:85], v[162:165], v[58:61]
	v_mfma_f32_16x16x32_bf16 v[46:49], v[66:69], v[184:187], v[46:49]
	v_mfma_f32_16x16x32_bf16 v[42:45], v[82:85], v[184:187], v[42:45]
	v_mfma_f32_16x16x32_bf16 v[30:33], v[66:69], v[192:195], v[30:33]
	v_mfma_f32_16x16x32_bf16 v[26:29], v[82:85], v[192:195], v[26:29]
	v_mfma_f32_16x16x32_bf16 v[14:17], v[66:69], v[206:209], v[14:17]
	v_mfma_f32_16x16x32_bf16 v[10:13], v[82:85], v[206:209], v[10:13]
	v_mfma_f32_16x16x32_bf16 v[62:65], v[70:73], v[166:169], v[62:65]
	v_mfma_f32_16x16x32_bf16 v[58:61], v[86:89], v[166:169], v[58:61]
	v_mfma_f32_16x16x32_bf16 v[46:49], v[70:73], v[188:191], v[46:49]
	v_mfma_f32_16x16x32_bf16 v[42:45], v[86:89], v[188:191], v[42:45]
	v_mfma_f32_16x16x32_bf16 v[30:33], v[70:73], v[202:205], v[30:33]
	v_mfma_f32_16x16x32_bf16 v[26:29], v[86:89], v[202:205], v[26:29]
	v_mfma_f32_16x16x32_bf16 v[14:17], v[70:73], v[210:213], v[14:17]
	v_mfma_f32_16x16x32_bf16 v[10:13], v[86:89], v[210:213], v[10:13]
	v_mfma_f32_16x16x32_bf16 v[54:57], v[146:149], v[162:165], v[54:57]
	v_mfma_f32_16x16x32_bf16 v[50:53], v[154:157], v[162:165], v[50:53]
	v_mfma_f32_16x16x32_bf16 v[38:41], v[146:149], v[184:187], v[38:41]
	v_mfma_f32_16x16x32_bf16 v[34:37], v[154:157], v[184:187], v[34:37]
	v_mfma_f32_16x16x32_bf16 v[22:25], v[146:149], v[192:195], v[22:25]
	v_mfma_f32_16x16x32_bf16 v[18:21], v[154:157], v[192:195], v[18:21]
	v_mfma_f32_16x16x32_bf16 v[6:9], v[146:149], v[206:209], v[6:9]
	v_mfma_f32_16x16x32_bf16 v[2:5], v[154:157], v[206:209], v[2:5]
	v_mfma_f32_16x16x32_bf16 v[54:57], v[150:153], v[166:169], v[54:57]
	v_mfma_f32_16x16x32_bf16 v[50:53], v[158:161], v[166:169], v[50:53]
	v_mfma_f32_16x16x32_bf16 v[38:41], v[150:153], v[188:191], v[38:41]
	v_mfma_f32_16x16x32_bf16 v[34:37], v[158:161], v[188:191], v[34:37]
	v_mfma_f32_16x16x32_bf16 v[22:25], v[150:153], v[202:205], v[22:25]
	v_mfma_f32_16x16x32_bf16 v[18:21], v[158:161], v[202:205], v[18:21]
	v_mfma_f32_16x16x32_bf16 v[6:9], v[150:153], v[210:213], v[6:9]
	v_mfma_f32_16x16x32_bf16 v[2:5], v[158:161], v[210:213], v[2:5]
	s_barrier
	s_setprio 0
	s_add_i32 s73, s73, 2
	s_add_u32 s71, s71, 0x10000
	s_addc_u32 s72, s72, 0
	s_add_u32 s56, s56, 0x100
	s_addc_u32 s57, s57, 0
	s_cmp_gt_u32 s73, 13
.LBB0_1192:
	ds_read_b128 v[66:69], v199
	ds_read_b128 v[70:73], v199 offset:1024
	ds_read_b128 v[82:85], v199 offset:2048
	ds_read_b128 v[86:89], v199 offset:3072
	ds_read_b128 v[146:149], v200
	ds_read_b128 v[150:153], v200 offset:1024
	ds_read_b128 v[154:157], v200 offset:2048
	ds_read_b128 v[158:161], v200 offset:3072
	s_add_u32 s26, s56, 0xfffc0080
	s_addc_u32 s27, s57, -1
	s_cmp_eq_u32 s73, 12
	s_cselect_b32 s59, s45, s27
	s_cselect_b32 s58, s69, s26
	s_cselect_b32 s27, s41, s72
	s_cselect_b32 s26, s70, s71
	v_lshl_add_u64 v[214:215], s[56:57], 0, v[176:177]
	s_add_i32 m0, s55, 0xc000
	ds_read_b128 v[162:165], v201
	ds_read_b128 v[166:169], v201 offset:1024
	ds_read_b128 v[184:187], v201 offset:2048
	ds_read_b128 v[188:191], v201 offset:3072
	ds_read_b128 v[192:195], v201 offset:4096
	ds_read_b128 v[202:205], v201 offset:5120
	ds_read_b128 v[206:209], v201 offset:6144
	ds_read_b128 v[210:213], v201 offset:7168
	global_load_lds_dwordx4 v[214:215], off
	v_lshl_add_u64 v[214:215], s[56:57], 0, v[178:179]
	s_add_i32 m0, s55, 0xe000
	s_nop 0
	global_load_lds_dwordx4 v[214:215], off
	s_setprio 1
	s_waitcnt vmcnt(8)
	s_waitcnt lgkmcnt(0)
	s_barrier
	v_mfma_f32_16x16x32_bf16 v[142:145], v[66:69], v[162:165], v[142:145]
	v_mfma_f32_16x16x32_bf16 v[138:141], v[82:85], v[162:165], v[138:141]
	v_mfma_f32_16x16x32_bf16 v[126:129], v[66:69], v[184:187], v[126:129]
	v_mfma_f32_16x16x32_bf16 v[122:125], v[82:85], v[184:187], v[122:125]
	v_mfma_f32_16x16x32_bf16 v[110:113], v[66:69], v[192:195], v[110:113]
	v_mfma_f32_16x16x32_bf16 v[106:109], v[82:85], v[192:195], v[106:109]
	v_mfma_f32_16x16x32_bf16 v[94:97], v[66:69], v[206:209], v[94:97]
	v_mfma_f32_16x16x32_bf16 v[90:93], v[82:85], v[206:209], v[90:93]
	v_mfma_f32_16x16x32_bf16 v[142:145], v[70:73], v[166:169], v[142:145]
	v_mfma_f32_16x16x32_bf16 v[138:141], v[86:89], v[166:169], v[138:141]
	v_mfma_f32_16x16x32_bf16 v[126:129], v[70:73], v[188:191], v[126:129]
	v_mfma_f32_16x16x32_bf16 v[122:125], v[86:89], v[188:191], v[122:125]
	v_mfma_f32_16x16x32_bf16 v[110:113], v[70:73], v[202:205], v[110:113]
	v_mfma_f32_16x16x32_bf16 v[106:109], v[86:89], v[202:205], v[106:109]
	v_mfma_f32_16x16x32_bf16 v[94:97], v[70:73], v[210:213], v[94:97]
	v_mfma_f32_16x16x32_bf16 v[90:93], v[86:89], v[210:213], v[90:93]
	v_mfma_f32_16x16x32_bf16 v[134:137], v[146:149], v[162:165], v[134:137]
	v_mfma_f32_16x16x32_bf16 v[130:133], v[154:157], v[162:165], v[130:133]
	v_mfma_f32_16x16x32_bf16 v[118:121], v[146:149], v[184:187], v[118:121]
	v_mfma_f32_16x16x32_bf16 v[114:117], v[154:157], v[184:187], v[114:117]
	v_mfma_f32_16x16x32_bf16 v[102:105], v[146:149], v[192:195], v[102:105]
	v_mfma_f32_16x16x32_bf16 v[98:101], v[154:157], v[192:195], v[98:101]
	v_mfma_f32_16x16x32_bf16 v[78:81], v[146:149], v[206:209], v[78:81]
	v_mfma_f32_16x16x32_bf16 v[74:77], v[154:157], v[206:209], v[74:77]
	v_mfma_f32_16x16x32_bf16 v[134:137], v[150:153], v[166:169], v[134:137]
	v_mfma_f32_16x16x32_bf16 v[130:133], v[158:161], v[166:169], v[130:133]
	v_mfma_f32_16x16x32_bf16 v[118:121], v[150:153], v[188:191], v[118:121]
	v_mfma_f32_16x16x32_bf16 v[114:117], v[158:161], v[188:191], v[114:117]
	v_mfma_f32_16x16x32_bf16 v[102:105], v[150:153], v[202:205], v[102:105]
	v_mfma_f32_16x16x32_bf16 v[98:101], v[158:161], v[202:205], v[98:101]
	v_mfma_f32_16x16x32_bf16 v[78:81], v[150:153], v[210:213], v[78:81]
	v_mfma_f32_16x16x32_bf16 v[74:77], v[158:161], v[210:213], v[74:77]
	s_barrier
	s_setprio 0
	v_lshl_add_u64 v[214:215], s[26:27], 0, v[170:171]
	s_add_i32 s26, s67, s35
	s_mov_b32 m0, s26
	ds_read_b128 v[162:165], v201 offset:16384
	ds_read_b128 v[166:169], v201 offset:17408
	ds_read_b128 v[184:187], v201 offset:18432
	ds_read_b128 v[188:191], v201 offset:19456
	ds_read_b128 v[192:195], v201 offset:20480
	ds_read_b128 v[202:205], v201 offset:21504
	ds_read_b128 v[206:209], v201 offset:22528
	ds_read_b128 v[210:213], v201 offset:23552
	global_load_lds_dwordx4 v[214:215], off
	v_lshl_add_u64 v[216:217], v[214:215], 0, s[6:7]
	s_add_i32 m0, s26, 0x2000
	s_add_i32 s26, s68, s35
	global_load_lds_dwordx4 v[216:217], off
	v_lshl_add_u64 v[216:217], v[214:215], 0, s[10:11]
	s_mov_b32 m0, s26
	v_lshl_add_u64 v[220:221], s[58:59], 0, v[174:175]
	global_load_lds_dwordx4 v[216:217], off
	v_lshl_add_u64 v[216:217], v[214:215], 0, s[12:13]
	s_add_i32 m0, s26, 0x2000
	s_nop 0
	global_load_lds_dwordx4 v[216:217], off
	v_lshl_add_u64 v[216:217], s[58:59], 0, v[172:173]
	s_mov_b32 m0, s55
	s_nop 0
	global_load_lds_dwordx4 v[216:217], off
	s_mov_b32 m0, s60
	s_nop 0
	global_load_lds_dwordx4 v[220:221], off
	s_setprio 1
	s_waitcnt vmcnt(8)
	s_waitcnt lgkmcnt(0)
	s_barrier
	v_mfma_f32_16x16x32_bf16 v[62:65], v[66:69], v[162:165], v[62:65]
	v_mfma_f32_16x16x32_bf16 v[58:61], v[82:85], v[162:165], v[58:61]
	v_mfma_f32_16x16x32_bf16 v[46:49], v[66:69], v[184:187], v[46:49]
	v_mfma_f32_16x16x32_bf16 v[42:45], v[82:85], v[184:187], v[42:45]
	v_mfma_f32_16x16x32_bf16 v[30:33], v[66:69], v[192:195], v[30:33]
	v_mfma_f32_16x16x32_bf16 v[26:29], v[82:85], v[192:195], v[26:29]
	v_mfma_f32_16x16x32_bf16 v[14:17], v[66:69], v[206:209], v[14:17]
	v_mfma_f32_16x16x32_bf16 v[10:13], v[82:85], v[206:209], v[10:13]
	v_mfma_f32_16x16x32_bf16 v[62:65], v[70:73], v[166:169], v[62:65]
	v_mfma_f32_16x16x32_bf16 v[58:61], v[86:89], v[166:169], v[58:61]
	v_mfma_f32_16x16x32_bf16 v[46:49], v[70:73], v[188:191], v[46:49]
	v_mfma_f32_16x16x32_bf16 v[42:45], v[86:89], v[188:191], v[42:45]
	v_mfma_f32_16x16x32_bf16 v[30:33], v[70:73], v[202:205], v[30:33]
	v_mfma_f32_16x16x32_bf16 v[26:29], v[86:89], v[202:205], v[26:29]
	v_mfma_f32_16x16x32_bf16 v[14:17], v[70:73], v[210:213], v[14:17]
	v_mfma_f32_16x16x32_bf16 v[10:13], v[86:89], v[210:213], v[10:13]
	v_mfma_f32_16x16x32_bf16 v[54:57], v[146:149], v[162:165], v[54:57]
	v_mfma_f32_16x16x32_bf16 v[50:53], v[154:157], v[162:165], v[50:53]
	v_mfma_f32_16x16x32_bf16 v[38:41], v[146:149], v[184:187], v[38:41]
	v_mfma_f32_16x16x32_bf16 v[34:37], v[154:157], v[184:187], v[34:37]
	v_mfma_f32_16x16x32_bf16 v[22:25], v[146:149], v[192:195], v[22:25]
	v_mfma_f32_16x16x32_bf16 v[18:21], v[154:157], v[192:195], v[18:21]
	v_mfma_f32_16x16x32_bf16 v[6:9], v[146:149], v[206:209], v[6:9]
	v_mfma_f32_16x16x32_bf16 v[2:5], v[154:157], v[206:209], v[2:5]
	v_mfma_f32_16x16x32_bf16 v[54:57], v[150:153], v[166:169], v[54:57]
	v_mfma_f32_16x16x32_bf16 v[50:53], v[158:161], v[166:169], v[50:53]
	v_mfma_f32_16x16x32_bf16 v[38:41], v[150:153], v[188:191], v[38:41]
	v_mfma_f32_16x16x32_bf16 v[34:37], v[158:161], v[188:191], v[34:37]
	v_mfma_f32_16x16x32_bf16 v[22:25], v[150:153], v[202:205], v[22:25]
	v_mfma_f32_16x16x32_bf16 v[18:21], v[158:161], v[202:205], v[18:21]
	v_mfma_f32_16x16x32_bf16 v[6:9], v[150:153], v[210:213], v[6:9]
	v_mfma_f32_16x16x32_bf16 v[2:5], v[158:161], v[210:213], v[2:5]
	s_barrier
	s_setprio 0
	s_add_i32 s74, 0, 0x18000
	s_add_i32 s75, 0, 0x1c000
	v_add_u32_e32 v86, s74, v197
	v_add_u32_e32 v158, s75, v197
	ds_read_b128 v[66:69], v86
	ds_read_b128 v[70:73], v86 offset:1024
	ds_read_b128 v[82:85], v86 offset:2048
	ds_read_b128 v[86:89], v86 offset:3072
	ds_read_b128 v[146:149], v158
	ds_read_b128 v[150:153], v158 offset:1024
	ds_read_b128 v[154:157], v158 offset:2048
	ds_read_b128 v[158:161], v158 offset:3072
	s_add_u32 s26, s58, 0x40000
	s_addc_u32 s27, s59, 0
	s_mov_b32 m0, s61
	v_lshl_add_u64 v[222:223], s[26:27], 0, v[172:173]
	ds_read_b128 v[162:165], v201 offset:32768
	ds_read_b128 v[166:169], v201 offset:33792
	ds_read_b128 v[184:187], v201 offset:34816
	ds_read_b128 v[188:191], v201 offset:35840
	ds_read_b128 v[192:195], v201 offset:36864
	ds_read_b128 v[202:205], v201 offset:37888
	ds_read_b128 v[206:209], v201 offset:38912
	ds_read_b128 v[210:213], v201 offset:39936
	global_load_lds_dwordx4 v[222:223], off
	v_lshl_add_u64 v[222:223], s[26:27], 0, v[174:175]
	s_mov_b32 m0, s62
	s_nop 0
	global_load_lds_dwordx4 v[222:223], off
	s_setprio 1
	s_waitcnt vmcnt(8)
	s_waitcnt lgkmcnt(0)
	s_barrier
	v_mfma_f32_16x16x32_bf16 v[142:145], v[66:69], v[162:165], v[142:145]
	v_mfma_f32_16x16x32_bf16 v[138:141], v[82:85], v[162:165], v[138:141]
	v_mfma_f32_16x16x32_bf16 v[126:129], v[66:69], v[184:187], v[126:129]
	v_mfma_f32_16x16x32_bf16 v[122:125], v[82:85], v[184:187], v[122:125]
	v_mfma_f32_16x16x32_bf16 v[110:113], v[66:69], v[192:195], v[110:113]
	v_mfma_f32_16x16x32_bf16 v[106:109], v[82:85], v[192:195], v[106:109]
	v_mfma_f32_16x16x32_bf16 v[94:97], v[66:69], v[206:209], v[94:97]
	v_mfma_f32_16x16x32_bf16 v[90:93], v[82:85], v[206:209], v[90:93]
	v_mfma_f32_16x16x32_bf16 v[142:145], v[70:73], v[166:169], v[142:145]
	v_mfma_f32_16x16x32_bf16 v[138:141], v[86:89], v[166:169], v[138:141]
	v_mfma_f32_16x16x32_bf16 v[126:129], v[70:73], v[188:191], v[126:129]
	v_mfma_f32_16x16x32_bf16 v[122:125], v[86:89], v[188:191], v[122:125]
	v_mfma_f32_16x16x32_bf16 v[110:113], v[70:73], v[202:205], v[110:113]
	v_mfma_f32_16x16x32_bf16 v[106:109], v[86:89], v[202:205], v[106:109]
	v_mfma_f32_16x16x32_bf16 v[94:97], v[70:73], v[210:213], v[94:97]
	v_mfma_f32_16x16x32_bf16 v[90:93], v[86:89], v[210:213], v[90:93]
	v_mfma_f32_16x16x32_bf16 v[134:137], v[146:149], v[162:165], v[134:137]
	v_mfma_f32_16x16x32_bf16 v[130:133], v[154:157], v[162:165], v[130:133]
	v_mfma_f32_16x16x32_bf16 v[118:121], v[146:149], v[184:187], v[118:121]
	v_mfma_f32_16x16x32_bf16 v[114:117], v[154:157], v[184:187], v[114:117]
	v_mfma_f32_16x16x32_bf16 v[102:105], v[146:149], v[192:195], v[102:105]
	v_mfma_f32_16x16x32_bf16 v[98:101], v[154:157], v[192:195], v[98:101]
	v_mfma_f32_16x16x32_bf16 v[78:81], v[146:149], v[206:209], v[78:81]
	v_mfma_f32_16x16x32_bf16 v[74:77], v[154:157], v[206:209], v[74:77]
	v_mfma_f32_16x16x32_bf16 v[134:137], v[150:153], v[166:169], v[134:137]
	v_mfma_f32_16x16x32_bf16 v[130:133], v[158:161], v[166:169], v[130:133]
	v_mfma_f32_16x16x32_bf16 v[118:121], v[150:153], v[188:191], v[118:121]
	v_mfma_f32_16x16x32_bf16 v[114:117], v[158:161], v[188:191], v[114:117]
	v_mfma_f32_16x16x32_bf16 v[102:105], v[150:153], v[202:205], v[102:105]
	v_mfma_f32_16x16x32_bf16 v[98:101], v[158:161], v[202:205], v[98:101]
	v_mfma_f32_16x16x32_bf16 v[78:81], v[150:153], v[210:213], v[78:81]
	v_mfma_f32_16x16x32_bf16 v[74:77], v[158:161], v[210:213], v[74:77]
	s_barrier
	s_setprio 0
	s_add_i32 s26, s74, s35
	v_lshl_add_u64 v[222:223], v[214:215], 0, s[16:17]
	s_mov_b32 m0, s26
	ds_read_b128 v[162:165], v201 offset:49152
	ds_read_b128 v[166:169], v201 offset:50176
	ds_read_b128 v[184:187], v201 offset:51200
	ds_read_b128 v[188:191], v201 offset:52224
	ds_read_b128 v[192:195], v201 offset:53248
	ds_read_b128 v[202:205], v201 offset:54272
	ds_read_b128 v[206:209], v201 offset:55296
	ds_read_b128 v[210:213], v201 offset:56320
	global_load_lds_dwordx4 v[222:223], off
	v_lshl_add_u64 v[222:223], v[214:215], 0, s[18:19]
	s_add_i32 m0, s26, 0x2000
	s_add_i32 s26, s75, s35
	global_load_lds_dwordx4 v[222:223], off
	v_lshl_add_u64 v[222:223], v[214:215], 0, s[22:23]
	s_mov_b32 m0, s26
	v_lshl_add_u64 v[214:215], v[214:215], 0, s[24:25]
	global_load_lds_dwordx4 v[222:223], off
	s_add_i32 m0, s26, 0x2000
	s_nop 0
	global_load_lds_dwordx4 v[214:215], off
	v_lshl_add_u64 v[214:215], v[216:217], 0, s[20:21]
	s_mov_b32 m0, s64
	s_nop 0
	global_load_lds_dwordx4 v[214:215], off
	v_lshl_add_u64 v[214:215], v[220:221], 0, s[20:21]
	s_mov_b32 m0, s65
	s_nop 0
	global_load_lds_dwordx4 v[214:215], off
	s_setprio 1
	s_waitcnt vmcnt(8)
	s_waitcnt lgkmcnt(0)
	s_barrier
	v_mfma_f32_16x16x32_bf16 v[62:65], v[66:69], v[162:165], v[62:65]
	v_mfma_f32_16x16x32_bf16 v[58:61], v[82:85], v[162:165], v[58:61]
	v_mfma_f32_16x16x32_bf16 v[46:49], v[66:69], v[184:187], v[46:49]
	v_mfma_f32_16x16x32_bf16 v[42:45], v[82:85], v[184:187], v[42:45]
	v_mfma_f32_16x16x32_bf16 v[30:33], v[66:69], v[192:195], v[30:33]
	v_mfma_f32_16x16x32_bf16 v[26:29], v[82:85], v[192:195], v[26:29]
	v_mfma_f32_16x16x32_bf16 v[14:17], v[66:69], v[206:209], v[14:17]
	v_mfma_f32_16x16x32_bf16 v[10:13], v[82:85], v[206:209], v[10:13]
	v_mfma_f32_16x16x32_bf16 v[62:65], v[70:73], v[166:169], v[62:65]
	v_mfma_f32_16x16x32_bf16 v[58:61], v[86:89], v[166:169], v[58:61]
	v_mfma_f32_16x16x32_bf16 v[46:49], v[70:73], v[188:191], v[46:49]
	v_mfma_f32_16x16x32_bf16 v[42:45], v[86:89], v[188:191], v[42:45]
	v_mfma_f32_16x16x32_bf16 v[30:33], v[70:73], v[202:205], v[30:33]
	v_mfma_f32_16x16x32_bf16 v[26:29], v[86:89], v[202:205], v[26:29]
	v_mfma_f32_16x16x32_bf16 v[14:17], v[70:73], v[210:213], v[14:17]
	v_mfma_f32_16x16x32_bf16 v[10:13], v[86:89], v[210:213], v[10:13]
	v_mfma_f32_16x16x32_bf16 v[54:57], v[146:149], v[162:165], v[54:57]
	v_mfma_f32_16x16x32_bf16 v[50:53], v[154:157], v[162:165], v[50:53]
	v_mfma_f32_16x16x32_bf16 v[38:41], v[146:149], v[184:187], v[38:41]
	v_mfma_f32_16x16x32_bf16 v[34:37], v[154:157], v[184:187], v[34:37]
	v_mfma_f32_16x16x32_bf16 v[22:25], v[146:149], v[192:195], v[22:25]
	v_mfma_f32_16x16x32_bf16 v[18:21], v[154:157], v[192:195], v[18:21]
	v_mfma_f32_16x16x32_bf16 v[6:9], v[146:149], v[206:209], v[6:9]
	v_mfma_f32_16x16x32_bf16 v[2:5], v[154:157], v[206:209], v[2:5]
	v_mfma_f32_16x16x32_bf16 v[54:57], v[150:153], v[166:169], v[54:57]
	v_mfma_f32_16x16x32_bf16 v[50:53], v[158:161], v[166:169], v[50:53]
	v_mfma_f32_16x16x32_bf16 v[38:41], v[150:153], v[188:191], v[38:41]
	v_mfma_f32_16x16x32_bf16 v[34:37], v[158:161], v[188:191], v[34:37]
	v_mfma_f32_16x16x32_bf16 v[22:25], v[150:153], v[202:205], v[22:25]
	v_mfma_f32_16x16x32_bf16 v[18:21], v[158:161], v[202:205], v[18:21]
	v_mfma_f32_16x16x32_bf16 v[6:9], v[150:153], v[210:213], v[6:9]
	v_mfma_f32_16x16x32_bf16 v[2:5], v[158:161], v[210:213], v[2:5]
	s_barrier
	s_setprio 0
	s_add_i32 s73, s73, 2
	s_add_u32 s71, s71, 0x10000
	s_addc_u32 s72, s72, 0
	s_add_u32 s56, s56, 0x100
	s_addc_u32 s57, s57, 0
	s_cmp_gt_u32 s73, 13
	s_cbranch_scc0 .LBB0_1192
	s_and_b64 vcc, exec, s[36:37]
	s_cbranch_vccz .LBB0_1195
	s_barrier
	s_setprio 3

.LBB0_1270:
	s_ashr_i32 s51, s50, 31
	s_lshl_b64 s[26:27], s[50:51], 20
	v_readlane_b32 s52, v254, 58
	v_readlane_b32 s53, v254, 59
	s_add_u32 s52, s52, s26
	s_addc_u32 s53, s53, s27
	s_and_b64 s[26:27], s[0:1], exec
	s_cselect_b32 s51, s53, s61
	s_cselect_b32 s57, s52, s60
	s_ashr_i32 s45, s44, 31
	s_lshl_b64 s[26:27], s[44:45], 20
	s_add_u32 s54, s3, s26
	s_addc_u32 s55, s33, s27
	s_and_b64 s[26:27], s[0:1], exec
	s_cselect_b32 s45, s55, s59
	s_cselect_b32 s73, s54, s58
	s_add_u32 s74, s58, 0x10000
	s_addc_u32 s75, s59, 0
	s_add_u32 s58, s60, 0x80080
	s_addc_u32 s59, s61, 0
	s_mov_b32 s80, -2
	ds_read_b128 v[144:147], v158
	ds_read_b128 v[148:151], v158 offset:1024
	ds_read_b128 v[152:155], v158 offset:2048
	ds_read_b128 v[162:165], v158 offset:3072
	ds_read_b128 v[166:169], v159
	ds_read_b128 v[170:173], v159 offset:1024
	ds_read_b128 v[174:177], v159 offset:2048
	ds_read_b128 v[178:181], v159 offset:3072
	s_add_u32 s26, s58, 0xfff80080
	s_addc_u32 s27, s59, -1
	s_cmp_eq_u32 s80, 28
	s_cselect_b32 s61, s51, s27
	s_cselect_b32 s60, s57, s26
	s_cselect_b32 s27, s45, s75
	s_cselect_b32 s26, s73, s74
	v_lshl_add_u64 v[214:215], s[58:59], 0, v[136:137]
	s_add_i32 m0, s63, 0xc000
	ds_read_b128 v[182:185], v160
	ds_read_b128 v[186:189], v160 offset:1024
	ds_read_b128 v[190:193], v160 offset:2048
	ds_read_b128 v[194:197], v160 offset:3072
	ds_read_b128 v[198:201], v160 offset:4096
	ds_read_b128 v[202:205], v160 offset:5120
	ds_read_b128 v[206:209], v160 offset:6144
	ds_read_b128 v[210:213], v160 offset:7168
	global_load_lds_dwordx4 v[214:215], off
	v_lshl_add_u64 v[214:215], s[58:59], 0, v[138:139]
	s_add_i32 m0, s63, 0xe000
	s_nop 0
	global_load_lds_dwordx4 v[214:215], off
	s_setprio 1
	s_waitcnt vmcnt(8)
	s_waitcnt lgkmcnt(0)
	s_barrier
	v_mfma_f32_16x16x32_bf16 v[126:129], v[144:147], v[182:185], 0
	v_mfma_f32_16x16x32_bf16 v[122:125], v[152:155], v[182:185], 0
	v_mfma_f32_16x16x32_bf16 v[118:121], v[144:147], v[190:193], 0
	v_mfma_f32_16x16x32_bf16 v[114:117], v[152:155], v[190:193], 0
	v_mfma_f32_16x16x32_bf16 v[106:109], v[144:147], v[198:201], 0
	v_mfma_f32_16x16x32_bf16 v[98:101], v[152:155], v[198:201], 0
	v_mfma_f32_16x16x32_bf16 v[90:93], v[144:147], v[206:209], 0
	v_mfma_f32_16x16x32_bf16 v[82:85], v[152:155], v[206:209], 0
	v_mfma_f32_16x16x32_bf16 v[126:129], v[148:151], v[186:189], v[126:129]
	v_mfma_f32_16x16x32_bf16 v[122:125], v[162:165], v[186:189], v[122:125]
	v_mfma_f32_16x16x32_bf16 v[118:121], v[148:151], v[194:197], v[118:121]
	v_mfma_f32_16x16x32_bf16 v[114:117], v[162:165], v[194:197], v[114:117]
	v_mfma_f32_16x16x32_bf16 v[106:109], v[148:151], v[202:205], v[106:109]
	v_mfma_f32_16x16x32_bf16 v[98:101], v[162:165], v[202:205], v[98:101]
	v_mfma_f32_16x16x32_bf16 v[90:93], v[148:151], v[210:213], v[90:93]
	v_mfma_f32_16x16x32_bf16 v[82:85], v[162:165], v[210:213], v[82:85]
	v_mfma_f32_16x16x32_bf16 v[110:113], v[166:169], v[182:185], 0
	v_mfma_f32_16x16x32_bf16 v[102:105], v[174:177], v[182:185], 0
	v_mfma_f32_16x16x32_bf16 v[94:97], v[166:169], v[190:193], 0
	v_mfma_f32_16x16x32_bf16 v[86:89], v[174:177], v[190:193], 0
	v_mfma_f32_16x16x32_bf16 v[78:81], v[166:169], v[198:201], 0
	v_mfma_f32_16x16x32_bf16 v[74:77], v[174:177], v[198:201], 0
	v_mfma_f32_16x16x32_bf16 v[70:73], v[166:169], v[206:209], 0
	v_mfma_f32_16x16x32_bf16 v[66:69], v[174:177], v[206:209], 0
	v_mfma_f32_16x16x32_bf16 v[110:113], v[170:173], v[186:189], v[110:113]
	v_mfma_f32_16x16x32_bf16 v[102:105], v[178:181], v[186:189], v[102:105]
	v_mfma_f32_16x16x32_bf16 v[94:97], v[170:173], v[194:197], v[94:97]
	v_mfma_f32_16x16x32_bf16 v[86:89], v[178:181], v[194:197], v[86:89]
	v_mfma_f32_16x16x32_bf16 v[78:81], v[170:173], v[202:205], v[78:81]
	v_mfma_f32_16x16x32_bf16 v[74:77], v[178:181], v[202:205], v[74:77]
	v_mfma_f32_16x16x32_bf16 v[70:73], v[170:173], v[210:213], v[70:73]
	v_mfma_f32_16x16x32_bf16 v[66:69], v[178:181], v[210:213], v[66:69]
	s_barrier
	s_setprio 0
	v_lshl_add_u64 v[214:215], s[26:27], 0, v[130:131]
	s_add_i32 s26, s71, s35
	s_mov_b32 m0, s26
	ds_read_b128 v[182:185], v160 offset:16384
	ds_read_b128 v[186:189], v160 offset:17408
	ds_read_b128 v[190:193], v160 offset:18432
	ds_read_b128 v[194:197], v160 offset:19456
	ds_read_b128 v[198:201], v160 offset:20480
	ds_read_b128 v[202:205], v160 offset:21504
	ds_read_b128 v[206:209], v160 offset:22528
	ds_read_b128 v[210:213], v160 offset:23552
	global_load_lds_dwordx4 v[214:215], off
	v_lshl_add_u64 v[216:217], v[214:215], 0, s[6:7]
	s_add_i32 m0, s26, 0x2000
	s_add_i32 s26, s72, s35
	global_load_lds_dwordx4 v[216:217], off
	v_lshl_add_u64 v[216:217], v[214:215], 0, s[8:9]
	s_mov_b32 m0, s26
	v_lshl_add_u64 v[220:221], s[60:61], 0, v[134:135]
	global_load_lds_dwordx4 v[216:217], off
	v_lshl_add_u64 v[216:217], v[214:215], 0, s[10:11]
	s_add_i32 m0, s26, 0x2000
	s_nop 0
	global_load_lds_dwordx4 v[216:217], off
	v_lshl_add_u64 v[216:217], s[60:61], 0, v[132:133]
	s_mov_b32 m0, s63
	s_nop 0
	global_load_lds_dwordx4 v[216:217], off
	s_mov_b32 m0, s64
	s_nop 0
	global_load_lds_dwordx4 v[220:221], off
	s_setprio 1
	s_waitcnt vmcnt(8)
	s_waitcnt lgkmcnt(0)
	s_barrier
	v_mfma_f32_16x16x32_bf16 v[62:65], v[144:147], v[182:185], 0
	v_mfma_f32_16x16x32_bf16 v[58:61], v[152:155], v[182:185], 0
	v_mfma_f32_16x16x32_bf16 v[54:57], v[144:147], v[190:193], 0
	v_mfma_f32_16x16x32_bf16 v[46:49], v[152:155], v[190:193], 0
	v_mfma_f32_16x16x32_bf16 v[38:41], v[144:147], v[198:201], 0
	v_mfma_f32_16x16x32_bf16 v[30:33], v[152:155], v[198:201], 0
	v_mfma_f32_16x16x32_bf16 v[22:25], v[144:147], v[206:209], 0
	v_mfma_f32_16x16x32_bf16 v[14:17], v[152:155], v[206:209], 0
	v_mfma_f32_16x16x32_bf16 v[62:65], v[148:151], v[186:189], v[62:65]
	v_mfma_f32_16x16x32_bf16 v[58:61], v[162:165], v[186:189], v[58:61]
	v_mfma_f32_16x16x32_bf16 v[54:57], v[148:151], v[194:197], v[54:57]
	v_mfma_f32_16x16x32_bf16 v[46:49], v[162:165], v[194:197], v[46:49]
	v_mfma_f32_16x16x32_bf16 v[38:41], v[148:151], v[202:205], v[38:41]
	v_mfma_f32_16x16x32_bf16 v[30:33], v[162:165], v[202:205], v[30:33]
	v_mfma_f32_16x16x32_bf16 v[22:25], v[148:151], v[210:213], v[22:25]
	v_mfma_f32_16x16x32_bf16 v[14:17], v[162:165], v[210:213], v[14:17]
	v_mfma_f32_16x16x32_bf16 v[50:53], v[166:169], v[182:185], 0
	v_mfma_f32_16x16x32_bf16 v[42:45], v[174:177], v[182:185], 0
	v_mfma_f32_16x16x32_bf16 v[34:37], v[166:169], v[190:193], 0
	v_mfma_f32_16x16x32_bf16 v[26:29], v[174:177], v[190:193], 0
	v_mfma_f32_16x16x32_bf16 v[18:21], v[166:169], v[198:201], 0
	v_mfma_f32_16x16x32_bf16 v[10:13], v[174:177], v[198:201], 0
	v_mfma_f32_16x16x32_bf16 v[6:9], v[166:169], v[206:209], 0
	v_mfma_f32_16x16x32_bf16 v[2:5], v[174:177], v[206:209], 0
	v_mfma_f32_16x16x32_bf16 v[50:53], v[170:173], v[186:189], v[50:53]
	v_mfma_f32_16x16x32_bf16 v[42:45], v[178:181], v[186:189], v[42:45]
	v_mfma_f32_16x16x32_bf16 v[34:37], v[170:173], v[194:197], v[34:37]
	v_mfma_f32_16x16x32_bf16 v[26:29], v[178:181], v[194:197], v[26:29]
	v_mfma_f32_16x16x32_bf16 v[18:21], v[170:173], v[202:205], v[18:21]
	v_mfma_f32_16x16x32_bf16 v[10:13], v[178:181], v[202:205], v[10:13]
	v_mfma_f32_16x16x32_bf16 v[6:9], v[170:173], v[210:213], v[6:9]
	v_mfma_f32_16x16x32_bf16 v[2:5], v[178:181], v[210:213], v[2:5]
	s_barrier
	s_setprio 0
	s_add_i32 s81, 0, 0x18000
	v_add_u32_e32 v161, s81, v156
	s_add_i32 s82, 0, 0x1c000
	ds_read_b128 v[144:147], v161
	ds_read_b128 v[148:151], v161 offset:1024
	ds_read_b128 v[152:155], v161 offset:2048
	ds_read_b128 v[162:165], v161 offset:3072
	v_add_u32_e32 v161, s82, v156
	ds_read_b128 v[166:169], v161
	ds_read_b128 v[170:173], v161 offset:1024
	ds_read_b128 v[174:177], v161 offset:2048
	ds_read_b128 v[178:181], v161 offset:3072
	s_add_u32 s26, s60, 0x80000
	s_addc_u32 s27, s61, 0
	s_mov_b32 m0, s65
	v_lshl_add_u64 v[222:223], s[26:27], 0, v[132:133]
	ds_read_b128 v[182:185], v160 offset:32768
	ds_read_b128 v[186:189], v160 offset:33792
	ds_read_b128 v[190:193], v160 offset:34816
	ds_read_b128 v[194:197], v160 offset:35840
	ds_read_b128 v[198:201], v160 offset:36864
	ds_read_b128 v[202:205], v160 offset:37888
	ds_read_b128 v[206:209], v160 offset:38912
	ds_read_b128 v[210:213], v160 offset:39936
	global_load_lds_dwordx4 v[222:223], off
	v_lshl_add_u64 v[222:223], s[26:27], 0, v[134:135]
	s_mov_b32 m0, s66
	s_nop 0
	global_load_lds_dwordx4 v[222:223], off
	s_setprio 1
	s_waitcnt vmcnt(8)
	s_waitcnt lgkmcnt(0)
	s_barrier
	v_mfma_f32_16x16x32_bf16 v[126:129], v[144:147], v[182:185], v[126:129]
	v_mfma_f32_16x16x32_bf16 v[122:125], v[152:155], v[182:185], v[122:125]
	v_mfma_f32_16x16x32_bf16 v[118:121], v[144:147], v[190:193], v[118:121]
	v_mfma_f32_16x16x32_bf16 v[114:117], v[152:155], v[190:193], v[114:117]
	v_mfma_f32_16x16x32_bf16 v[106:109], v[144:147], v[198:201], v[106:109]
	v_mfma_f32_16x16x32_bf16 v[98:101], v[152:155], v[198:201], v[98:101]
	v_mfma_f32_16x16x32_bf16 v[90:93], v[144:147], v[206:209], v[90:93]
	v_mfma_f32_16x16x32_bf16 v[82:85], v[152:155], v[206:209], v[82:85]
	v_mfma_f32_16x16x32_bf16 v[126:129], v[148:151], v[186:189], v[126:129]
	v_mfma_f32_16x16x32_bf16 v[122:125], v[162:165], v[186:189], v[122:125]
	v_mfma_f32_16x16x32_bf16 v[118:121], v[148:151], v[194:197], v[118:121]
	v_mfma_f32_16x16x32_bf16 v[114:117], v[162:165], v[194:197], v[114:117]
	v_mfma_f32_16x16x32_bf16 v[106:109], v[148:151], v[202:205], v[106:109]
	v_mfma_f32_16x16x32_bf16 v[98:101], v[162:165], v[202:205], v[98:101]
	v_mfma_f32_16x16x32_bf16 v[90:93], v[148:151], v[210:213], v[90:93]
	v_mfma_f32_16x16x32_bf16 v[82:85], v[162:165], v[210:213], v[82:85]
	v_mfma_f32_16x16x32_bf16 v[110:113], v[166:169], v[182:185], v[110:113]
	v_mfma_f32_16x16x32_bf16 v[102:105], v[174:177], v[182:185], v[102:105]
	v_mfma_f32_16x16x32_bf16 v[94:97], v[166:169], v[190:193], v[94:97]
	v_mfma_f32_16x16x32_bf16 v[86:89], v[174:177], v[190:193], v[86:89]
	v_mfma_f32_16x16x32_bf16 v[78:81], v[166:169], v[198:201], v[78:81]
	v_mfma_f32_16x16x32_bf16 v[74:77], v[174:177], v[198:201], v[74:77]
	v_mfma_f32_16x16x32_bf16 v[70:73], v[166:169], v[206:209], v[70:73]
	v_mfma_f32_16x16x32_bf16 v[66:69], v[174:177], v[206:209], v[66:69]
	v_mfma_f32_16x16x32_bf16 v[110:113], v[170:173], v[186:189], v[110:113]
	v_mfma_f32_16x16x32_bf16 v[102:105], v[178:181], v[186:189], v[102:105]
	v_mfma_f32_16x16x32_bf16 v[94:97], v[170:173], v[194:197], v[94:97]
	v_mfma_f32_16x16x32_bf16 v[86:89], v[178:181], v[194:197], v[86:89]
	v_mfma_f32_16x16x32_bf16 v[78:81], v[170:173], v[202:205], v[78:81]
	v_mfma_f32_16x16x32_bf16 v[74:77], v[178:181], v[202:205], v[74:77]
	v_mfma_f32_16x16x32_bf16 v[70:73], v[170:173], v[210:213], v[70:73]
	v_mfma_f32_16x16x32_bf16 v[66:69], v[178:181], v[210:213], v[66:69]
	s_barrier
	s_setprio 0
	s_add_i32 s26, s81, s35
	v_lshl_add_u64 v[222:223], v[214:215], 0, s[14:15]
	s_mov_b32 m0, s26
	ds_read_b128 v[182:185], v160 offset:49152
	ds_read_b128 v[186:189], v160 offset:50176
	ds_read_b128 v[190:193], v160 offset:51200
	ds_read_b128 v[194:197], v160 offset:52224
	ds_read_b128 v[198:201], v160 offset:53248
	ds_read_b128 v[202:205], v160 offset:54272
	ds_read_b128 v[206:209], v160 offset:55296
	ds_read_b128 v[210:213], v160 offset:56320
	global_load_lds_dwordx4 v[222:223], off
	v_lshl_add_u64 v[222:223], v[214:215], 0, s[16:17]
	s_add_i32 m0, s26, 0x2000
	s_add_i32 s26, s82, s35
	global_load_lds_dwordx4 v[222:223], off
	v_lshl_add_u64 v[222:223], v[214:215], 0, s[20:21]
	s_mov_b32 m0, s26
	v_lshl_add_u64 v[214:215], v[214:215], 0, s[22:23]
	global_load_lds_dwordx4 v[222:223], off
	s_add_i32 m0, s26, 0x2000
	s_nop 0
	global_load_lds_dwordx4 v[214:215], off
	v_lshl_add_u64 v[214:215], v[216:217], 0, s[18:19]
	s_mov_b32 m0, s68
	s_nop 0
	global_load_lds_dwordx4 v[214:215], off
	v_lshl_add_u64 v[214:215], v[220:221], 0, s[18:19]
	s_mov_b32 m0, s69
	s_nop 0
	global_load_lds_dwordx4 v[214:215], off
	s_setprio 1
	s_waitcnt vmcnt(8)
	s_waitcnt lgkmcnt(0)
	s_barrier
	v_mfma_f32_16x16x32_bf16 v[62:65], v[144:147], v[182:185], v[62:65]
	v_mfma_f32_16x16x32_bf16 v[58:61], v[152:155], v[182:185], v[58:61]
	v_mfma_f32_16x16x32_bf16 v[54:57], v[144:147], v[190:193], v[54:57]
	v_mfma_f32_16x16x32_bf16 v[46:49], v[152:155], v[190:193], v[46:49]
	v_mfma_f32_16x16x32_bf16 v[38:41], v[144:147], v[198:201], v[38:41]
	v_mfma_f32_16x16x32_bf16 v[30:33], v[152:155], v[198:201], v[30:33]
	v_mfma_f32_16x16x32_bf16 v[22:25], v[144:147], v[206:209], v[22:25]
	v_mfma_f32_16x16x32_bf16 v[14:17], v[152:155], v[206:209], v[14:17]
	v_mfma_f32_16x16x32_bf16 v[62:65], v[148:151], v[186:189], v[62:65]
	v_mfma_f32_16x16x32_bf16 v[58:61], v[162:165], v[186:189], v[58:61]
	v_mfma_f32_16x16x32_bf16 v[54:57], v[148:151], v[194:197], v[54:57]
	v_mfma_f32_16x16x32_bf16 v[46:49], v[162:165], v[194:197], v[46:49]
	v_mfma_f32_16x16x32_bf16 v[38:41], v[148:151], v[202:205], v[38:41]
	v_mfma_f32_16x16x32_bf16 v[30:33], v[162:165], v[202:205], v[30:33]
	v_mfma_f32_16x16x32_bf16 v[22:25], v[148:151], v[210:213], v[22:25]
	v_mfma_f32_16x16x32_bf16 v[14:17], v[162:165], v[210:213], v[14:17]
	v_mfma_f32_16x16x32_bf16 v[50:53], v[166:169], v[182:185], v[50:53]
	v_mfma_f32_16x16x32_bf16 v[42:45], v[174:177], v[182:185], v[42:45]
	v_mfma_f32_16x16x32_bf16 v[34:37], v[166:169], v[190:193], v[34:37]
	v_mfma_f32_16x16x32_bf16 v[26:29], v[174:177], v[190:193], v[26:29]
	v_mfma_f32_16x16x32_bf16 v[18:21], v[166:169], v[198:201], v[18:21]
	v_mfma_f32_16x16x32_bf16 v[10:13], v[174:177], v[198:201], v[10:13]
	v_mfma_f32_16x16x32_bf16 v[6:9], v[166:169], v[206:209], v[6:9]
	v_mfma_f32_16x16x32_bf16 v[2:5], v[174:177], v[206:209], v[2:5]
	v_mfma_f32_16x16x32_bf16 v[50:53], v[170:173], v[186:189], v[50:53]
	v_mfma_f32_16x16x32_bf16 v[42:45], v[178:181], v[186:189], v[42:45]
	v_mfma_f32_16x16x32_bf16 v[34:37], v[170:173], v[194:197], v[34:37]
	v_mfma_f32_16x16x32_bf16 v[26:29], v[178:181], v[194:197], v[26:29]
	v_mfma_f32_16x16x32_bf16 v[18:21], v[170:173], v[202:205], v[18:21]
	v_mfma_f32_16x16x32_bf16 v[10:13], v[178:181], v[202:205], v[10:13]
	v_mfma_f32_16x16x32_bf16 v[6:9], v[170:173], v[210:213], v[6:9]
	v_mfma_f32_16x16x32_bf16 v[2:5], v[178:181], v[210:213], v[2:5]
	s_barrier
	s_setprio 0
	s_add_i32 s80, s80, 2
	s_add_u32 s74, s74, 0x10000
	s_addc_u32 s75, s75, 0
	s_add_u32 s58, s58, 0x100
	s_addc_u32 s59, s59, 0
	s_cmp_gt_u32 s80, 29
.LBB0_1271:
	ds_read_b128 v[144:147], v158
	ds_read_b128 v[148:151], v158 offset:1024
	ds_read_b128 v[152:155], v158 offset:2048
	ds_read_b128 v[162:165], v158 offset:3072
	ds_read_b128 v[166:169], v159
	ds_read_b128 v[170:173], v159 offset:1024
	ds_read_b128 v[174:177], v159 offset:2048
	ds_read_b128 v[178:181], v159 offset:3072
	s_add_u32 s26, s58, 0xfff80080
	s_addc_u32 s27, s59, -1
	s_cmp_eq_u32 s80, 28
	s_cselect_b32 s61, s51, s27
	s_cselect_b32 s60, s57, s26
	s_cselect_b32 s27, s45, s75
	s_cselect_b32 s26, s73, s74
	v_lshl_add_u64 v[214:215], s[58:59], 0, v[136:137]
	s_add_i32 m0, s63, 0xc000
	ds_read_b128 v[182:185], v160
	ds_read_b128 v[186:189], v160 offset:1024
	ds_read_b128 v[190:193], v160 offset:2048
	ds_read_b128 v[194:197], v160 offset:3072
	ds_read_b128 v[198:201], v160 offset:4096
	ds_read_b128 v[202:205], v160 offset:5120
	ds_read_b128 v[206:209], v160 offset:6144
	ds_read_b128 v[210:213], v160 offset:7168
	global_load_lds_dwordx4 v[214:215], off
	v_lshl_add_u64 v[214:215], s[58:59], 0, v[138:139]
	s_add_i32 m0, s63, 0xe000
	s_nop 0
	global_load_lds_dwordx4 v[214:215], off
	s_setprio 1
	s_waitcnt vmcnt(8)
	s_waitcnt lgkmcnt(0)
	s_barrier
	v_mfma_f32_16x16x32_bf16 v[126:129], v[144:147], v[182:185], v[126:129]
	v_mfma_f32_16x16x32_bf16 v[122:125], v[152:155], v[182:185], v[122:125]
	v_mfma_f32_16x16x32_bf16 v[118:121], v[144:147], v[190:193], v[118:121]
	v_mfma_f32_16x16x32_bf16 v[114:117], v[152:155], v[190:193], v[114:117]
	v_mfma_f32_16x16x32_bf16 v[106:109], v[144:147], v[198:201], v[106:109]
	v_mfma_f32_16x16x32_bf16 v[98:101], v[152:155], v[198:201], v[98:101]
	v_mfma_f32_16x16x32_bf16 v[90:93], v[144:147], v[206:209], v[90:93]
	v_mfma_f32_16x16x32_bf16 v[82:85], v[152:155], v[206:209], v[82:85]
	v_mfma_f32_16x16x32_bf16 v[126:129], v[148:151], v[186:189], v[126:129]
	v_mfma_f32_16x16x32_bf16 v[122:125], v[162:165], v[186:189], v[122:125]
	v_mfma_f32_16x16x32_bf16 v[118:121], v[148:151], v[194:197], v[118:121]
	v_mfma_f32_16x16x32_bf16 v[114:117], v[162:165], v[194:197], v[114:117]
	v_mfma_f32_16x16x32_bf16 v[106:109], v[148:151], v[202:205], v[106:109]
	v_mfma_f32_16x16x32_bf16 v[98:101], v[162:165], v[202:205], v[98:101]
	v_mfma_f32_16x16x32_bf16 v[90:93], v[148:151], v[210:213], v[90:93]
	v_mfma_f32_16x16x32_bf16 v[82:85], v[162:165], v[210:213], v[82:85]
	v_mfma_f32_16x16x32_bf16 v[110:113], v[166:169], v[182:185], v[110:113]
	v_mfma_f32_16x16x32_bf16 v[102:105], v[174:177], v[182:185], v[102:105]
	v_mfma_f32_16x16x32_bf16 v[94:97], v[166:169], v[190:193], v[94:97]
	v_mfma_f32_16x16x32_bf16 v[86:89], v[174:177], v[190:193], v[86:89]
	v_mfma_f32_16x16x32_bf16 v[78:81], v[166:169], v[198:201], v[78:81]
	v_mfma_f32_16x16x32_bf16 v[74:77], v[174:177], v[198:201], v[74:77]
	v_mfma_f32_16x16x32_bf16 v[70:73], v[166:169], v[206:209], v[70:73]
	v_mfma_f32_16x16x32_bf16 v[66:69], v[174:177], v[206:209], v[66:69]
	v_mfma_f32_16x16x32_bf16 v[110:113], v[170:173], v[186:189], v[110:113]
	v_mfma_f32_16x16x32_bf16 v[102:105], v[178:181], v[186:189], v[102:105]
	v_mfma_f32_16x16x32_bf16 v[94:97], v[170:173], v[194:197], v[94:97]
	v_mfma_f32_16x16x32_bf16 v[86:89], v[178:181], v[194:197], v[86:89]
	v_mfma_f32_16x16x32_bf16 v[78:81], v[170:173], v[202:205], v[78:81]
	v_mfma_f32_16x16x32_bf16 v[74:77], v[178:181], v[202:205], v[74:77]
	v_mfma_f32_16x16x32_bf16 v[70:73], v[170:173], v[210:213], v[70:73]
	v_mfma_f32_16x16x32_bf16 v[66:69], v[178:181], v[210:213], v[66:69]
	s_barrier
	s_setprio 0
	v_lshl_add_u64 v[214:215], s[26:27], 0, v[130:131]
	s_add_i32 s26, s71, s35
	s_mov_b32 m0, s26
	ds_read_b128 v[182:185], v160 offset:16384
	ds_read_b128 v[186:189], v160 offset:17408
	ds_read_b128 v[190:193], v160 offset:18432
	ds_read_b128 v[194:197], v160 offset:19456
	ds_read_b128 v[198:201], v160 offset:20480
	ds_read_b128 v[202:205], v160 offset:21504
	ds_read_b128 v[206:209], v160 offset:22528
	ds_read_b128 v[210:213], v160 offset:23552
	global_load_lds_dwordx4 v[214:215], off
	v_lshl_add_u64 v[216:217], v[214:215], 0, s[6:7]
	s_add_i32 m0, s26, 0x2000
	s_add_i32 s26, s72, s35
	global_load_lds_dwordx4 v[216:217], off
	v_lshl_add_u64 v[216:217], v[214:215], 0, s[8:9]
	s_mov_b32 m0, s26
	v_lshl_add_u64 v[220:221], s[60:61], 0, v[134:135]
	global_load_lds_dwordx4 v[216:217], off
	v_lshl_add_u64 v[216:217], v[214:215], 0, s[10:11]
	s_add_i32 m0, s26, 0x2000
	s_nop 0
	global_load_lds_dwordx4 v[216:217], off
	v_lshl_add_u64 v[216:217], s[60:61], 0, v[132:133]
	s_mov_b32 m0, s63
	s_nop 0
	global_load_lds_dwordx4 v[216:217], off
	s_mov_b32 m0, s64
	s_nop 0
	global_load_lds_dwordx4 v[220:221], off
	s_setprio 1
	s_waitcnt vmcnt(8)
	s_waitcnt lgkmcnt(0)
	s_barrier
	v_mfma_f32_16x16x32_bf16 v[62:65], v[144:147], v[182:185], v[62:65]
	v_mfma_f32_16x16x32_bf16 v[58:61], v[152:155], v[182:185], v[58:61]
	v_mfma_f32_16x16x32_bf16 v[54:57], v[144:147], v[190:193], v[54:57]
	v_mfma_f32_16x16x32_bf16 v[46:49], v[152:155], v[190:193], v[46:49]
	v_mfma_f32_16x16x32_bf16 v[38:41], v[144:147], v[198:201], v[38:41]
	v_mfma_f32_16x16x32_bf16 v[30:33], v[152:155], v[198:201], v[30:33]
	v_mfma_f32_16x16x32_bf16 v[22:25], v[144:147], v[206:209], v[22:25]
	v_mfma_f32_16x16x32_bf16 v[14:17], v[152:155], v[206:209], v[14:17]
	v_mfma_f32_16x16x32_bf16 v[62:65], v[148:151], v[186:189], v[62:65]
	v_mfma_f32_16x16x32_bf16 v[58:61], v[162:165], v[186:189], v[58:61]
	v_mfma_f32_16x16x32_bf16 v[54:57], v[148:151], v[194:197], v[54:57]
	v_mfma_f32_16x16x32_bf16 v[46:49], v[162:165], v[194:197], v[46:49]
	v_mfma_f32_16x16x32_bf16 v[38:41], v[148:151], v[202:205], v[38:41]
	v_mfma_f32_16x16x32_bf16 v[30:33], v[162:165], v[202:205], v[30:33]
	v_mfma_f32_16x16x32_bf16 v[22:25], v[148:151], v[210:213], v[22:25]
	v_mfma_f32_16x16x32_bf16 v[14:17], v[162:165], v[210:213], v[14:17]
	v_mfma_f32_16x16x32_bf16 v[50:53], v[166:169], v[182:185], v[50:53]
	v_mfma_f32_16x16x32_bf16 v[42:45], v[174:177], v[182:185], v[42:45]
	v_mfma_f32_16x16x32_bf16 v[34:37], v[166:169], v[190:193], v[34:37]
	v_mfma_f32_16x16x32_bf16 v[26:29], v[174:177], v[190:193], v[26:29]
	v_mfma_f32_16x16x32_bf16 v[18:21], v[166:169], v[198:201], v[18:21]
	v_mfma_f32_16x16x32_bf16 v[10:13], v[174:177], v[198:201], v[10:13]
	v_mfma_f32_16x16x32_bf16 v[6:9], v[166:169], v[206:209], v[6:9]
	v_mfma_f32_16x16x32_bf16 v[2:5], v[174:177], v[206:209], v[2:5]
	v_mfma_f32_16x16x32_bf16 v[50:53], v[170:173], v[186:189], v[50:53]
	v_mfma_f32_16x16x32_bf16 v[42:45], v[178:181], v[186:189], v[42:45]
	v_mfma_f32_16x16x32_bf16 v[34:37], v[170:173], v[194:197], v[34:37]
	v_mfma_f32_16x16x32_bf16 v[26:29], v[178:181], v[194:197], v[26:29]
	v_mfma_f32_16x16x32_bf16 v[18:21], v[170:173], v[202:205], v[18:21]
	v_mfma_f32_16x16x32_bf16 v[10:13], v[178:181], v[202:205], v[10:13]
	v_mfma_f32_16x16x32_bf16 v[6:9], v[170:173], v[210:213], v[6:9]
	v_mfma_f32_16x16x32_bf16 v[2:5], v[178:181], v[210:213], v[2:5]
	s_barrier
	s_setprio 0
	s_add_i32 s81, 0, 0x18000
	v_add_u32_e32 v161, s81, v156
	s_add_i32 s82, 0, 0x1c000
	ds_read_b128 v[144:147], v161
	ds_read_b128 v[148:151], v161 offset:1024
	ds_read_b128 v[152:155], v161 offset:2048
	ds_read_b128 v[162:165], v161 offset:3072
	v_add_u32_e32 v161, s82, v156
	ds_read_b128 v[166:169], v161
	ds_read_b128 v[170:173], v161 offset:1024
	ds_read_b128 v[174:177], v161 offset:2048
	ds_read_b128 v[178:181], v161 offset:3072
	s_add_u32 s26, s60, 0x80000
	s_addc_u32 s27, s61, 0
	s_mov_b32 m0, s65
	v_lshl_add_u64 v[222:223], s[26:27], 0, v[132:133]
	ds_read_b128 v[182:185], v160 offset:32768
	ds_read_b128 v[186:189], v160 offset:33792
	ds_read_b128 v[190:193], v160 offset:34816
	ds_read_b128 v[194:197], v160 offset:35840
	ds_read_b128 v[198:201], v160 offset:36864
	ds_read_b128 v[202:205], v160 offset:37888
	ds_read_b128 v[206:209], v160 offset:38912
	ds_read_b128 v[210:213], v160 offset:39936
	global_load_lds_dwordx4 v[222:223], off
	v_lshl_add_u64 v[222:223], s[26:27], 0, v[134:135]
	s_mov_b32 m0, s66
	s_nop 0
	global_load_lds_dwordx4 v[222:223], off
	s_setprio 1
	s_waitcnt vmcnt(8)
	s_waitcnt lgkmcnt(0)
	s_barrier
	v_mfma_f32_16x16x32_bf16 v[126:129], v[144:147], v[182:185], v[126:129]
	v_mfma_f32_16x16x32_bf16 v[122:125], v[152:155], v[182:185], v[122:125]
	v_mfma_f32_16x16x32_bf16 v[118:121], v[144:147], v[190:193], v[118:121]
	v_mfma_f32_16x16x32_bf16 v[114:117], v[152:155], v[190:193], v[114:117]
	v_mfma_f32_16x16x32_bf16 v[106:109], v[144:147], v[198:201], v[106:109]
	v_mfma_f32_16x16x32_bf16 v[98:101], v[152:155], v[198:201], v[98:101]
	v_mfma_f32_16x16x32_bf16 v[90:93], v[144:147], v[206:209], v[90:93]
	v_mfma_f32_16x16x32_bf16 v[82:85], v[152:155], v[206:209], v[82:85]
	v_mfma_f32_16x16x32_bf16 v[126:129], v[148:151], v[186:189], v[126:129]
	v_mfma_f32_16x16x32_bf16 v[122:125], v[162:165], v[186:189], v[122:125]
	v_mfma_f32_16x16x32_bf16 v[118:121], v[148:151], v[194:197], v[118:121]
	v_mfma_f32_16x16x32_bf16 v[114:117], v[162:165], v[194:197], v[114:117]
	v_mfma_f32_16x16x32_bf16 v[106:109], v[148:151], v[202:205], v[106:109]
	v_mfma_f32_16x16x32_bf16 v[98:101], v[162:165], v[202:205], v[98:101]
	v_mfma_f32_16x16x32_bf16 v[90:93], v[148:151], v[210:213], v[90:93]
	v_mfma_f32_16x16x32_bf16 v[82:85], v[162:165], v[210:213], v[82:85]
	v_mfma_f32_16x16x32_bf16 v[110:113], v[166:169], v[182:185], v[110:113]
	v_mfma_f32_16x16x32_bf16 v[102:105], v[174:177], v[182:185], v[102:105]
	v_mfma_f32_16x16x32_bf16 v[94:97], v[166:169], v[190:193], v[94:97]
	v_mfma_f32_16x16x32_bf16 v[86:89], v[174:177], v[190:193], v[86:89]
	v_mfma_f32_16x16x32_bf16 v[78:81], v[166:169], v[198:201], v[78:81]
	v_mfma_f32_16x16x32_bf16 v[74:77], v[174:177], v[198:201], v[74:77]
	v_mfma_f32_16x16x32_bf16 v[70:73], v[166:169], v[206:209], v[70:73]
	v_mfma_f32_16x16x32_bf16 v[66:69], v[174:177], v[206:209], v[66:69]
	v_mfma_f32_16x16x32_bf16 v[110:113], v[170:173], v[186:189], v[110:113]
	v_mfma_f32_16x16x32_bf16 v[102:105], v[178:181], v[186:189], v[102:105]
	v_mfma_f32_16x16x32_bf16 v[94:97], v[170:173], v[194:197], v[94:97]
	v_mfma_f32_16x16x32_bf16 v[86:89], v[178:181], v[194:197], v[86:89]
	v_mfma_f32_16x16x32_bf16 v[78:81], v[170:173], v[202:205], v[78:81]
	v_mfma_f32_16x16x32_bf16 v[74:77], v[178:181], v[202:205], v[74:77]
	v_mfma_f32_16x16x32_bf16 v[70:73], v[170:173], v[210:213], v[70:73]
	v_mfma_f32_16x16x32_bf16 v[66:69], v[178:181], v[210:213], v[66:69]
	s_barrier
	s_setprio 0
	s_add_i32 s26, s81, s35
	v_lshl_add_u64 v[222:223], v[214:215], 0, s[14:15]
	s_mov_b32 m0, s26
	ds_read_b128 v[182:185], v160 offset:49152
	ds_read_b128 v[186:189], v160 offset:50176
	ds_read_b128 v[190:193], v160 offset:51200
	ds_read_b128 v[194:197], v160 offset:52224
	ds_read_b128 v[198:201], v160 offset:53248
	ds_read_b128 v[202:205], v160 offset:54272
	ds_read_b128 v[206:209], v160 offset:55296
	ds_read_b128 v[210:213], v160 offset:56320
	global_load_lds_dwordx4 v[222:223], off
	v_lshl_add_u64 v[222:223], v[214:215], 0, s[16:17]
	s_add_i32 m0, s26, 0x2000
	s_add_i32 s26, s82, s35
	global_load_lds_dwordx4 v[222:223], off
	v_lshl_add_u64 v[222:223], v[214:215], 0, s[20:21]
	s_mov_b32 m0, s26
	v_lshl_add_u64 v[214:215], v[214:215], 0, s[22:23]
	global_load_lds_dwordx4 v[222:223], off
	s_add_i32 m0, s26, 0x2000
	s_nop 0
	global_load_lds_dwordx4 v[214:215], off
	v_lshl_add_u64 v[214:215], v[216:217], 0, s[18:19]
	s_mov_b32 m0, s68
	s_nop 0
	global_load_lds_dwordx4 v[214:215], off
	v_lshl_add_u64 v[214:215], v[220:221], 0, s[18:19]
	s_mov_b32 m0, s69
	s_nop 0
	global_load_lds_dwordx4 v[214:215], off
	s_setprio 1
	s_waitcnt vmcnt(8)
	s_waitcnt lgkmcnt(0)
	s_barrier
	v_mfma_f32_16x16x32_bf16 v[62:65], v[144:147], v[182:185], v[62:65]
	v_mfma_f32_16x16x32_bf16 v[58:61], v[152:155], v[182:185], v[58:61]
	v_mfma_f32_16x16x32_bf16 v[54:57], v[144:147], v[190:193], v[54:57]
	v_mfma_f32_16x16x32_bf16 v[46:49], v[152:155], v[190:193], v[46:49]
	v_mfma_f32_16x16x32_bf16 v[38:41], v[144:147], v[198:201], v[38:41]
	v_mfma_f32_16x16x32_bf16 v[30:33], v[152:155], v[198:201], v[30:33]
	v_mfma_f32_16x16x32_bf16 v[22:25], v[144:147], v[206:209], v[22:25]
	v_mfma_f32_16x16x32_bf16 v[14:17], v[152:155], v[206:209], v[14:17]
	v_mfma_f32_16x16x32_bf16 v[62:65], v[148:151], v[186:189], v[62:65]
	v_mfma_f32_16x16x32_bf16 v[58:61], v[162:165], v[186:189], v[58:61]
	v_mfma_f32_16x16x32_bf16 v[54:57], v[148:151], v[194:197], v[54:57]
	v_mfma_f32_16x16x32_bf16 v[46:49], v[162:165], v[194:197], v[46:49]
	v_mfma_f32_16x16x32_bf16 v[38:41], v[148:151], v[202:205], v[38:41]
	v_mfma_f32_16x16x32_bf16 v[30:33], v[162:165], v[202:205], v[30:33]
	v_mfma_f32_16x16x32_bf16 v[22:25], v[148:151], v[210:213], v[22:25]
	v_mfma_f32_16x16x32_bf16 v[14:17], v[162:165], v[210:213], v[14:17]
	v_mfma_f32_16x16x32_bf16 v[50:53], v[166:169], v[182:185], v[50:53]
	v_mfma_f32_16x16x32_bf16 v[42:45], v[174:177], v[182:185], v[42:45]
	v_mfma_f32_16x16x32_bf16 v[34:37], v[166:169], v[190:193], v[34:37]
	v_mfma_f32_16x16x32_bf16 v[26:29], v[174:177], v[190:193], v[26:29]
	v_mfma_f32_16x16x32_bf16 v[18:21], v[166:169], v[198:201], v[18:21]
	v_mfma_f32_16x16x32_bf16 v[10:13], v[174:177], v[198:201], v[10:13]
	v_mfma_f32_16x16x32_bf16 v[6:9], v[166:169], v[206:209], v[6:9]
	v_mfma_f32_16x16x32_bf16 v[2:5], v[174:177], v[206:209], v[2:5]
	v_mfma_f32_16x16x32_bf16 v[50:53], v[170:173], v[186:189], v[50:53]
	v_mfma_f32_16x16x32_bf16 v[42:45], v[178:181], v[186:189], v[42:45]
	v_mfma_f32_16x16x32_bf16 v[34:37], v[170:173], v[194:197], v[34:37]
	v_mfma_f32_16x16x32_bf16 v[26:29], v[178:181], v[194:197], v[26:29]
	v_mfma_f32_16x16x32_bf16 v[18:21], v[170:173], v[202:205], v[18:21]
	v_mfma_f32_16x16x32_bf16 v[10:13], v[178:181], v[202:205], v[10:13]
	v_mfma_f32_16x16x32_bf16 v[6:9], v[170:173], v[210:213], v[6:9]
	v_mfma_f32_16x16x32_bf16 v[2:5], v[178:181], v[210:213], v[2:5]
	s_barrier
	s_setprio 0
	s_add_i32 s80, s80, 2
	s_add_u32 s74, s74, 0x10000
	s_addc_u32 s75, s75, 0
	s_add_u32 s58, s58, 0x100
	s_addc_u32 s59, s59, 0
	s_cmp_gt_u32 s80, 29
	s_cbranch_scc0 .LBB0_1271
	s_and_b64 vcc, exec, s[24:25]
	s_cbranch_vccz .LBB0_1274
	s_barrier
	s_setprio 3

.LBB0_1496:
	s_lshl_b64 s[50:51], s[48:49], 19
	s_add_u32 s50, s59, s50
	s_addc_u32 s51, s60, s51
	s_and_b64 s[4:5], s[4:5], exec
	s_cselect_b32 s2, s51, s57
	s_cselect_b32 s47, s50, s56
	s_add_u32 s4, s56, 0x40080
	v_lshl_add_u64 v[176:177], v[2:3], 0, s[40:41]
	s_addc_u32 s5, s57, 0
	s_mov_b32 s49, -2
	ds_read_b128 v[26:29], v186
	ds_read_b128 v[30:33], v186 offset:1024
	ds_read_b128 v[18:21], v186 offset:2048
	ds_read_b128 v[22:25], v186 offset:3072
	ds_read_b128 v[10:13], v187
	ds_read_b128 v[14:17], v187 offset:1024
	ds_read_b128 v[2:5], v187 offset:2048
	ds_read_b128 v[6:9], v187 offset:3072
	s_add_u32 s56, s4, 0xfffc0080
	s_addc_u32 s57, s5, -1
	s_cmp_eq_u32 s49, 12
	s_cselect_b64 vcc, -1, 0
	s_cselect_b32 s57, s2, s57
	s_cselect_b32 s56, s47, s56
	v_cndmask_b32_e32 v179, v177, v175, vcc
	v_cndmask_b32_e32 v178, v176, v174, vcc
	v_lshl_add_u64 v[180:181], s[4:5], 0, v[168:169]
	s_add_i32 m0, s62, 0xc000
	ds_read_b128 v[192:195], v188
	ds_read_b128 v[196:199], v188 offset:1024
	ds_read_b128 v[200:203], v188 offset:2048
	ds_read_b128 v[204:207], v188 offset:3072
	ds_read_b128 v[208:211], v188 offset:4096
	ds_read_b128 v[212:215], v188 offset:5120
	ds_read_b128 v[220:223], v188 offset:6144
	ds_read_b128 v[224:227], v188 offset:7168
	global_load_lds_dwordx4 v[180:181], off
	v_lshl_add_u64 v[180:181], s[4:5], 0, v[170:171]
	s_add_i32 m0, s62, 0xe000
	s_nop 0
	global_load_lds_dwordx4 v[180:181], off
	s_setprio 1
	s_waitcnt vmcnt(16)
	s_waitcnt lgkmcnt(0)
	s_barrier
	v_mfma_scale_f32_16x16x128_f8f6f4 v[158:161], v[26:33], v[192:199], 0, v189, v190 op_sel_hi:[0,0,0]
	v_mfma_scale_f32_16x16x128_f8f6f4 v[150:153], v[18:25], v[192:199], 0, v189, v190 op_sel_hi:[0,0,0]
	v_mfma_scale_f32_16x16x128_f8f6f4 v[142:145], v[26:33], v[200:207], 0, v189, v190 op_sel_hi:[0,0,0]
	v_mfma_scale_f32_16x16x128_f8f6f4 v[134:137], v[18:25], v[200:207], 0, v189, v190 op_sel_hi:[0,0,0]
	v_mfma_scale_f32_16x16x128_f8f6f4 v[126:129], v[26:33], v[208:215], 0, v189, v190 op_sel_hi:[0,0,0]
	v_mfma_scale_f32_16x16x128_f8f6f4 v[118:121], v[18:25], v[208:215], 0, v189, v190 op_sel_hi:[0,0,0]
	v_mfma_scale_f32_16x16x128_f8f6f4 v[110:113], v[26:33], v[220:227], 0, v189, v190 op_sel_hi:[0,0,0]
	v_mfma_scale_f32_16x16x128_f8f6f4 v[102:105], v[18:25], v[220:227], 0, v189, v190 op_sel_hi:[0,0,0]
	v_mfma_scale_f32_16x16x128_f8f6f4 v[154:157], v[10:17], v[192:199], 0, v189, v190 op_sel_hi:[0,0,0]
	v_mfma_scale_f32_16x16x128_f8f6f4 v[146:149], v[2:9], v[192:199], 0, v189, v190 op_sel_hi:[0,0,0]
	v_mfma_scale_f32_16x16x128_f8f6f4 v[138:141], v[10:17], v[200:207], 0, v189, v190 op_sel_hi:[0,0,0]
	v_mfma_scale_f32_16x16x128_f8f6f4 v[130:133], v[2:9], v[200:207], 0, v189, v190 op_sel_hi:[0,0,0]
	v_mfma_scale_f32_16x16x128_f8f6f4 v[122:125], v[10:17], v[208:215], 0, v189, v190 op_sel_hi:[0,0,0]
	v_mfma_scale_f32_16x16x128_f8f6f4 v[114:117], v[2:9], v[208:215], 0, v189, v190 op_sel_hi:[0,0,0]
	v_mfma_scale_f32_16x16x128_f8f6f4 v[106:109], v[10:17], v[220:227], 0, v189, v190 op_sel_hi:[0,0,0]
	v_mfma_scale_f32_16x16x128_f8f6f4 v[98:101], v[2:9], v[220:227], 0, v189, v190 op_sel_hi:[0,0,0]
	s_barrier
	s_setprio 0
	s_add_i32 s73, s69, s61
	v_lshl_add_u64 v[178:179], v[178:179], 0, v[162:163]
	s_mov_b32 m0, s73
	ds_read_b128 v[192:195], v188 offset:16384
	ds_read_b128 v[196:199], v188 offset:17408
	ds_read_b128 v[200:203], v188 offset:18432
	ds_read_b128 v[204:207], v188 offset:19456
	ds_read_b128 v[208:211], v188 offset:20480
	ds_read_b128 v[212:215], v188 offset:21504
	ds_read_b128 v[220:223], v188 offset:22528
	ds_read_b128 v[224:227], v188 offset:23552
	global_load_lds_dwordx4 v[178:179], off
	v_lshl_add_u64 v[180:181], v[178:179], 0, s[10:11]
	s_add_i32 m0, s73, 0x2000
	s_add_i32 s73, s70, s61
	global_load_lds_dwordx4 v[180:181], off
	v_lshl_add_u64 v[180:181], v[178:179], 0, s[12:13]
	s_mov_b32 m0, s73
	v_lshl_add_u64 v[182:183], s[56:57], 0, v[166:167]
	global_load_lds_dwordx4 v[180:181], off
	v_lshl_add_u64 v[180:181], v[178:179], 0, s[14:15]
	s_add_i32 m0, s73, 0x2000
	s_nop 0
	global_load_lds_dwordx4 v[180:181], off
	v_lshl_add_u64 v[180:181], s[56:57], 0, v[164:165]
	s_mov_b32 m0, s62
	s_nop 0
	global_load_lds_dwordx4 v[180:181], off
	s_mov_b32 m0, s53
	s_nop 0
	global_load_lds_dwordx4 v[182:183], off
	s_setprio 1
	s_waitcnt vmcnt(16)
	s_waitcnt lgkmcnt(0)
	s_barrier
	v_mfma_scale_f32_16x16x128_f8f6f4 v[94:97], v[26:33], v[192:199], 0, v189, v190 op_sel_hi:[0,0,0]
	v_mfma_scale_f32_16x16x128_f8f6f4 v[86:89], v[18:25], v[192:199], 0, v189, v190 op_sel_hi:[0,0,0]
	v_mfma_scale_f32_16x16x128_f8f6f4 v[78:81], v[26:33], v[200:207], 0, v189, v190 op_sel_hi:[0,0,0]
	v_mfma_scale_f32_16x16x128_f8f6f4 v[70:73], v[18:25], v[200:207], 0, v189, v190 op_sel_hi:[0,0,0]
	v_mfma_scale_f32_16x16x128_f8f6f4 v[62:65], v[26:33], v[208:215], 0, v189, v190 op_sel_hi:[0,0,0]
	v_mfma_scale_f32_16x16x128_f8f6f4 v[54:57], v[18:25], v[208:215], 0, v189, v190 op_sel_hi:[0,0,0]
	v_mfma_scale_f32_16x16x128_f8f6f4 v[46:49], v[26:33], v[220:227], 0, v189, v190 op_sel_hi:[0,0,0]
	v_mfma_scale_f32_16x16x128_f8f6f4 v[38:41], v[18:25], v[220:227], 0, v189, v190 op_sel_hi:[0,0,0]
	v_mfma_scale_f32_16x16x128_f8f6f4 v[90:93], v[10:17], v[192:199], 0, v189, v190 op_sel_hi:[0,0,0]
	v_mfma_scale_f32_16x16x128_f8f6f4 v[82:85], v[2:9], v[192:199], 0, v189, v190 op_sel_hi:[0,0,0]
	v_mfma_scale_f32_16x16x128_f8f6f4 v[74:77], v[10:17], v[200:207], 0, v189, v190 op_sel_hi:[0,0,0]
	v_mfma_scale_f32_16x16x128_f8f6f4 v[66:69], v[2:9], v[200:207], 0, v189, v190 op_sel_hi:[0,0,0]
	v_mfma_scale_f32_16x16x128_f8f6f4 v[58:61], v[10:17], v[208:215], 0, v189, v190 op_sel_hi:[0,0,0]
	v_mfma_scale_f32_16x16x128_f8f6f4 v[50:53], v[2:9], v[208:215], 0, v189, v190 op_sel_hi:[0,0,0]
	v_mfma_scale_f32_16x16x128_f8f6f4 v[42:45], v[10:17], v[220:227], 0, v189, v190 op_sel_hi:[0,0,0]
	v_mfma_scale_f32_16x16x128_f8f6f4 v[34:37], v[2:9], v[220:227], 0, v189, v190 op_sel_hi:[0,0,0]
	s_barrier
	s_setprio 0
	s_add_i32 s73, 0, 0x18000
	s_add_i32 s74, 0, 0x1c000
	v_add_u32_e32 v14, s73, v184
	v_add_u32_e32 v30, s74, v184
	ds_read_b128 v[2:5], v14
	ds_read_b128 v[6:9], v14 offset:1024
	ds_read_b128 v[10:13], v14 offset:2048
	ds_read_b128 v[14:17], v14 offset:3072
	ds_read_b128 v[18:21], v30
	ds_read_b128 v[22:25], v30 offset:1024
	ds_read_b128 v[26:29], v30 offset:2048
	ds_read_b128 v[30:33], v30 offset:3072
	s_add_u32 s56, s56, 0x40000
	s_addc_u32 s57, s57, 0
	s_mov_b32 m0, s63
	v_lshl_add_u64 v[216:217], s[56:57], 0, v[164:165]
	ds_read_b128 v[192:195], v188 offset:32768
	ds_read_b128 v[196:199], v188 offset:33792
	ds_read_b128 v[200:203], v188 offset:34816
	ds_read_b128 v[204:207], v188 offset:35840
	ds_read_b128 v[208:211], v188 offset:36864
	ds_read_b128 v[212:215], v188 offset:37888
	ds_read_b128 v[220:223], v188 offset:38912
	ds_read_b128 v[224:227], v188 offset:39936
	global_load_lds_dwordx4 v[216:217], off
	v_lshl_add_u64 v[216:217], s[56:57], 0, v[166:167]
	s_mov_b32 m0, s64
	s_nop 0
	global_load_lds_dwordx4 v[216:217], off
	s_setprio 1
	s_waitcnt vmcnt(8)
	s_waitcnt lgkmcnt(0)
	s_barrier
	v_mfma_scale_f32_16x16x128_f8f6f4 v[158:161], v[2:9], v[192:199], v[158:161], v189, v190 op_sel_hi:[0,0,0]
	v_mfma_scale_f32_16x16x128_f8f6f4 v[150:153], v[10:17], v[192:199], v[150:153], v189, v190 op_sel_hi:[0,0,0]
	v_mfma_scale_f32_16x16x128_f8f6f4 v[142:145], v[2:9], v[200:207], v[142:145], v189, v190 op_sel_hi:[0,0,0]
	v_mfma_scale_f32_16x16x128_f8f6f4 v[134:137], v[10:17], v[200:207], v[134:137], v189, v190 op_sel_hi:[0,0,0]
	v_mfma_scale_f32_16x16x128_f8f6f4 v[126:129], v[2:9], v[208:215], v[126:129], v189, v190 op_sel_hi:[0,0,0]
	v_mfma_scale_f32_16x16x128_f8f6f4 v[118:121], v[10:17], v[208:215], v[118:121], v189, v190 op_sel_hi:[0,0,0]
	v_mfma_scale_f32_16x16x128_f8f6f4 v[110:113], v[2:9], v[220:227], v[110:113], v189, v190 op_sel_hi:[0,0,0]
	v_mfma_scale_f32_16x16x128_f8f6f4 v[102:105], v[10:17], v[220:227], v[102:105], v189, v190 op_sel_hi:[0,0,0]
	v_mfma_scale_f32_16x16x128_f8f6f4 v[154:157], v[18:25], v[192:199], v[154:157], v189, v190 op_sel_hi:[0,0,0]
	v_mfma_scale_f32_16x16x128_f8f6f4 v[146:149], v[26:33], v[192:199], v[146:149], v189, v190 op_sel_hi:[0,0,0]
	v_mfma_scale_f32_16x16x128_f8f6f4 v[138:141], v[18:25], v[200:207], v[138:141], v189, v190 op_sel_hi:[0,0,0]
	v_mfma_scale_f32_16x16x128_f8f6f4 v[130:133], v[26:33], v[200:207], v[130:133], v189, v190 op_sel_hi:[0,0,0]
	v_mfma_scale_f32_16x16x128_f8f6f4 v[122:125], v[18:25], v[208:215], v[122:125], v189, v190 op_sel_hi:[0,0,0]
	v_mfma_scale_f32_16x16x128_f8f6f4 v[114:117], v[26:33], v[208:215], v[114:117], v189, v190 op_sel_hi:[0,0,0]
	v_mfma_scale_f32_16x16x128_f8f6f4 v[106:109], v[18:25], v[220:227], v[106:109], v189, v190 op_sel_hi:[0,0,0]
	v_mfma_scale_f32_16x16x128_f8f6f4 v[98:101], v[26:33], v[220:227], v[98:101], v189, v190 op_sel_hi:[0,0,0]
	s_barrier
	s_setprio 0
	s_add_i32 s56, s73, s61
	v_lshl_add_u64 v[216:217], v[178:179], 0, s[20:21]
	s_mov_b32 m0, s56
	ds_read_b128 v[192:195], v188 offset:49152
	ds_read_b128 v[196:199], v188 offset:50176
	ds_read_b128 v[200:203], v188 offset:51200
	ds_read_b128 v[204:207], v188 offset:52224
	ds_read_b128 v[208:211], v188 offset:53248
	ds_read_b128 v[212:215], v188 offset:54272
	ds_read_b128 v[220:223], v188 offset:55296
	ds_read_b128 v[224:227], v188 offset:56320
	global_load_lds_dwordx4 v[216:217], off
	v_lshl_add_u64 v[216:217], v[178:179], 0, s[22:23]
	s_add_i32 m0, s56, 0x2000
	s_add_i32 s56, s74, s61
	global_load_lds_dwordx4 v[216:217], off
	v_lshl_add_u64 v[216:217], v[178:179], 0, s[26:27]
	s_mov_b32 m0, s56
	v_lshl_add_u64 v[178:179], v[178:179], 0, s[36:37]
	global_load_lds_dwordx4 v[216:217], off
	s_add_i32 m0, s56, 0x2000
	s_nop 0
	global_load_lds_dwordx4 v[178:179], off
	v_lshl_add_u64 v[178:179], v[180:181], 0, s[24:25]
	s_mov_b32 m0, s66
	s_nop 0
	global_load_lds_dwordx4 v[178:179], off
	v_lshl_add_u64 v[178:179], v[182:183], 0, s[24:25]
	s_mov_b32 m0, s67
	s_nop 0
	global_load_lds_dwordx4 v[178:179], off
	s_setprio 1
	s_waitcnt vmcnt(8)
	s_waitcnt lgkmcnt(0)
	s_barrier
	v_mfma_scale_f32_16x16x128_f8f6f4 v[94:97], v[2:9], v[192:199], v[94:97], v189, v190 op_sel_hi:[0,0,0]
	v_mfma_scale_f32_16x16x128_f8f6f4 v[86:89], v[10:17], v[192:199], v[86:89], v189, v190 op_sel_hi:[0,0,0]
	v_mfma_scale_f32_16x16x128_f8f6f4 v[78:81], v[2:9], v[200:207], v[78:81], v189, v190 op_sel_hi:[0,0,0]
	v_mfma_scale_f32_16x16x128_f8f6f4 v[70:73], v[10:17], v[200:207], v[70:73], v189, v190 op_sel_hi:[0,0,0]
	v_mfma_scale_f32_16x16x128_f8f6f4 v[62:65], v[2:9], v[208:215], v[62:65], v189, v190 op_sel_hi:[0,0,0]
	v_mfma_scale_f32_16x16x128_f8f6f4 v[54:57], v[10:17], v[208:215], v[54:57], v189, v190 op_sel_hi:[0,0,0]
	v_mfma_scale_f32_16x16x128_f8f6f4 v[46:49], v[2:9], v[220:227], v[46:49], v189, v190 op_sel_hi:[0,0,0]
	v_mfma_scale_f32_16x16x128_f8f6f4 v[38:41], v[10:17], v[220:227], v[38:41], v189, v190 op_sel_hi:[0,0,0]
	v_mfma_scale_f32_16x16x128_f8f6f4 v[90:93], v[18:25], v[192:199], v[90:93], v189, v190 op_sel_hi:[0,0,0]
	v_mfma_scale_f32_16x16x128_f8f6f4 v[82:85], v[26:33], v[192:199], v[82:85], v189, v190 op_sel_hi:[0,0,0]
	v_mfma_scale_f32_16x16x128_f8f6f4 v[74:77], v[18:25], v[200:207], v[74:77], v189, v190 op_sel_hi:[0,0,0]
	v_mfma_scale_f32_16x16x128_f8f6f4 v[66:69], v[26:33], v[200:207], v[66:69], v189, v190 op_sel_hi:[0,0,0]
	v_mfma_scale_f32_16x16x128_f8f6f4 v[58:61], v[18:25], v[208:215], v[58:61], v189, v190 op_sel_hi:[0,0,0]
	v_mfma_scale_f32_16x16x128_f8f6f4 v[50:53], v[26:33], v[208:215], v[50:53], v189, v190 op_sel_hi:[0,0,0]
	v_mfma_scale_f32_16x16x128_f8f6f4 v[42:45], v[18:25], v[220:227], v[42:45], v189, v190 op_sel_hi:[0,0,0]
	v_mfma_scale_f32_16x16x128_f8f6f4 v[34:37], v[26:33], v[220:227], v[34:37], v189, v190 op_sel_hi:[0,0,0]
	s_barrier
	s_setprio 0
	s_add_i32 s49, s49, 2
	s_add_u32 s4, s4, 0x100
	s_addc_u32 s5, s5, 0
	s_cmp_gt_u32 s49, 13
	v_lshl_add_u64 v[176:177], v[176:177], 0, s[40:41]
.LBB0_1497:
	ds_read_b128 v[26:29], v186
	ds_read_b128 v[30:33], v186 offset:1024
	ds_read_b128 v[18:21], v186 offset:2048
	ds_read_b128 v[22:25], v186 offset:3072
	ds_read_b128 v[10:13], v187
	ds_read_b128 v[14:17], v187 offset:1024
	ds_read_b128 v[2:5], v187 offset:2048
	ds_read_b128 v[6:9], v187 offset:3072
	s_add_u32 s56, s4, 0xfffc0080
	s_addc_u32 s57, s5, -1
	s_cmp_eq_u32 s49, 12
	s_cselect_b64 vcc, -1, 0
	s_cselect_b32 s57, s2, s57
	s_cselect_b32 s56, s47, s56
	v_cndmask_b32_e32 v179, v177, v175, vcc
	v_cndmask_b32_e32 v178, v176, v174, vcc
	v_lshl_add_u64 v[180:181], s[4:5], 0, v[168:169]
	s_add_i32 m0, s62, 0xc000
	ds_read_b128 v[192:195], v188
	ds_read_b128 v[196:199], v188 offset:1024
	ds_read_b128 v[200:203], v188 offset:2048
	ds_read_b128 v[204:207], v188 offset:3072
	ds_read_b128 v[208:211], v188 offset:4096
	ds_read_b128 v[212:215], v188 offset:5120
	ds_read_b128 v[220:223], v188 offset:6144
	ds_read_b128 v[224:227], v188 offset:7168
	global_load_lds_dwordx4 v[180:181], off
	v_lshl_add_u64 v[180:181], s[4:5], 0, v[170:171]
	s_add_i32 m0, s62, 0xe000
	s_nop 0
	global_load_lds_dwordx4 v[180:181], off
	s_setprio 1
	s_waitcnt vmcnt(8)
	s_waitcnt lgkmcnt(0)
	s_barrier
	v_mfma_scale_f32_16x16x128_f8f6f4 v[158:161], v[26:33], v[192:199], v[158:161], v189, v190 op_sel_hi:[0,0,0]
	v_mfma_scale_f32_16x16x128_f8f6f4 v[150:153], v[18:25], v[192:199], v[150:153], v189, v190 op_sel_hi:[0,0,0]
	v_mfma_scale_f32_16x16x128_f8f6f4 v[142:145], v[26:33], v[200:207], v[142:145], v189, v190 op_sel_hi:[0,0,0]
	v_mfma_scale_f32_16x16x128_f8f6f4 v[134:137], v[18:25], v[200:207], v[134:137], v189, v190 op_sel_hi:[0,0,0]
	v_mfma_scale_f32_16x16x128_f8f6f4 v[126:129], v[26:33], v[208:215], v[126:129], v189, v190 op_sel_hi:[0,0,0]
	v_mfma_scale_f32_16x16x128_f8f6f4 v[118:121], v[18:25], v[208:215], v[118:121], v189, v190 op_sel_hi:[0,0,0]
	v_mfma_scale_f32_16x16x128_f8f6f4 v[110:113], v[26:33], v[220:227], v[110:113], v189, v190 op_sel_hi:[0,0,0]
	v_mfma_scale_f32_16x16x128_f8f6f4 v[102:105], v[18:25], v[220:227], v[102:105], v189, v190 op_sel_hi:[0,0,0]
	v_mfma_scale_f32_16x16x128_f8f6f4 v[154:157], v[10:17], v[192:199], v[154:157], v189, v190 op_sel_hi:[0,0,0]
	v_mfma_scale_f32_16x16x128_f8f6f4 v[146:149], v[2:9], v[192:199], v[146:149], v189, v190 op_sel_hi:[0,0,0]
	v_mfma_scale_f32_16x16x128_f8f6f4 v[138:141], v[10:17], v[200:207], v[138:141], v189, v190 op_sel_hi:[0,0,0]
	v_mfma_scale_f32_16x16x128_f8f6f4 v[130:133], v[2:9], v[200:207], v[130:133], v189, v190 op_sel_hi:[0,0,0]
	v_mfma_scale_f32_16x16x128_f8f6f4 v[122:125], v[10:17], v[208:215], v[122:125], v189, v190 op_sel_hi:[0,0,0]
	v_mfma_scale_f32_16x16x128_f8f6f4 v[114:117], v[2:9], v[208:215], v[114:117], v189, v190 op_sel_hi:[0,0,0]
	v_mfma_scale_f32_16x16x128_f8f6f4 v[106:109], v[10:17], v[220:227], v[106:109], v189, v190 op_sel_hi:[0,0,0]
	v_mfma_scale_f32_16x16x128_f8f6f4 v[98:101], v[2:9], v[220:227], v[98:101], v189, v190 op_sel_hi:[0,0,0]
	s_barrier
	s_setprio 0
	s_add_i32 s73, s69, s61
	v_lshl_add_u64 v[178:179], v[178:179], 0, v[162:163]
	s_mov_b32 m0, s73
	ds_read_b128 v[192:195], v188 offset:16384
	ds_read_b128 v[196:199], v188 offset:17408
	ds_read_b128 v[200:203], v188 offset:18432
	ds_read_b128 v[204:207], v188 offset:19456
	ds_read_b128 v[208:211], v188 offset:20480
	ds_read_b128 v[212:215], v188 offset:21504
	ds_read_b128 v[220:223], v188 offset:22528
	ds_read_b128 v[224:227], v188 offset:23552
	global_load_lds_dwordx4 v[178:179], off
	v_lshl_add_u64 v[180:181], v[178:179], 0, s[10:11]
	s_add_i32 m0, s73, 0x2000
	s_add_i32 s73, s70, s61
	global_load_lds_dwordx4 v[180:181], off
	v_lshl_add_u64 v[180:181], v[178:179], 0, s[12:13]
	s_mov_b32 m0, s73
	v_lshl_add_u64 v[182:183], s[56:57], 0, v[166:167]
	global_load_lds_dwordx4 v[180:181], off
	v_lshl_add_u64 v[180:181], v[178:179], 0, s[14:15]
	s_add_i32 m0, s73, 0x2000
	s_nop 0
	global_load_lds_dwordx4 v[180:181], off
	v_lshl_add_u64 v[180:181], s[56:57], 0, v[164:165]
	s_mov_b32 m0, s62
	s_nop 0
	global_load_lds_dwordx4 v[180:181], off
	s_mov_b32 m0, s53
	s_nop 0
	global_load_lds_dwordx4 v[182:183], off
	s_setprio 1
	s_waitcnt vmcnt(8)
	s_waitcnt lgkmcnt(0)
	s_barrier
	v_mfma_scale_f32_16x16x128_f8f6f4 v[94:97], v[26:33], v[192:199], v[94:97], v189, v190 op_sel_hi:[0,0,0]
	v_mfma_scale_f32_16x16x128_f8f6f4 v[86:89], v[18:25], v[192:199], v[86:89], v189, v190 op_sel_hi:[0,0,0]
	v_mfma_scale_f32_16x16x128_f8f6f4 v[78:81], v[26:33], v[200:207], v[78:81], v189, v190 op_sel_hi:[0,0,0]
	v_mfma_scale_f32_16x16x128_f8f6f4 v[70:73], v[18:25], v[200:207], v[70:73], v189, v190 op_sel_hi:[0,0,0]
	v_mfma_scale_f32_16x16x128_f8f6f4 v[62:65], v[26:33], v[208:215], v[62:65], v189, v190 op_sel_hi:[0,0,0]
	v_mfma_scale_f32_16x16x128_f8f6f4 v[54:57], v[18:25], v[208:215], v[54:57], v189, v190 op_sel_hi:[0,0,0]
	v_mfma_scale_f32_16x16x128_f8f6f4 v[46:49], v[26:33], v[220:227], v[46:49], v189, v190 op_sel_hi:[0,0,0]
	v_mfma_scale_f32_16x16x128_f8f6f4 v[38:41], v[18:25], v[220:227], v[38:41], v189, v190 op_sel_hi:[0,0,0]
	v_mfma_scale_f32_16x16x128_f8f6f4 v[90:93], v[10:17], v[192:199], v[90:93], v189, v190 op_sel_hi:[0,0,0]
	v_mfma_scale_f32_16x16x128_f8f6f4 v[82:85], v[2:9], v[192:199], v[82:85], v189, v190 op_sel_hi:[0,0,0]
	v_mfma_scale_f32_16x16x128_f8f6f4 v[74:77], v[10:17], v[200:207], v[74:77], v189, v190 op_sel_hi:[0,0,0]
	v_mfma_scale_f32_16x16x128_f8f6f4 v[66:69], v[2:9], v[200:207], v[66:69], v189, v190 op_sel_hi:[0,0,0]
	v_mfma_scale_f32_16x16x128_f8f6f4 v[58:61], v[10:17], v[208:215], v[58:61], v189, v190 op_sel_hi:[0,0,0]
	v_mfma_scale_f32_16x16x128_f8f6f4 v[50:53], v[2:9], v[208:215], v[50:53], v189, v190 op_sel_hi:[0,0,0]
	v_mfma_scale_f32_16x16x128_f8f6f4 v[42:45], v[10:17], v[220:227], v[42:45], v189, v190 op_sel_hi:[0,0,0]
	v_mfma_scale_f32_16x16x128_f8f6f4 v[34:37], v[2:9], v[220:227], v[34:37], v189, v190 op_sel_hi:[0,0,0]
	s_barrier
	s_setprio 0
	s_add_i32 s73, 0, 0x18000
	s_add_i32 s74, 0, 0x1c000
	v_add_u32_e32 v14, s73, v184
	v_add_u32_e32 v30, s74, v184
	ds_read_b128 v[2:5], v14
	ds_read_b128 v[6:9], v14 offset:1024
	ds_read_b128 v[10:13], v14 offset:2048
	ds_read_b128 v[14:17], v14 offset:3072
	ds_read_b128 v[18:21], v30
	ds_read_b128 v[22:25], v30 offset:1024
	ds_read_b128 v[26:29], v30 offset:2048
	ds_read_b128 v[30:33], v30 offset:3072
	s_add_u32 s56, s56, 0x40000
	s_addc_u32 s57, s57, 0
	s_mov_b32 m0, s63
	v_lshl_add_u64 v[216:217], s[56:57], 0, v[164:165]
	ds_read_b128 v[192:195], v188 offset:32768
	ds_read_b128 v[196:199], v188 offset:33792
	ds_read_b128 v[200:203], v188 offset:34816
	ds_read_b128 v[204:207], v188 offset:35840
	ds_read_b128 v[208:211], v188 offset:36864
	ds_read_b128 v[212:215], v188 offset:37888
	ds_read_b128 v[220:223], v188 offset:38912
	ds_read_b128 v[224:227], v188 offset:39936
	global_load_lds_dwordx4 v[216:217], off
	v_lshl_add_u64 v[216:217], s[56:57], 0, v[166:167]
	s_mov_b32 m0, s64
	s_nop 0
	global_load_lds_dwordx4 v[216:217], off
	s_setprio 1
	s_waitcnt vmcnt(8)
	s_waitcnt lgkmcnt(0)
	s_barrier
	v_mfma_scale_f32_16x16x128_f8f6f4 v[158:161], v[2:9], v[192:199], v[158:161], v189, v190 op_sel_hi:[0,0,0]
	v_mfma_scale_f32_16x16x128_f8f6f4 v[150:153], v[10:17], v[192:199], v[150:153], v189, v190 op_sel_hi:[0,0,0]
	v_mfma_scale_f32_16x16x128_f8f6f4 v[142:145], v[2:9], v[200:207], v[142:145], v189, v190 op_sel_hi:[0,0,0]
	v_mfma_scale_f32_16x16x128_f8f6f4 v[134:137], v[10:17], v[200:207], v[134:137], v189, v190 op_sel_hi:[0,0,0]
	v_mfma_scale_f32_16x16x128_f8f6f4 v[126:129], v[2:9], v[208:215], v[126:129], v189, v190 op_sel_hi:[0,0,0]
	v_mfma_scale_f32_16x16x128_f8f6f4 v[118:121], v[10:17], v[208:215], v[118:121], v189, v190 op_sel_hi:[0,0,0]
	v_mfma_scale_f32_16x16x128_f8f6f4 v[110:113], v[2:9], v[220:227], v[110:113], v189, v190 op_sel_hi:[0,0,0]
	v_mfma_scale_f32_16x16x128_f8f6f4 v[102:105], v[10:17], v[220:227], v[102:105], v189, v190 op_sel_hi:[0,0,0]
	v_mfma_scale_f32_16x16x128_f8f6f4 v[154:157], v[18:25], v[192:199], v[154:157], v189, v190 op_sel_hi:[0,0,0]
	v_mfma_scale_f32_16x16x128_f8f6f4 v[146:149], v[26:33], v[192:199], v[146:149], v189, v190 op_sel_hi:[0,0,0]
	v_mfma_scale_f32_16x16x128_f8f6f4 v[138:141], v[18:25], v[200:207], v[138:141], v189, v190 op_sel_hi:[0,0,0]
	v_mfma_scale_f32_16x16x128_f8f6f4 v[130:133], v[26:33], v[200:207], v[130:133], v189, v190 op_sel_hi:[0,0,0]
	v_mfma_scale_f32_16x16x128_f8f6f4 v[122:125], v[18:25], v[208:215], v[122:125], v189, v190 op_sel_hi:[0,0,0]
	v_mfma_scale_f32_16x16x128_f8f6f4 v[114:117], v[26:33], v[208:215], v[114:117], v189, v190 op_sel_hi:[0,0,0]
	v_mfma_scale_f32_16x16x128_f8f6f4 v[106:109], v[18:25], v[220:227], v[106:109], v189, v190 op_sel_hi:[0,0,0]
	v_mfma_scale_f32_16x16x128_f8f6f4 v[98:101], v[26:33], v[220:227], v[98:101], v189, v190 op_sel_hi:[0,0,0]
	s_barrier
	s_setprio 0
	s_add_i32 s56, s73, s61
	v_lshl_add_u64 v[216:217], v[178:179], 0, s[20:21]
	s_mov_b32 m0, s56
	ds_read_b128 v[192:195], v188 offset:49152
	ds_read_b128 v[196:199], v188 offset:50176
	ds_read_b128 v[200:203], v188 offset:51200
	ds_read_b128 v[204:207], v188 offset:52224
	ds_read_b128 v[208:211], v188 offset:53248
	ds_read_b128 v[212:215], v188 offset:54272
	ds_read_b128 v[220:223], v188 offset:55296
	ds_read_b128 v[224:227], v188 offset:56320
	global_load_lds_dwordx4 v[216:217], off
	v_lshl_add_u64 v[216:217], v[178:179], 0, s[22:23]
	s_add_i32 m0, s56, 0x2000
	s_add_i32 s56, s74, s61
	global_load_lds_dwordx4 v[216:217], off
	v_lshl_add_u64 v[216:217], v[178:179], 0, s[26:27]
	s_mov_b32 m0, s56
	v_lshl_add_u64 v[178:179], v[178:179], 0, s[36:37]
	global_load_lds_dwordx4 v[216:217], off
	s_add_i32 m0, s56, 0x2000
	s_nop 0
	global_load_lds_dwordx4 v[178:179], off
	v_lshl_add_u64 v[178:179], v[180:181], 0, s[24:25]
	s_mov_b32 m0, s66
	s_nop 0
	global_load_lds_dwordx4 v[178:179], off
	v_lshl_add_u64 v[178:179], v[182:183], 0, s[24:25]
	s_mov_b32 m0, s67
	s_nop 0
	global_load_lds_dwordx4 v[178:179], off
	s_setprio 1
	s_waitcnt vmcnt(8)
	s_waitcnt lgkmcnt(0)
	s_barrier
	v_mfma_scale_f32_16x16x128_f8f6f4 v[94:97], v[2:9], v[192:199], v[94:97], v189, v190 op_sel_hi:[0,0,0]
	v_mfma_scale_f32_16x16x128_f8f6f4 v[86:89], v[10:17], v[192:199], v[86:89], v189, v190 op_sel_hi:[0,0,0]
	v_mfma_scale_f32_16x16x128_f8f6f4 v[78:81], v[2:9], v[200:207], v[78:81], v189, v190 op_sel_hi:[0,0,0]
	v_mfma_scale_f32_16x16x128_f8f6f4 v[70:73], v[10:17], v[200:207], v[70:73], v189, v190 op_sel_hi:[0,0,0]
	v_mfma_scale_f32_16x16x128_f8f6f4 v[62:65], v[2:9], v[208:215], v[62:65], v189, v190 op_sel_hi:[0,0,0]
	v_mfma_scale_f32_16x16x128_f8f6f4 v[54:57], v[10:17], v[208:215], v[54:57], v189, v190 op_sel_hi:[0,0,0]
	v_mfma_scale_f32_16x16x128_f8f6f4 v[46:49], v[2:9], v[220:227], v[46:49], v189, v190 op_sel_hi:[0,0,0]
	v_mfma_scale_f32_16x16x128_f8f6f4 v[38:41], v[10:17], v[220:227], v[38:41], v189, v190 op_sel_hi:[0,0,0]
	v_mfma_scale_f32_16x16x128_f8f6f4 v[90:93], v[18:25], v[192:199], v[90:93], v189, v190 op_sel_hi:[0,0,0]
	v_mfma_scale_f32_16x16x128_f8f6f4 v[82:85], v[26:33], v[192:199], v[82:85], v189, v190 op_sel_hi:[0,0,0]
	v_mfma_scale_f32_16x16x128_f8f6f4 v[74:77], v[18:25], v[200:207], v[74:77], v189, v190 op_sel_hi:[0,0,0]
	v_mfma_scale_f32_16x16x128_f8f6f4 v[66:69], v[26:33], v[200:207], v[66:69], v189, v190 op_sel_hi:[0,0,0]
	v_mfma_scale_f32_16x16x128_f8f6f4 v[58:61], v[18:25], v[208:215], v[58:61], v189, v190 op_sel_hi:[0,0,0]
	v_mfma_scale_f32_16x16x128_f8f6f4 v[50:53], v[26:33], v[208:215], v[50:53], v189, v190 op_sel_hi:[0,0,0]
	v_mfma_scale_f32_16x16x128_f8f6f4 v[42:45], v[18:25], v[220:227], v[42:45], v189, v190 op_sel_hi:[0,0,0]
	v_mfma_scale_f32_16x16x128_f8f6f4 v[34:37], v[26:33], v[220:227], v[34:37], v189, v190 op_sel_hi:[0,0,0]
	s_barrier
	s_setprio 0
	s_add_i32 s49, s49, 2
	s_add_u32 s4, s4, 0x100
	s_addc_u32 s5, s5, 0
	s_cmp_gt_u32 s49, 13
	v_lshl_add_u64 v[176:177], v[176:177], 0, s[40:41]
	s_cbranch_scc0 .LBB0_1497
	s_and_b64 vcc, exec, s[38:39]
	s_cbranch_vccz .LBB0_1500
	s_barrier
	s_setprio 3

.LBB0_1567:
	s_add_u32 s56, s56, 0xb0080
	v_lshl_add_u64 v[176:177], v[2:3], 0, s[44:45]
	s_addc_u32 s57, s57, 0
	s_mov_b32 s53, -2
	ds_read_b128 v[26:29], v186
	ds_read_b128 v[30:33], v186 offset:1024
	ds_read_b128 v[18:21], v186 offset:2048
	ds_read_b128 v[22:25], v186 offset:3072
	ds_read_b128 v[10:13], v187
	ds_read_b128 v[14:17], v187 offset:1024
	ds_read_b128 v[2:5], v187 offset:2048
	ds_read_b128 v[6:9], v187 offset:3072
	s_add_u32 s58, s56, 0xfff50080
	s_addc_u32 s59, s57, -1
	s_cmp_eq_u32 s53, 40
	s_cselect_b64 vcc, -1, 0
	s_cselect_b32 s59, s5, s59
	s_cselect_b32 s58, s4, s58
	v_cndmask_b32_e32 v179, v177, v175, vcc
	v_cndmask_b32_e32 v178, v176, v174, vcc
	v_lshl_add_u64 v[180:181], s[56:57], 0, v[170:171]
	s_add_i32 m0, s61, 0xc000
	ds_read_b128 v[192:195], v188
	ds_read_b128 v[196:199], v188 offset:1024
	ds_read_b128 v[200:203], v188 offset:2048
	ds_read_b128 v[204:207], v188 offset:3072
	ds_read_b128 v[208:211], v188 offset:4096
	ds_read_b128 v[212:215], v188 offset:5120
	ds_read_b128 v[220:223], v188 offset:6144
	ds_read_b128 v[224:227], v188 offset:7168
	global_load_lds_dwordx4 v[180:181], off
	v_lshl_add_u64 v[180:181], s[56:57], 0, v[172:173]
	s_add_i32 m0, s61, 0xe000
	s_nop 0
	global_load_lds_dwordx4 v[180:181], off
	s_setprio 1
	s_waitcnt vmcnt(24)
	s_waitcnt lgkmcnt(0)
	s_barrier
	v_mfma_scale_f32_16x16x128_f8f6f4 v[158:161], v[26:33], v[192:199], 0, v189, v190 op_sel_hi:[0,0,0]
	v_mfma_scale_f32_16x16x128_f8f6f4 v[154:157], v[18:25], v[192:199], 0, v189, v190 op_sel_hi:[0,0,0]
	v_mfma_scale_f32_16x16x128_f8f6f4 v[150:153], v[26:33], v[200:207], 0, v189, v190 op_sel_hi:[0,0,0]
	v_mfma_scale_f32_16x16x128_f8f6f4 v[142:145], v[18:25], v[200:207], 0, v189, v190 op_sel_hi:[0,0,0]
	v_mfma_scale_f32_16x16x128_f8f6f4 v[134:137], v[26:33], v[208:215], 0, v189, v190 op_sel_hi:[0,0,0]
	v_mfma_scale_f32_16x16x128_f8f6f4 v[126:129], v[18:25], v[208:215], 0, v189, v190 op_sel_hi:[0,0,0]
	v_mfma_scale_f32_16x16x128_f8f6f4 v[118:121], v[26:33], v[220:227], 0, v189, v190 op_sel_hi:[0,0,0]
	v_mfma_scale_f32_16x16x128_f8f6f4 v[110:113], v[18:25], v[220:227], 0, v189, v190 op_sel_hi:[0,0,0]
	v_mfma_scale_f32_16x16x128_f8f6f4 v[146:149], v[10:17], v[192:199], 0, v189, v190 op_sel_hi:[0,0,0]
	v_mfma_scale_f32_16x16x128_f8f6f4 v[138:141], v[2:9], v[192:199], 0, v189, v190 op_sel_hi:[0,0,0]
	v_mfma_scale_f32_16x16x128_f8f6f4 v[130:133], v[10:17], v[200:207], 0, v189, v190 op_sel_hi:[0,0,0]
	v_mfma_scale_f32_16x16x128_f8f6f4 v[122:125], v[2:9], v[200:207], 0, v189, v190 op_sel_hi:[0,0,0]
	v_mfma_scale_f32_16x16x128_f8f6f4 v[114:117], v[10:17], v[208:215], 0, v189, v190 op_sel_hi:[0,0,0]
	v_mfma_scale_f32_16x16x128_f8f6f4 v[106:109], v[2:9], v[208:215], 0, v189, v190 op_sel_hi:[0,0,0]
	v_mfma_scale_f32_16x16x128_f8f6f4 v[102:105], v[10:17], v[220:227], 0, v189, v190 op_sel_hi:[0,0,0]
	v_mfma_scale_f32_16x16x128_f8f6f4 v[98:101], v[2:9], v[220:227], 0, v189, v190 op_sel_hi:[0,0,0]
	s_barrier
	s_setprio 0
	s_add_i32 s80, s69, s33
	v_lshl_add_u64 v[178:179], v[178:179], 0, v[164:165]
	s_mov_b32 m0, s80
	ds_read_b128 v[192:195], v188 offset:16384
	ds_read_b128 v[196:199], v188 offset:17408
	ds_read_b128 v[200:203], v188 offset:18432
	ds_read_b128 v[204:207], v188 offset:19456
	ds_read_b128 v[208:211], v188 offset:20480
	ds_read_b128 v[212:215], v188 offset:21504
	ds_read_b128 v[220:223], v188 offset:22528
	ds_read_b128 v[224:227], v188 offset:23552
	global_load_lds_dwordx4 v[178:179], off
	v_lshl_add_u64 v[180:181], v[178:179], 0, s[10:11]
	s_add_i32 m0, s80, 0x2000
	s_add_i32 s80, s70, s33
	global_load_lds_dwordx4 v[180:181], off
	v_lshl_add_u64 v[180:181], v[178:179], 0, s[12:13]
	s_mov_b32 m0, s80
	v_lshl_add_u64 v[182:183], s[58:59], 0, v[168:169]
	global_load_lds_dwordx4 v[180:181], off
	v_lshl_add_u64 v[180:181], v[178:179], 0, s[14:15]
	s_add_i32 m0, s80, 0x2000
	s_nop 0
	global_load_lds_dwordx4 v[180:181], off
	v_lshl_add_u64 v[180:181], s[58:59], 0, v[166:167]
	s_mov_b32 m0, s61
	s_nop 0
	global_load_lds_dwordx4 v[180:181], off
	s_mov_b32 m0, s62
	s_nop 0
	global_load_lds_dwordx4 v[182:183], off
	s_setprio 1
	s_waitcnt vmcnt(24)
	s_waitcnt lgkmcnt(0)
	s_barrier
	v_mfma_scale_f32_16x16x128_f8f6f4 v[94:97], v[26:33], v[192:199], 0, v189, v190 op_sel_hi:[0,0,0]
	v_mfma_scale_f32_16x16x128_f8f6f4 v[90:93], v[18:25], v[192:199], 0, v189, v190 op_sel_hi:[0,0,0]
	v_mfma_scale_f32_16x16x128_f8f6f4 v[86:89], v[26:33], v[200:207], 0, v189, v190 op_sel_hi:[0,0,0]
	v_mfma_scale_f32_16x16x128_f8f6f4 v[78:81], v[18:25], v[200:207], 0, v189, v190 op_sel_hi:[0,0,0]
	v_mfma_scale_f32_16x16x128_f8f6f4 v[70:73], v[26:33], v[208:215], 0, v189, v190 op_sel_hi:[0,0,0]
	v_mfma_scale_f32_16x16x128_f8f6f4 v[62:65], v[18:25], v[208:215], 0, v189, v190 op_sel_hi:[0,0,0]
	v_mfma_scale_f32_16x16x128_f8f6f4 v[54:57], v[26:33], v[220:227], 0, v189, v190 op_sel_hi:[0,0,0]
	v_mfma_scale_f32_16x16x128_f8f6f4 v[46:49], v[18:25], v[220:227], 0, v189, v190 op_sel_hi:[0,0,0]
	v_mfma_scale_f32_16x16x128_f8f6f4 v[82:85], v[10:17], v[192:199], 0, v189, v190 op_sel_hi:[0,0,0]
	v_mfma_scale_f32_16x16x128_f8f6f4 v[74:77], v[2:9], v[192:199], 0, v189, v190 op_sel_hi:[0,0,0]
	v_mfma_scale_f32_16x16x128_f8f6f4 v[66:69], v[10:17], v[200:207], 0, v189, v190 op_sel_hi:[0,0,0]
	v_mfma_scale_f32_16x16x128_f8f6f4 v[58:61], v[2:9], v[200:207], 0, v189, v190 op_sel_hi:[0,0,0]
	v_mfma_scale_f32_16x16x128_f8f6f4 v[50:53], v[10:17], v[208:215], 0, v189, v190 op_sel_hi:[0,0,0]
	v_mfma_scale_f32_16x16x128_f8f6f4 v[42:45], v[2:9], v[208:215], 0, v189, v190 op_sel_hi:[0,0,0]
	v_mfma_scale_f32_16x16x128_f8f6f4 v[38:41], v[10:17], v[220:227], 0, v189, v190 op_sel_hi:[0,0,0]
	v_mfma_scale_f32_16x16x128_f8f6f4 v[34:37], v[2:9], v[220:227], 0, v189, v190 op_sel_hi:[0,0,0]
	s_barrier
	s_setprio 0
	s_add_i32 s80, 0, 0x18000
	s_add_i32 s81, 0, 0x1c000
	v_add_u32_e32 v14, s80, v184
	v_add_u32_e32 v30, s81, v184
	ds_read_b128 v[2:5], v14
	ds_read_b128 v[6:9], v14 offset:1024
	ds_read_b128 v[10:13], v14 offset:2048
	ds_read_b128 v[14:17], v14 offset:3072
	ds_read_b128 v[18:21], v30
	ds_read_b128 v[22:25], v30 offset:1024
	ds_read_b128 v[26:29], v30 offset:2048
	ds_read_b128 v[30:33], v30 offset:3072
	s_add_u32 s58, s58, 0xb0000
	s_addc_u32 s59, s59, 0
	s_mov_b32 m0, s63
	v_lshl_add_u64 v[216:217], s[58:59], 0, v[166:167]
	ds_read_b128 v[192:195], v188 offset:32768
	ds_read_b128 v[196:199], v188 offset:33792
	ds_read_b128 v[200:203], v188 offset:34816
	ds_read_b128 v[204:207], v188 offset:35840
	ds_read_b128 v[208:211], v188 offset:36864
	ds_read_b128 v[212:215], v188 offset:37888
	ds_read_b128 v[220:223], v188 offset:38912
	ds_read_b128 v[224:227], v188 offset:39936
	global_load_lds_dwordx4 v[216:217], off
	v_lshl_add_u64 v[216:217], s[58:59], 0, v[168:169]
	s_mov_b32 m0, s64
	s_nop 0
	global_load_lds_dwordx4 v[216:217], off
	s_setprio 1
	s_waitcnt vmcnt(8)
	s_waitcnt lgkmcnt(0)
	s_barrier
	v_mfma_scale_f32_16x16x128_f8f6f4 v[158:161], v[2:9], v[192:199], v[158:161], v189, v190 op_sel_hi:[0,0,0]
	v_mfma_scale_f32_16x16x128_f8f6f4 v[154:157], v[10:17], v[192:199], v[154:157], v189, v190 op_sel_hi:[0,0,0]
	v_mfma_scale_f32_16x16x128_f8f6f4 v[150:153], v[2:9], v[200:207], v[150:153], v189, v190 op_sel_hi:[0,0,0]
	v_mfma_scale_f32_16x16x128_f8f6f4 v[142:145], v[10:17], v[200:207], v[142:145], v189, v190 op_sel_hi:[0,0,0]
	v_mfma_scale_f32_16x16x128_f8f6f4 v[134:137], v[2:9], v[208:215], v[134:137], v189, v190 op_sel_hi:[0,0,0]
	v_mfma_scale_f32_16x16x128_f8f6f4 v[126:129], v[10:17], v[208:215], v[126:129], v189, v190 op_sel_hi:[0,0,0]
	v_mfma_scale_f32_16x16x128_f8f6f4 v[118:121], v[2:9], v[220:227], v[118:121], v189, v190 op_sel_hi:[0,0,0]
	v_mfma_scale_f32_16x16x128_f8f6f4 v[110:113], v[10:17], v[220:227], v[110:113], v189, v190 op_sel_hi:[0,0,0]
	v_mfma_scale_f32_16x16x128_f8f6f4 v[146:149], v[18:25], v[192:199], v[146:149], v189, v190 op_sel_hi:[0,0,0]
	v_mfma_scale_f32_16x16x128_f8f6f4 v[138:141], v[26:33], v[192:199], v[138:141], v189, v190 op_sel_hi:[0,0,0]
	v_mfma_scale_f32_16x16x128_f8f6f4 v[130:133], v[18:25], v[200:207], v[130:133], v189, v190 op_sel_hi:[0,0,0]
	v_mfma_scale_f32_16x16x128_f8f6f4 v[122:125], v[26:33], v[200:207], v[122:125], v189, v190 op_sel_hi:[0,0,0]
	v_mfma_scale_f32_16x16x128_f8f6f4 v[114:117], v[18:25], v[208:215], v[114:117], v189, v190 op_sel_hi:[0,0,0]
	v_mfma_scale_f32_16x16x128_f8f6f4 v[106:109], v[26:33], v[208:215], v[106:109], v189, v190 op_sel_hi:[0,0,0]
	v_mfma_scale_f32_16x16x128_f8f6f4 v[102:105], v[18:25], v[220:227], v[102:105], v189, v190 op_sel_hi:[0,0,0]
	v_mfma_scale_f32_16x16x128_f8f6f4 v[98:101], v[26:33], v[220:227], v[98:101], v189, v190 op_sel_hi:[0,0,0]
	s_barrier
	s_setprio 0
	s_add_i32 s58, s80, s33
	v_lshl_add_u64 v[216:217], v[178:179], 0, s[24:25]
	s_mov_b32 m0, s58
	ds_read_b128 v[192:195], v188 offset:49152
	ds_read_b128 v[196:199], v188 offset:50176
	ds_read_b128 v[200:203], v188 offset:51200
	ds_read_b128 v[204:207], v188 offset:52224
	ds_read_b128 v[208:211], v188 offset:53248
	ds_read_b128 v[212:215], v188 offset:54272
	ds_read_b128 v[220:223], v188 offset:55296
	ds_read_b128 v[224:227], v188 offset:56320
	global_load_lds_dwordx4 v[216:217], off
	v_lshl_add_u64 v[216:217], v[178:179], 0, s[26:27]
	s_add_i32 m0, s58, 0x2000
	s_add_i32 s58, s81, s33
	global_load_lds_dwordx4 v[216:217], off
	v_lshl_add_u64 v[216:217], v[178:179], 0, s[38:39]
	s_mov_b32 m0, s58
	v_lshl_add_u64 v[178:179], v[178:179], 0, s[40:41]
	global_load_lds_dwordx4 v[216:217], off
	s_add_i32 m0, s58, 0x2000
	s_nop 0
	global_load_lds_dwordx4 v[178:179], off
	v_lshl_add_u64 v[178:179], v[180:181], 0, s[36:37]
	s_mov_b32 m0, s66
	s_nop 0
	global_load_lds_dwordx4 v[178:179], off
	v_lshl_add_u64 v[178:179], v[182:183], 0, s[36:37]
	s_mov_b32 m0, s67
	s_nop 0
	global_load_lds_dwordx4 v[178:179], off
	s_setprio 1
	s_waitcnt vmcnt(8)
	s_waitcnt lgkmcnt(0)
	s_barrier
	v_mfma_scale_f32_16x16x128_f8f6f4 v[94:97], v[2:9], v[192:199], v[94:97], v189, v190 op_sel_hi:[0,0,0]
	v_mfma_scale_f32_16x16x128_f8f6f4 v[90:93], v[10:17], v[192:199], v[90:93], v189, v190 op_sel_hi:[0,0,0]
	v_mfma_scale_f32_16x16x128_f8f6f4 v[86:89], v[2:9], v[200:207], v[86:89], v189, v190 op_sel_hi:[0,0,0]
	v_mfma_scale_f32_16x16x128_f8f6f4 v[78:81], v[10:17], v[200:207], v[78:81], v189, v190 op_sel_hi:[0,0,0]
	v_mfma_scale_f32_16x16x128_f8f6f4 v[70:73], v[2:9], v[208:215], v[70:73], v189, v190 op_sel_hi:[0,0,0]
	v_mfma_scale_f32_16x16x128_f8f6f4 v[62:65], v[10:17], v[208:215], v[62:65], v189, v190 op_sel_hi:[0,0,0]
	v_mfma_scale_f32_16x16x128_f8f6f4 v[54:57], v[2:9], v[220:227], v[54:57], v189, v190 op_sel_hi:[0,0,0]
	v_mfma_scale_f32_16x16x128_f8f6f4 v[46:49], v[10:17], v[220:227], v[46:49], v189, v190 op_sel_hi:[0,0,0]
	v_mfma_scale_f32_16x16x128_f8f6f4 v[82:85], v[18:25], v[192:199], v[82:85], v189, v190 op_sel_hi:[0,0,0]
	v_mfma_scale_f32_16x16x128_f8f6f4 v[74:77], v[26:33], v[192:199], v[74:77], v189, v190 op_sel_hi:[0,0,0]
	v_mfma_scale_f32_16x16x128_f8f6f4 v[66:69], v[18:25], v[200:207], v[66:69], v189, v190 op_sel_hi:[0,0,0]
	v_mfma_scale_f32_16x16x128_f8f6f4 v[58:61], v[26:33], v[200:207], v[58:61], v189, v190 op_sel_hi:[0,0,0]
	v_mfma_scale_f32_16x16x128_f8f6f4 v[50:53], v[18:25], v[208:215], v[50:53], v189, v190 op_sel_hi:[0,0,0]
	v_mfma_scale_f32_16x16x128_f8f6f4 v[42:45], v[26:33], v[208:215], v[42:45], v189, v190 op_sel_hi:[0,0,0]
	v_mfma_scale_f32_16x16x128_f8f6f4 v[38:41], v[18:25], v[220:227], v[38:41], v189, v190 op_sel_hi:[0,0,0]
	v_mfma_scale_f32_16x16x128_f8f6f4 v[34:37], v[26:33], v[220:227], v[34:37], v189, v190 op_sel_hi:[0,0,0]
	s_barrier
	s_setprio 0
	s_add_i32 s53, s53, 2
	s_add_u32 s56, s56, 0x100
	s_addc_u32 s57, s57, 0
	s_cmp_gt_u32 s53, 41
	v_lshl_add_u64 v[176:177], v[176:177], 0, s[44:45]
.LBB0_1568:
	ds_read_b128 v[26:29], v186
	ds_read_b128 v[30:33], v186 offset:1024
	ds_read_b128 v[18:21], v186 offset:2048
	ds_read_b128 v[22:25], v186 offset:3072
	ds_read_b128 v[10:13], v187
	ds_read_b128 v[14:17], v187 offset:1024
	ds_read_b128 v[2:5], v187 offset:2048
	ds_read_b128 v[6:9], v187 offset:3072
	s_add_u32 s58, s56, 0xfff50080
	s_addc_u32 s59, s57, -1
	s_cmp_eq_u32 s53, 40
	s_cselect_b64 vcc, -1, 0
	s_cselect_b32 s59, s5, s59
	s_cselect_b32 s58, s4, s58
	v_cndmask_b32_e32 v179, v177, v175, vcc
	v_cndmask_b32_e32 v178, v176, v174, vcc
	v_lshl_add_u64 v[180:181], s[56:57], 0, v[170:171]
	s_add_i32 m0, s61, 0xc000
	ds_read_b128 v[192:195], v188
	ds_read_b128 v[196:199], v188 offset:1024
	ds_read_b128 v[200:203], v188 offset:2048
	ds_read_b128 v[204:207], v188 offset:3072
	ds_read_b128 v[208:211], v188 offset:4096
	ds_read_b128 v[212:215], v188 offset:5120
	ds_read_b128 v[220:223], v188 offset:6144
	ds_read_b128 v[224:227], v188 offset:7168
	global_load_lds_dwordx4 v[180:181], off
	v_lshl_add_u64 v[180:181], s[56:57], 0, v[172:173]
	s_add_i32 m0, s61, 0xe000
	s_nop 0
	global_load_lds_dwordx4 v[180:181], off
	s_setprio 1
	s_waitcnt vmcnt(8)
	s_waitcnt lgkmcnt(0)
	s_barrier
	v_mfma_scale_f32_16x16x128_f8f6f4 v[158:161], v[26:33], v[192:199], v[158:161], v189, v190 op_sel_hi:[0,0,0]
	v_mfma_scale_f32_16x16x128_f8f6f4 v[154:157], v[18:25], v[192:199], v[154:157], v189, v190 op_sel_hi:[0,0,0]
	v_mfma_scale_f32_16x16x128_f8f6f4 v[150:153], v[26:33], v[200:207], v[150:153], v189, v190 op_sel_hi:[0,0,0]
	v_mfma_scale_f32_16x16x128_f8f6f4 v[142:145], v[18:25], v[200:207], v[142:145], v189, v190 op_sel_hi:[0,0,0]
	v_mfma_scale_f32_16x16x128_f8f6f4 v[134:137], v[26:33], v[208:215], v[134:137], v189, v190 op_sel_hi:[0,0,0]
	v_mfma_scale_f32_16x16x128_f8f6f4 v[126:129], v[18:25], v[208:215], v[126:129], v189, v190 op_sel_hi:[0,0,0]
	v_mfma_scale_f32_16x16x128_f8f6f4 v[118:121], v[26:33], v[220:227], v[118:121], v189, v190 op_sel_hi:[0,0,0]
	v_mfma_scale_f32_16x16x128_f8f6f4 v[110:113], v[18:25], v[220:227], v[110:113], v189, v190 op_sel_hi:[0,0,0]
	v_mfma_scale_f32_16x16x128_f8f6f4 v[146:149], v[10:17], v[192:199], v[146:149], v189, v190 op_sel_hi:[0,0,0]
	v_mfma_scale_f32_16x16x128_f8f6f4 v[138:141], v[2:9], v[192:199], v[138:141], v189, v190 op_sel_hi:[0,0,0]
	v_mfma_scale_f32_16x16x128_f8f6f4 v[130:133], v[10:17], v[200:207], v[130:133], v189, v190 op_sel_hi:[0,0,0]
	v_mfma_scale_f32_16x16x128_f8f6f4 v[122:125], v[2:9], v[200:207], v[122:125], v189, v190 op_sel_hi:[0,0,0]
	v_mfma_scale_f32_16x16x128_f8f6f4 v[114:117], v[10:17], v[208:215], v[114:117], v189, v190 op_sel_hi:[0,0,0]
	v_mfma_scale_f32_16x16x128_f8f6f4 v[106:109], v[2:9], v[208:215], v[106:109], v189, v190 op_sel_hi:[0,0,0]
	v_mfma_scale_f32_16x16x128_f8f6f4 v[102:105], v[10:17], v[220:227], v[102:105], v189, v190 op_sel_hi:[0,0,0]
	v_mfma_scale_f32_16x16x128_f8f6f4 v[98:101], v[2:9], v[220:227], v[98:101], v189, v190 op_sel_hi:[0,0,0]
	s_barrier
	s_setprio 0
	s_add_i32 s80, s69, s33
	v_lshl_add_u64 v[178:179], v[178:179], 0, v[164:165]
	s_mov_b32 m0, s80
	ds_read_b128 v[192:195], v188 offset:16384
	ds_read_b128 v[196:199], v188 offset:17408
	ds_read_b128 v[200:203], v188 offset:18432
	ds_read_b128 v[204:207], v188 offset:19456
	ds_read_b128 v[208:211], v188 offset:20480
	ds_read_b128 v[212:215], v188 offset:21504
	ds_read_b128 v[220:223], v188 offset:22528
	ds_read_b128 v[224:227], v188 offset:23552
	global_load_lds_dwordx4 v[178:179], off
	v_lshl_add_u64 v[180:181], v[178:179], 0, s[10:11]
	s_add_i32 m0, s80, 0x2000
	s_add_i32 s80, s70, s33
	global_load_lds_dwordx4 v[180:181], off
	v_lshl_add_u64 v[180:181], v[178:179], 0, s[12:13]
	s_mov_b32 m0, s80
	v_lshl_add_u64 v[182:183], s[58:59], 0, v[168:169]
	global_load_lds_dwordx4 v[180:181], off
	v_lshl_add_u64 v[180:181], v[178:179], 0, s[14:15]
	s_add_i32 m0, s80, 0x2000
	s_nop 0
	global_load_lds_dwordx4 v[180:181], off
	v_lshl_add_u64 v[180:181], s[58:59], 0, v[166:167]
	s_mov_b32 m0, s61
	s_nop 0
	global_load_lds_dwordx4 v[180:181], off
	s_mov_b32 m0, s62
	s_nop 0
	global_load_lds_dwordx4 v[182:183], off
	s_setprio 1
	s_waitcnt vmcnt(8)
	s_waitcnt lgkmcnt(0)
	s_barrier
	v_mfma_scale_f32_16x16x128_f8f6f4 v[94:97], v[26:33], v[192:199], v[94:97], v189, v190 op_sel_hi:[0,0,0]
	v_mfma_scale_f32_16x16x128_f8f6f4 v[90:93], v[18:25], v[192:199], v[90:93], v189, v190 op_sel_hi:[0,0,0]
	v_mfma_scale_f32_16x16x128_f8f6f4 v[86:89], v[26:33], v[200:207], v[86:89], v189, v190 op_sel_hi:[0,0,0]
	v_mfma_scale_f32_16x16x128_f8f6f4 v[78:81], v[18:25], v[200:207], v[78:81], v189, v190 op_sel_hi:[0,0,0]
	v_mfma_scale_f32_16x16x128_f8f6f4 v[70:73], v[26:33], v[208:215], v[70:73], v189, v190 op_sel_hi:[0,0,0]
	v_mfma_scale_f32_16x16x128_f8f6f4 v[62:65], v[18:25], v[208:215], v[62:65], v189, v190 op_sel_hi:[0,0,0]
	v_mfma_scale_f32_16x16x128_f8f6f4 v[54:57], v[26:33], v[220:227], v[54:57], v189, v190 op_sel_hi:[0,0,0]
	v_mfma_scale_f32_16x16x128_f8f6f4 v[46:49], v[18:25], v[220:227], v[46:49], v189, v190 op_sel_hi:[0,0,0]
	v_mfma_scale_f32_16x16x128_f8f6f4 v[82:85], v[10:17], v[192:199], v[82:85], v189, v190 op_sel_hi:[0,0,0]
	v_mfma_scale_f32_16x16x128_f8f6f4 v[74:77], v[2:9], v[192:199], v[74:77], v189, v190 op_sel_hi:[0,0,0]
	v_mfma_scale_f32_16x16x128_f8f6f4 v[66:69], v[10:17], v[200:207], v[66:69], v189, v190 op_sel_hi:[0,0,0]
	v_mfma_scale_f32_16x16x128_f8f6f4 v[58:61], v[2:9], v[200:207], v[58:61], v189, v190 op_sel_hi:[0,0,0]
	v_mfma_scale_f32_16x16x128_f8f6f4 v[50:53], v[10:17], v[208:215], v[50:53], v189, v190 op_sel_hi:[0,0,0]
	v_mfma_scale_f32_16x16x128_f8f6f4 v[42:45], v[2:9], v[208:215], v[42:45], v189, v190 op_sel_hi:[0,0,0]
	v_mfma_scale_f32_16x16x128_f8f6f4 v[38:41], v[10:17], v[220:227], v[38:41], v189, v190 op_sel_hi:[0,0,0]
	v_mfma_scale_f32_16x16x128_f8f6f4 v[34:37], v[2:9], v[220:227], v[34:37], v189, v190 op_sel_hi:[0,0,0]
	s_barrier
	s_setprio 0
	s_add_i32 s80, 0, 0x18000
	s_add_i32 s81, 0, 0x1c000
	v_add_u32_e32 v14, s80, v184
	v_add_u32_e32 v30, s81, v184
	ds_read_b128 v[2:5], v14
	ds_read_b128 v[6:9], v14 offset:1024
	ds_read_b128 v[10:13], v14 offset:2048
	ds_read_b128 v[14:17], v14 offset:3072
	ds_read_b128 v[18:21], v30
	ds_read_b128 v[22:25], v30 offset:1024
	ds_read_b128 v[26:29], v30 offset:2048
	ds_read_b128 v[30:33], v30 offset:3072
	s_add_u32 s58, s58, 0xb0000
	s_addc_u32 s59, s59, 0
	s_mov_b32 m0, s63
	v_lshl_add_u64 v[216:217], s[58:59], 0, v[166:167]
	ds_read_b128 v[192:195], v188 offset:32768
	ds_read_b128 v[196:199], v188 offset:33792
	ds_read_b128 v[200:203], v188 offset:34816
	ds_read_b128 v[204:207], v188 offset:35840
	ds_read_b128 v[208:211], v188 offset:36864
	ds_read_b128 v[212:215], v188 offset:37888
	ds_read_b128 v[220:223], v188 offset:38912
	ds_read_b128 v[224:227], v188 offset:39936
	global_load_lds_dwordx4 v[216:217], off
	v_lshl_add_u64 v[216:217], s[58:59], 0, v[168:169]
	s_mov_b32 m0, s64
	s_nop 0
	global_load_lds_dwordx4 v[216:217], off
	s_setprio 1
	s_waitcnt vmcnt(8)
	s_waitcnt lgkmcnt(0)
	s_barrier
	v_mfma_scale_f32_16x16x128_f8f6f4 v[158:161], v[2:9], v[192:199], v[158:161], v189, v190 op_sel_hi:[0,0,0]
	v_mfma_scale_f32_16x16x128_f8f6f4 v[154:157], v[10:17], v[192:199], v[154:157], v189, v190 op_sel_hi:[0,0,0]
	v_mfma_scale_f32_16x16x128_f8f6f4 v[150:153], v[2:9], v[200:207], v[150:153], v189, v190 op_sel_hi:[0,0,0]
	v_mfma_scale_f32_16x16x128_f8f6f4 v[142:145], v[10:17], v[200:207], v[142:145], v189, v190 op_sel_hi:[0,0,0]
	v_mfma_scale_f32_16x16x128_f8f6f4 v[134:137], v[2:9], v[208:215], v[134:137], v189, v190 op_sel_hi:[0,0,0]
	v_mfma_scale_f32_16x16x128_f8f6f4 v[126:129], v[10:17], v[208:215], v[126:129], v189, v190 op_sel_hi:[0,0,0]
	v_mfma_scale_f32_16x16x128_f8f6f4 v[118:121], v[2:9], v[220:227], v[118:121], v189, v190 op_sel_hi:[0,0,0]
	v_mfma_scale_f32_16x16x128_f8f6f4 v[110:113], v[10:17], v[220:227], v[110:113], v189, v190 op_sel_hi:[0,0,0]
	v_mfma_scale_f32_16x16x128_f8f6f4 v[146:149], v[18:25], v[192:199], v[146:149], v189, v190 op_sel_hi:[0,0,0]
	v_mfma_scale_f32_16x16x128_f8f6f4 v[138:141], v[26:33], v[192:199], v[138:141], v189, v190 op_sel_hi:[0,0,0]
	v_mfma_scale_f32_16x16x128_f8f6f4 v[130:133], v[18:25], v[200:207], v[130:133], v189, v190 op_sel_hi:[0,0,0]
	v_mfma_scale_f32_16x16x128_f8f6f4 v[122:125], v[26:33], v[200:207], v[122:125], v189, v190 op_sel_hi:[0,0,0]
	v_mfma_scale_f32_16x16x128_f8f6f4 v[114:117], v[18:25], v[208:215], v[114:117], v189, v190 op_sel_hi:[0,0,0]
	v_mfma_scale_f32_16x16x128_f8f6f4 v[106:109], v[26:33], v[208:215], v[106:109], v189, v190 op_sel_hi:[0,0,0]
	v_mfma_scale_f32_16x16x128_f8f6f4 v[102:105], v[18:25], v[220:227], v[102:105], v189, v190 op_sel_hi:[0,0,0]
	v_mfma_scale_f32_16x16x128_f8f6f4 v[98:101], v[26:33], v[220:227], v[98:101], v189, v190 op_sel_hi:[0,0,0]
	s_barrier
	s_setprio 0
	s_add_i32 s58, s80, s33
	v_lshl_add_u64 v[216:217], v[178:179], 0, s[24:25]
	s_mov_b32 m0, s58
	ds_read_b128 v[192:195], v188 offset:49152
	ds_read_b128 v[196:199], v188 offset:50176
	ds_read_b128 v[200:203], v188 offset:51200
	ds_read_b128 v[204:207], v188 offset:52224
	ds_read_b128 v[208:211], v188 offset:53248
	ds_read_b128 v[212:215], v188 offset:54272
	ds_read_b128 v[220:223], v188 offset:55296
	ds_read_b128 v[224:227], v188 offset:56320
	global_load_lds_dwordx4 v[216:217], off
	v_lshl_add_u64 v[216:217], v[178:179], 0, s[26:27]
	s_add_i32 m0, s58, 0x2000
	s_add_i32 s58, s81, s33
	global_load_lds_dwordx4 v[216:217], off
	v_lshl_add_u64 v[216:217], v[178:179], 0, s[38:39]
	s_mov_b32 m0, s58
	v_lshl_add_u64 v[178:179], v[178:179], 0, s[40:41]
	global_load_lds_dwordx4 v[216:217], off
	s_add_i32 m0, s58, 0x2000
	s_nop 0
	global_load_lds_dwordx4 v[178:179], off
	v_lshl_add_u64 v[178:179], v[180:181], 0, s[36:37]
	s_mov_b32 m0, s66
	s_nop 0
	global_load_lds_dwordx4 v[178:179], off
	v_lshl_add_u64 v[178:179], v[182:183], 0, s[36:37]
	s_mov_b32 m0, s67
	s_nop 0
	global_load_lds_dwordx4 v[178:179], off
	s_setprio 1
	s_waitcnt vmcnt(8)
	s_waitcnt lgkmcnt(0)
	s_barrier
	v_mfma_scale_f32_16x16x128_f8f6f4 v[94:97], v[2:9], v[192:199], v[94:97], v189, v190 op_sel_hi:[0,0,0]
	v_mfma_scale_f32_16x16x128_f8f6f4 v[90:93], v[10:17], v[192:199], v[90:93], v189, v190 op_sel_hi:[0,0,0]
	v_mfma_scale_f32_16x16x128_f8f6f4 v[86:89], v[2:9], v[200:207], v[86:89], v189, v190 op_sel_hi:[0,0,0]
	v_mfma_scale_f32_16x16x128_f8f6f4 v[78:81], v[10:17], v[200:207], v[78:81], v189, v190 op_sel_hi:[0,0,0]
	v_mfma_scale_f32_16x16x128_f8f6f4 v[70:73], v[2:9], v[208:215], v[70:73], v189, v190 op_sel_hi:[0,0,0]
	v_mfma_scale_f32_16x16x128_f8f6f4 v[62:65], v[10:17], v[208:215], v[62:65], v189, v190 op_sel_hi:[0,0,0]
	v_mfma_scale_f32_16x16x128_f8f6f4 v[54:57], v[2:9], v[220:227], v[54:57], v189, v190 op_sel_hi:[0,0,0]
	v_mfma_scale_f32_16x16x128_f8f6f4 v[46:49], v[10:17], v[220:227], v[46:49], v189, v190 op_sel_hi:[0,0,0]
	v_mfma_scale_f32_16x16x128_f8f6f4 v[82:85], v[18:25], v[192:199], v[82:85], v189, v190 op_sel_hi:[0,0,0]
	v_mfma_scale_f32_16x16x128_f8f6f4 v[74:77], v[26:33], v[192:199], v[74:77], v189, v190 op_sel_hi:[0,0,0]
	v_mfma_scale_f32_16x16x128_f8f6f4 v[66:69], v[18:25], v[200:207], v[66:69], v189, v190 op_sel_hi:[0,0,0]
	v_mfma_scale_f32_16x16x128_f8f6f4 v[58:61], v[26:33], v[200:207], v[58:61], v189, v190 op_sel_hi:[0,0,0]
	v_mfma_scale_f32_16x16x128_f8f6f4 v[50:53], v[18:25], v[208:215], v[50:53], v189, v190 op_sel_hi:[0,0,0]
	v_mfma_scale_f32_16x16x128_f8f6f4 v[42:45], v[26:33], v[208:215], v[42:45], v189, v190 op_sel_hi:[0,0,0]
	v_mfma_scale_f32_16x16x128_f8f6f4 v[38:41], v[18:25], v[220:227], v[38:41], v189, v190 op_sel_hi:[0,0,0]
	v_mfma_scale_f32_16x16x128_f8f6f4 v[34:37], v[26:33], v[220:227], v[34:37], v189, v190 op_sel_hi:[0,0,0]
	s_barrier
	s_setprio 0
	s_add_i32 s53, s53, 2
	s_add_u32 s56, s56, 0x100
	s_addc_u32 s57, s57, 0
	s_cmp_gt_u32 s53, 41
	v_lshl_add_u64 v[176:177], v[176:177], 0, s[44:45]
	s_cbranch_scc0 .LBB0_1568
	s_and_b64 vcc, exec, s[42:43]
	s_cbranch_vccz .LBB0_1571
	s_barrier
	s_setprio 3
